# attention: gain rows of the task epilogue loaded once up front, per-key rstd partial loads issued together, bf16 pair packs by v_cvt_pk_bf16_f32 in attention scan and retention
# speedup vs baseline: 1.0731x; 1.0114x over previous
; __device__ __forceinline__ unsigned pk2(float lo, float hi) { return f2bf(lo) | (f2bf(hi) << 16); }
; __device__ __forceinline__ void scan_task(const Frame& F, int task) {
;     ...
;     for (int eb = 0; eb < 4; ++eb) { u32x2 w; w.x = pk2(st[eb][0], st[eb][1]); w.y = pk2(st[eb][2], st[eb][3]); st_u2(sp + (size_t)(NCH - 1) * HD * HD + eb * 16 * HD, w); }
.LBB0_482:
	s_or_b32 s0, s13, s9
	s_ashr_i32 s1, s0, 31
	s_lshl_b64 s[0:1], s[0:1], 12
	s_or_b32 s0, s0, s14
	s_nop 0
	v_mov_b32_e32 v1, s1
	v_mov_b32_e32 v0, s0
	v_readlane_b32 s0, v253, 46
	s_nop 1
	v_lshlrev_b64 v[0:1], 8, v[0:1]
	v_readlane_b32 s1, v253, 47
	s_nop 1
	v_lshl_add_u64 v[0:1], s[0:1], 0, v[0:1]
	s_lshl_b32 s96, s12, 5
	v_cvt_pk_bf16_f32 v2, v88, v89
	s_nop 0
	v_lshl_add_u64 v[0:1], v[0:1], 0, s[96:97]
	s_nop 1
	v_lshl_add_u64 v[0:1], v[240:241], 0, v[0:1]
	s_nop 1
	s_mov_b32 s0, 0xf9000
	v_cvt_pk_bf16_f32 v3, v90, v91
	v_add_co_u32_e32 v4, vcc, s0, v0
	v_bfe_u32 v6, v95, 16, 1
	s_nop 0
	v_addc_co_u32_e32 v5, vcc, 0, v1, vcc
	global_store_dwordx2 v[4:5], v[2:3], off offset:-4096
	s_nop 4
	v_cvt_pk_bf16_f32 v2, v92, v93
	s_nop 2
	v_add3_u32 v6, v95, v6, s76
	v_cvt_pk_bf16_f32 v3, v94, v95
	global_store_dwordx2 v[4:5], v[2:3], off
	s_nop 4
	v_cvt_pk_bf16_f32 v2, v84, v85
	s_nop 4
	s_mov_b32 s0, 0xfa000
	v_cvt_pk_bf16_f32 v3, v86, v87
	v_add_co_u32_e32 v4, vcc, s0, v0
	v_readlane_b32 s0, v251, 18
	s_nop 0
	v_addc_co_u32_e32 v5, vcc, 0, v1, vcc
	global_store_dwordx2 v[4:5], v[2:3], off
	s_nop 4
	v_cvt_pk_bf16_f32 v2, v80, v81
	s_nop 1
	v_bfe_u32 v4, v83, 16, 1
	s_nop 0
	v_add3_u32 v4, v83, v4, s76
	v_add_co_u32_e32 v0, vcc, 0xfb000, v0
	s_add_i32 s8, s8, s82
	s_add_i32 s3, s3, s67
	s_add_i32 s2, s2, s0
	v_cvt_pk_bf16_f32 v3, v82, v83
	v_addc_co_u32_e32 v1, vcc, 0, v1, vcc
	s_cmpk_gt_i32 s8, 0x3ff
	global_store_dwordx2 v[0:1], v[2:3], off
	s_cbranch_scc1 .LBB0_477

; #define LAS __attribute__((address_space(3)))
; #define LDS_WAIT() asm volatile("s_waitcnt lgkmcnt(0)" ::: "memory")
; __device__ __forceinline__ unsigned pk2(float lo, float hi) { return f2bf(lo) | (f2bf(hi) << 16); }
; __device__ __forceinline__ f32x4 mfma16(bf16x8 a, bf16x8 b, f32x4 c) { return __builtin_amdgcn_mfma_f32_16x16x32_bf16(a, b, c, 0, 0, 0); }
; __device__ __forceinline__ void scan_step(f32x4 (&st)[4], const ScanOps& o, const float (&dec)[16], LAS unsigned char* kw, const LAS unsigned char* kr, bf16* sp, int n, float cd) {
; #pragma unroll
;     for (int eb = 0; eb < 4; ++eb) { u32x2 w; w.x = pk2(st[eb][0], st[eb][1]); w.y = pk2(st[eb][2], st[eb][3]); st_u2(sp + (size_t)n * HD * HD + eb * 16 * HD, w); }
; #pragma unroll
;     for (int i = 0; i < 2; ++i)
; #pragma unroll
;         for (int d = 0; d < 4; ++d) *(LAS unsigned*)(kw + i * 32 * SC_PITCH + d * 4) = o.kp[i][d];
;     LDS_WAIT(); asm volatile("" ::: "memory");
;     bf16x8 ka[2];
; #pragma unroll
;     for (int ks = 0; ks < 2; ++ks) { u32x4 w;
; #pragma unroll
;         for (int j = 0; j < 4; ++j) { const unsigned e0 = *(const LAS unsigned short*)(kr + (ks * 32 + 2 * j) * SC_PITCH), e1 = *(const LAS unsigned short*)(kr + (ks * 32 + 2 * j + 1) * SC_PITCH);
;             w[j] = pk2(bf_lo(e0) * dec[ks * 8 + 2 * j], bf_lo(e1) * dec[ks * 8 + 2 * j + 1]); }
;         ka[ks] = __builtin_bit_cast(bf16x8, w); }
;     LDS_WAIT(); asm volatile("" ::: "memory");
; #pragma unroll
;     for (int eb = 0; eb < 4; ++eb) { st[eb] *= cd;
; #pragma unroll
;         for (int ks = 0; ks < 2; ++ks) st[eb] = mfma16(ka[ks], o.va[eb][ks], st[eb]); }
.LBB0_505:
	s_nop 4
	v_cvt_pk_bf16_f32 v172, v88, v89
	s_nop 4
	v_cvt_pk_bf16_f32 v173, v90, v91
	s_mov_b32 s0, 0x22c11000
	s_nop 0
	v_add_co_u32_e32 v174, vcc, s0, v166
	s_nop 1
	v_addc_co_u32_e32 v175, vcc, 0, v167, vcc
	s_nop 1
	global_store_dwordx2 v[174:175], v[172:173], off offset:-4096
	v_cvt_pk_bf16_f32 v172, v92, v93
	s_nop 4
	v_cvt_pk_bf16_f32 v173, v94, v95
	s_nop 4
	global_store_dwordx2 v[174:175], v[172:173], off
	v_cvt_pk_bf16_f32 v172, v84, v85
	s_nop 4
	v_cvt_pk_bf16_f32 v173, v86, v87
	s_mov_b32 s0, 0x22c13000
	s_nop 0
	v_add_co_u32_e32 v166, vcc, s0, v166
	s_nop 1
	v_addc_co_u32_e32 v167, vcc, 0, v167, vcc
	s_nop 1
	global_store_dwordx2 v[166:167], v[172:173], off offset:-4096
	v_cvt_pk_bf16_f32 v172, v80, v81
	s_nop 4
	v_cvt_pk_bf16_f32 v173, v82, v83
	global_store_dwordx2 v[166:167], v[172:173], off
	ds_write2_b32 v137, v96, v97 offset1:1
	ds_write2_b32 v137, v98, v99 offset0:2 offset1:3
	ds_write2_b32 v169, v100, v101 offset1:1
	ds_write2_b32 v170, v102, v103 offset1:1
	s_waitcnt lgkmcnt(0)
	ds_read_u16 v157, v168 offset:72
	ds_read_u16 v169, v168 offset:108
	ds_read_u16 v166, v168
	ds_read_u16 v172, v168 offset:144
	ds_read_u16 v173, v168 offset:216
	ds_read_u16 v174, v168 offset:252
	ds_read_u16 v175, v168 offset:180
	ds_read_u16 v170, v168 offset:36
	s_waitcnt lgkmcnt(7)
	v_lshlrev_b32_e32 v167, 16, v157
	s_waitcnt lgkmcnt(5)
	v_lshlrev_b32_e32 v166, 16, v166
	v_pk_mul_f32 v[166:167], v[140:141], v[166:167]
	v_lshlrev_b32_e32 v171, 16, v169
	v_and_b32_sdwa v169, v166, v213 dst_sel:DWORD dst_unused:UNUSED_PAD src0_sel:WORD_1 src1_sel:DWORD
	v_and_b32_sdwa v157, v167, v213 dst_sel:DWORD dst_unused:UNUSED_PAD src0_sel:WORD_1 src1_sel:DWORD
	v_add3_u32 v166, v166, v169, s76
	v_add3_u32 v157, v167, v157, s76
	v_lshrrev_b32_e32 v169, 16, v166
	s_waitcnt lgkmcnt(3)
	v_lshlrev_b32_e32 v167, 16, v173
	v_lshlrev_b32_e32 v166, 16, v172
	s_waitcnt lgkmcnt(0)
	v_lshlrev_b32_e32 v170, 16, v170
	v_pk_mul_f32 v[166:167], v[144:145], v[166:167]
	v_lshlrev_b32_e32 v173, 16, v174
	v_lshlrev_b32_e32 v172, 16, v175
	v_pk_mul_f32 v[170:171], v[142:143], v[170:171]
	v_pk_mul_f32 v[172:173], v[146:147], v[172:173]
	v_and_b32_sdwa v174, v167, v213 dst_sel:DWORD dst_unused:UNUSED_PAD src0_sel:WORD_1 src1_sel:DWORD
	v_and_b32_sdwa v175, v166, v213 dst_sel:DWORD dst_unused:UNUSED_PAD src0_sel:WORD_1 src1_sel:DWORD
	v_add3_u32 v178, v167, v174, s76
	v_add3_u32 v166, v166, v175, s76
	v_bfe_u32 v167, v172, 16, 1
	v_bfe_u32 v174, v171, 16, 1
	v_bfe_u32 v175, v170, 16, 1
	v_lshrrev_b32_e32 v157, 16, v157
	v_lshrrev_b32_e32 v166, 16, v166
	v_bfe_u32 v176, v173, 16, 1
	v_add3_u32 v170, v170, v175, s76
	v_add3_u32 v171, v171, v174, s76
	v_add3_u32 v167, v172, v167, s76
	v_add3_u32 v173, v173, v176, s76
	v_and_or_b32 v172, v167, s75, v166
	v_and_or_b32 v171, v171, s75, v157
	v_and_or_b32 v170, v170, s75, v169
	ds_read_u16 v157, v168 offset:1152
	ds_read_u16 v166, v168 offset:1224
	ds_read_u16 v169, v168 offset:1260
	ds_read_u16 v176, v168 offset:1296
	ds_read_u16 v177, v168 offset:1368
	ds_read_u16 v179, v168 offset:1404
	ds_read_u16 v180, v168 offset:1332
	ds_read_u16 v174, v168 offset:1188
	s_waitcnt lgkmcnt(6)
	v_lshlrev_b32_e32 v167, 16, v166
	v_lshlrev_b32_e32 v166, 16, v157
	v_pk_mul_f32 v[166:167], v[148:149], v[166:167]
	s_waitcnt lgkmcnt(5)
	v_lshlrev_b32_e32 v175, 16, v169
	v_and_b32_sdwa v169, v166, v213 dst_sel:DWORD dst_unused:UNUSED_PAD src0_sel:WORD_1 src1_sel:DWORD
	v_and_b32_sdwa v157, v167, v213 dst_sel:DWORD dst_unused:UNUSED_PAD src0_sel:WORD_1 src1_sel:DWORD
	v_add3_u32 v166, v166, v169, s76
	v_add3_u32 v157, v167, v157, s76
	v_lshrrev_b32_e32 v169, 16, v166
	s_waitcnt lgkmcnt(3)
	v_lshlrev_b32_e32 v167, 16, v177
	v_lshlrev_b32_e32 v166, 16, v176
	s_waitcnt lgkmcnt(0)
	v_lshlrev_b32_e32 v174, 16, v174
	v_pk_mul_f32 v[166:167], v[152:153], v[166:167]
	v_pk_mul_f32 v[174:175], v[150:151], v[174:175]
	v_lshlrev_b32_e32 v177, 16, v179
	v_lshlrev_b32_e32 v176, 16, v180
	v_and_b32_sdwa v180, v166, v213 dst_sel:DWORD dst_unused:UNUSED_PAD src0_sel:WORD_1 src1_sel:DWORD
	v_perm_b32 v173, v173, v178, s71
	v_pk_mul_f32 v[176:177], v[154:155], v[176:177]
	v_and_b32_sdwa v179, v167, v213 dst_sel:DWORD dst_unused:UNUSED_PAD src0_sel:WORD_1 src1_sel:DWORD
	v_add3_u32 v166, v166, v180, s76
	v_bfe_u32 v180, v175, 16, 1
	v_lshrrev_b32_e32 v157, 16, v157
	v_add3_u32 v167, v167, v179, s76
	v_bfe_u32 v179, v176, 16, 1
	v_bfe_u32 v181, v174, 16, 1
	v_bfe_u32 v182, v177, 16, 1
	v_add3_u32 v175, v175, v180, s76
	v_lshrrev_b32_e32 v166, 16, v166
	v_add3_u32 v177, v177, v182, s76
	v_add3_u32 v174, v174, v181, s76
	v_add3_u32 v176, v176, v179, s76
	v_and_or_b32 v175, v175, s75, v157
	v_mov_b32_e32 v157, v156
	v_and_or_b32 v176, v176, s75, v166
	v_and_or_b32 v174, v174, s75, v169
	v_pk_mul_f32 v[90:91], v[156:157], v[90:91]
	v_pk_mul_f32 v[88:89], v[158:159], v[88:89]
	v_perm_b32 v177, v177, v167, s71
	v_pk_mul_f32 v[94:95], v[156:157], v[94:95]
	v_pk_mul_f32 v[92:93], v[158:159], v[92:93]
	v_pk_mul_f32 v[86:87], v[156:157], v[86:87]
	v_pk_mul_f32 v[84:85], v[158:159], v[84:85]
	v_pk_mul_f32 v[82:83], v[156:157], v[82:83]
	v_pk_mul_f32 v[80:81], v[158:159], v[80:81]
	v_mfma_f32_16x16x32_bf16 v[88:91], v[170:173], v[104:107], v[88:91]
	s_waitcnt lgkmcnt(0)
	s_waitcnt vmcnt(13)
	v_mfma_f32_16x16x32_bf16 v[92:95], v[170:173], v[112:115], v[92:95]
	s_waitcnt vmcnt(11)
	v_mfma_f32_16x16x32_bf16 v[84:87], v[170:173], v[120:123], v[84:87]
	s_waitcnt vmcnt(9)
	v_mfma_f32_16x16x32_bf16 v[80:83], v[170:173], v[128:131], v[80:83]
	v_mfma_f32_16x16x32_bf16 v[88:91], v[174:177], v[108:111], v[88:91]
	v_mfma_f32_16x16x32_bf16 v[92:95], v[174:177], v[116:119], v[92:95]
	v_mfma_f32_16x16x32_bf16 v[84:87], v[174:177], v[124:127], v[84:87]
	s_waitcnt vmcnt(8)
	v_mfma_f32_16x16x32_bf16 v[80:83], v[174:177], v[132:135], v[80:83]

; #define LAS __attribute__((address_space(3)))
; #define LDS_WAIT() asm volatile("s_waitcnt lgkmcnt(0)" ::: "memory")
; __device__ __forceinline__ unsigned pk2(float lo, float hi) { return f2bf(lo) | (f2bf(hi) << 16); }
; __device__ __forceinline__ f32x4 mfma16(bf16x8 a, bf16x8 b, f32x4 c) { return __builtin_amdgcn_mfma_f32_16x16x32_bf16(a, b, c, 0, 0, 0); }
; __device__ __forceinline__ void scan_step(f32x4 (&st)[4], const ScanOps& o, const float (&dec)[16], LAS unsigned char* kw, const LAS unsigned char* kr, bf16* sp, int n, float cd) {
; #pragma unroll
;     for (int eb = 0; eb < 4; ++eb) { u32x2 w; w.x = pk2(st[eb][0], st[eb][1]); w.y = pk2(st[eb][2], st[eb][3]); st_u2(sp + (size_t)n * HD * HD + eb * 16 * HD, w); }
; #pragma unroll
;     for (int i = 0; i < 2; ++i)
; #pragma unroll
;         for (int d = 0; d < 4; ++d) *(LAS unsigned*)(kw + i * 32 * SC_PITCH + d * 4) = o.kp[i][d];
;     LDS_WAIT(); asm volatile("" ::: "memory");
;     bf16x8 ka[2];
; #pragma unroll
;     for (int ks = 0; ks < 2; ++ks) { u32x4 w;
; #pragma unroll
;         for (int j = 0; j < 4; ++j) { const unsigned e0 = *(const LAS unsigned short*)(kr + (ks * 32 + 2 * j) * SC_PITCH), e1 = *(const LAS unsigned short*)(kr + (ks * 32 + 2 * j + 1) * SC_PITCH);
;             w[j] = pk2(bf_lo(e0) * dec[ks * 8 + 2 * j], bf_lo(e1) * dec[ks * 8 + 2 * j + 1]); }
;         ka[ks] = __builtin_bit_cast(bf16x8, w); }
;     LDS_WAIT(); asm volatile("" ::: "memory");
; #pragma unroll
;     for (int eb = 0; eb < 4; ++eb) { st[eb] *= cd;
; #pragma unroll
;         for (int ks = 0; ks < 2; ++ks) st[eb] = mfma16(ka[ks], o.va[eb][ks], st[eb]); }
.LBB0_509:
	s_nop 4
	v_cvt_pk_bf16_f32 v170, v88, v89
	s_nop 4
	v_lshl_add_u64 v[166:167], s[62:63], 0, v[162:163]
	v_cvt_pk_bf16_f32 v171, v90, v91
	s_mov_b32 s4, 0x22c01000
	s_nop 0
	v_add_co_u32_e32 v172, vcc, s4, v166
	s_nop 1
	v_addc_co_u32_e32 v173, vcc, 0, v167, vcc
	s_nop 1
	global_store_dwordx2 v[172:173], v[170:171], off offset:-4096
	v_cvt_pk_bf16_f32 v170, v92, v93
	s_nop 4
	v_cvt_pk_bf16_f32 v171, v94, v95
	s_nop 4
	global_store_dwordx2 v[172:173], v[170:171], off
	v_cvt_pk_bf16_f32 v170, v84, v85
	s_nop 4
	v_cvt_pk_bf16_f32 v171, v86, v87
	s_mov_b32 s4, 0x22c03000
	s_nop 0
	v_add_co_u32_e32 v172, vcc, s4, v166
	s_nop 1
	v_addc_co_u32_e32 v173, vcc, 0, v167, vcc
	s_nop 1
	global_store_dwordx2 v[172:173], v[170:171], off offset:-4096
	v_cvt_pk_bf16_f32 v170, v80, v81
	s_nop 4
	v_cvt_pk_bf16_f32 v171, v82, v83
	global_store_dwordx2 v[172:173], v[170:171], off
	v_add_u32_e32 v169, 0x480, v137
	v_add_u32_e32 v170, 0x488, v137
	s_waitcnt vmcnt(11)
	ds_write2_b32 v137, v24, v25 offset1:1
	ds_write2_b32 v137, v26, v27 offset0:2 offset1:3
	ds_write2_b32 v169, v0, v1 offset1:1
	ds_write2_b32 v170, v2, v3 offset1:1
	s_waitcnt lgkmcnt(0)
	ds_read_u16 v157, v168 offset:72
	ds_read_u16 v171, v168 offset:108
	ds_read_u16 v172, v168
	ds_read_u16 v176, v168 offset:144
	ds_read_u16 v177, v168 offset:216
	ds_read_u16 v178, v168 offset:252
	ds_read_u16 v179, v168 offset:180
	ds_read_u16 v174, v168 offset:36
	s_waitcnt lgkmcnt(7)
	v_lshlrev_b32_e32 v173, 16, v157
	s_waitcnt lgkmcnt(5)
	v_lshlrev_b32_e32 v172, 16, v172
	v_pk_mul_f32 v[172:173], v[140:141], v[172:173]
	v_lshlrev_b32_e32 v175, 16, v171
	v_and_b32_sdwa v157, v173, v213 dst_sel:DWORD dst_unused:UNUSED_PAD src0_sel:WORD_1 src1_sel:DWORD
	v_and_b32_sdwa v171, v172, v213 dst_sel:DWORD dst_unused:UNUSED_PAD src0_sel:WORD_1 src1_sel:DWORD
	v_add3_u32 v157, v173, v157, s76
	v_add3_u32 v171, v172, v171, s76
	s_waitcnt lgkmcnt(3)
	v_lshlrev_b32_e32 v173, 16, v177
	v_lshlrev_b32_e32 v172, 16, v176
	s_waitcnt lgkmcnt(0)
	v_lshlrev_b32_e32 v174, 16, v174
	v_pk_mul_f32 v[172:173], v[144:145], v[172:173]
	v_lshlrev_b32_e32 v177, 16, v178
	v_lshlrev_b32_e32 v176, 16, v179
	v_pk_mul_f32 v[174:175], v[142:143], v[174:175]
	v_pk_mul_f32 v[176:177], v[146:147], v[176:177]
	v_and_b32_sdwa v178, v173, v213 dst_sel:DWORD dst_unused:UNUSED_PAD src0_sel:WORD_1 src1_sel:DWORD
	v_and_b32_sdwa v179, v172, v213 dst_sel:DWORD dst_unused:UNUSED_PAD src0_sel:WORD_1 src1_sel:DWORD
	v_add3_u32 v182, v173, v178, s76
	v_add3_u32 v172, v172, v179, s76
	v_bfe_u32 v173, v176, 16, 1
	v_bfe_u32 v178, v175, 16, 1
	v_bfe_u32 v179, v174, 16, 1
	v_bfe_u32 v180, v177, 16, 1
	v_lshrrev_b32_e32 v171, 16, v171
	v_lshrrev_b32_e32 v157, 16, v157
	v_lshrrev_b32_e32 v172, 16, v172
	v_add3_u32 v183, v177, v180, s76
	v_add3_u32 v177, v174, v179, s76
	v_add3_u32 v175, v175, v178, s76
	v_add3_u32 v173, v176, v173, s76
	v_and_or_b32 v174, v173, s75, v172
	v_and_or_b32 v173, v175, s75, v157
	v_and_or_b32 v172, v177, s75, v171
	ds_read_u16 v157, v168 offset:1152
	ds_read_u16 v171, v168 offset:1224
	ds_read_u16 v175, v168 offset:1260
	ds_read_u16 v180, v168 offset:1296
	ds_read_u16 v181, v168 offset:1368
	ds_read_u16 v184, v168 offset:1404
	ds_read_u16 v194, v168 offset:1332
	ds_read_u16 v178, v168 offset:1188
	s_waitcnt lgkmcnt(6)
	v_lshlrev_b32_e32 v177, 16, v171
	v_lshlrev_b32_e32 v176, 16, v157
	v_pk_mul_f32 v[176:177], v[148:149], v[176:177]
	s_waitcnt lgkmcnt(5)
	v_lshlrev_b32_e32 v179, 16, v175
	v_and_b32_sdwa v157, v177, v213 dst_sel:DWORD dst_unused:UNUSED_PAD src0_sel:WORD_1 src1_sel:DWORD
	v_and_b32_sdwa v171, v176, v213 dst_sel:DWORD dst_unused:UNUSED_PAD src0_sel:WORD_1 src1_sel:DWORD
	v_add3_u32 v157, v177, v157, s76
	v_add3_u32 v171, v176, v171, s76
	s_waitcnt lgkmcnt(3)
	v_lshlrev_b32_e32 v177, 16, v181
	v_lshlrev_b32_e32 v176, 16, v180
	v_pk_mul_f32 v[176:177], v[152:153], v[176:177]
	s_waitcnt lgkmcnt(2)
	v_lshlrev_b32_e32 v181, 16, v184
	s_waitcnt lgkmcnt(1)
	v_lshlrev_b32_e32 v180, 16, v194
	s_waitcnt lgkmcnt(0)
	v_lshlrev_b32_e32 v178, 16, v178
	v_pk_mul_f32 v[180:181], v[154:155], v[180:181]
	v_and_b32_sdwa v175, v177, v213 dst_sel:DWORD dst_unused:UNUSED_PAD src0_sel:WORD_1 src1_sel:DWORD
	v_and_b32_sdwa v184, v176, v213 dst_sel:DWORD dst_unused:UNUSED_PAD src0_sel:WORD_1 src1_sel:DWORD
	v_pk_mul_f32 v[178:179], v[150:151], v[178:179]
	v_add3_u32 v194, v177, v175, s76
	v_add3_u32 v175, v176, v184, s76
	v_bfe_u32 v176, v180, 16, 1
	v_lshrrev_b32_e32 v175, 16, v175
	v_bfe_u32 v184, v178, 16, 1
	v_add3_u32 v176, v180, v176, s76
	v_add3_u32 v184, v178, v184, s76
	v_and_or_b32 v178, v176, s75, v175
	v_perm_b32 v175, v183, v182, s71
	v_bfe_u32 v177, v179, 16, 1
	v_lshrrev_b32_e32 v157, 16, v157
	v_bfe_u32 v195, v181, 16, 1
	v_add3_u32 v177, v179, v177, s76
	v_lshrrev_b32_e32 v171, 16, v171
	v_add3_u32 v181, v181, v195, s76
	v_and_or_b32 v177, v177, s75, v157
	v_mov_b32_e32 v157, v156
	v_and_or_b32 v176, v184, s75, v171
	v_pk_mul_f32 v[90:91], v[156:157], v[90:91]
	v_pk_mul_f32 v[88:89], v[158:159], v[88:89]
	v_perm_b32 v179, v181, v194, s71
	v_pk_mul_f32 v[94:95], v[156:157], v[94:95]
	v_pk_mul_f32 v[92:93], v[158:159], v[92:93]
	v_pk_mul_f32 v[86:87], v[156:157], v[86:87]
	v_pk_mul_f32 v[84:85], v[158:159], v[84:85]
	v_pk_mul_f32 v[82:83], v[156:157], v[82:83]
	v_pk_mul_f32 v[80:81], v[158:159], v[80:81]
	v_mfma_f32_16x16x32_bf16 v[88:91], v[172:175], v[4:7], v[88:91]
	s_waitcnt lgkmcnt(0)
	s_cmp_eq_u32 s15, 30
	v_mfma_f32_16x16x32_bf16 v[92:95], v[172:175], v[8:11], v[92:95]
	v_mfma_f32_16x16x32_bf16 v[84:87], v[172:175], v[28:31], v[84:87]
	s_waitcnt vmcnt(9)
	v_mfma_f32_16x16x32_bf16 v[80:83], v[172:175], v[48:51], v[80:83]
	v_mfma_f32_16x16x32_bf16 v[88:91], v[176:179], v[40:43], v[88:91]
	v_mfma_f32_16x16x32_bf16 v[92:95], v[176:179], v[12:15], v[92:95]
	v_mfma_f32_16x16x32_bf16 v[84:87], v[176:179], v[32:35], v[84:87]
	s_waitcnt vmcnt(8)
	v_mfma_f32_16x16x32_bf16 v[80:83], v[176:179], v[52:55], v[80:83]
	s_cbranch_scc1 .LBB0_513
; __device__ __forceinline__ void scan_load(ScanOps& o, const bf16* kg, const bf16* vrow, int n) {
; #pragma unroll
;     for (int i = 0; i < 2; ++i) o.kp[i] = ld_u4(kg + (size_t)(n * CH + i * 32) * TOKP);
; #pragma unroll
;     for (int eb = 0; eb < 4; ++eb)
; #pragma unroll
;         for (int ks = 0; ks < 2; ++ks) o.va[eb][ks] = ld_b8(vrow + (size_t)eb * 16 * SWPP + n * CH + ks * 32);
; }
	s_cmp_gt_u32 s15, 27
	s_cbranch_scc1 .LBB0_512
	v_lshl_add_u64 v[0:1], s[62:63], 0, v[164:165]
	v_add_co_u32_e32 v2, vcc, 0x121ed000, v0
	v_lshl_add_u64 v[48:49], s[62:63], 0, v[160:161]
	s_nop 0
	v_addc_co_u32_e32 v3, vcc, 0, v1, vcc
	v_add_co_u32_e32 v0, vcc, 0x1223f000, v0
	s_nop 1
	v_addc_co_u32_e32 v1, vcc, 0, v1, vcc
	v_add_co_u32_e32 v8, vcc, 0x1e840000, v48
	global_load_dwordx4 v[24:27], v[2:3], off offset:2048
	s_nop 0
	global_load_dwordx4 v[0:3], v[0:1], off offset:2048
	v_addc_co_u32_e32 v9, vcc, 0, v49, vcc
	v_add_co_u32_e32 v12, vcc, 0x1e8c1000, v48
	global_load_dwordx4 v[4:7], v[8:9], off offset:384
	global_load_dwordx4 v[40:43], v[8:9], off offset:448
	v_addc_co_u32_e32 v13, vcc, 0, v49, vcc
	v_add_co_u32_e32 v32, vcc, 0x1e942000, v48
	global_load_dwordx4 v[8:11], v[12:13], off offset:384
	s_nop 0
	global_load_dwordx4 v[12:15], v[12:13], off offset:448
	v_addc_co_u32_e32 v33, vcc, 0, v49, vcc
	v_add_co_u32_e32 v52, vcc, 0x1e9c3000, v48
	global_load_dwordx4 v[28:31], v[32:33], off offset:384
	s_nop 0
	global_load_dwordx4 v[32:35], v[32:33], off offset:448
	v_addc_co_u32_e32 v53, vcc, 0, v49, vcc
	global_load_dwordx4 v[48:51], v[52:53], off offset:384
	s_nop 0
	global_load_dwordx4 v[52:55], v[52:53], off offset:448
; #define LAS __attribute__((address_space(3)))
; #define LDS_WAIT() asm volatile("s_waitcnt lgkmcnt(0)" ::: "memory")
; __device__ __forceinline__ unsigned pk2(float lo, float hi) { return f2bf(lo) | (f2bf(hi) << 16); }
; __device__ __forceinline__ f32x4 mfma16(bf16x8 a, bf16x8 b, f32x4 c) { return __builtin_amdgcn_mfma_f32_16x16x32_bf16(a, b, c, 0, 0, 0); }
; __device__ __forceinline__ void scan_step(f32x4 (&st)[4], const ScanOps& o, const float (&dec)[16], LAS unsigned char* kw, const LAS unsigned char* kr, bf16* sp, int n, float cd) {
; #pragma unroll
;     for (int eb = 0; eb < 4; ++eb) { u32x2 w; w.x = pk2(st[eb][0], st[eb][1]); w.y = pk2(st[eb][2], st[eb][3]); st_u2(sp + (size_t)n * HD * HD + eb * 16 * HD, w); }
; #pragma unroll
;     for (int i = 0; i < 2; ++i)
; #pragma unroll
;         for (int d = 0; d < 4; ++d) *(LAS unsigned*)(kw + i * 32 * SC_PITCH + d * 4) = o.kp[i][d];
;     LDS_WAIT(); asm volatile("" ::: "memory");
;     bf16x8 ka[2];
; #pragma unroll
;     for (int ks = 0; ks < 2; ++ks) { u32x4 w;
; #pragma unroll
;         for (int j = 0; j < 4; ++j) { const unsigned e0 = *(const LAS unsigned short*)(kr + (ks * 32 + 2 * j) * SC_PITCH), e1 = *(const LAS unsigned short*)(kr + (ks * 32 + 2 * j + 1) * SC_PITCH);
;             w[j] = pk2(bf_lo(e0) * dec[ks * 8 + 2 * j], bf_lo(e1) * dec[ks * 8 + 2 * j + 1]); }
;         ka[ks] = __builtin_bit_cast(bf16x8, w); }
;     LDS_WAIT(); asm volatile("" ::: "memory");
; #pragma unroll
;     for (int eb = 0; eb < 4; ++eb) { st[eb] *= cd;
; #pragma unroll
;         for (int ks = 0; ks < 2; ++ks) st[eb] = mfma16(ka[ks], o.va[eb][ks], st[eb]); }
.LBB0_512:
	s_nop 0
	s_nop 4
	v_cvt_pk_bf16_f32 v172, v88, v89
	s_nop 4
	v_cvt_pk_bf16_f32 v173, v90, v91
	s_mov_b32 s4, 0x22c09000
	s_nop 0
	v_add_co_u32_e32 v174, vcc, s4, v166
	s_nop 1
	v_addc_co_u32_e32 v175, vcc, 0, v167, vcc
	s_nop 1
	global_store_dwordx2 v[174:175], v[172:173], off offset:-4096
	v_cvt_pk_bf16_f32 v172, v92, v93
	s_nop 4
	v_cvt_pk_bf16_f32 v173, v94, v95
	s_nop 4
	global_store_dwordx2 v[174:175], v[172:173], off
	v_cvt_pk_bf16_f32 v172, v84, v85
	s_nop 4
	v_cvt_pk_bf16_f32 v173, v86, v87
	s_mov_b32 s4, 0x22c0b000
	s_nop 0
	v_add_co_u32_e32 v174, vcc, s4, v166
	s_nop 1
	v_addc_co_u32_e32 v175, vcc, 0, v167, vcc
	s_nop 1
	global_store_dwordx2 v[174:175], v[172:173], off offset:-4096
	v_cvt_pk_bf16_f32 v172, v80, v81
	s_nop 4
	v_cvt_pk_bf16_f32 v173, v82, v83
	global_store_dwordx2 v[174:175], v[172:173], off
	ds_write2_b32 v137, v16, v17 offset1:1
	ds_write2_b32 v137, v18, v19 offset0:2 offset1:3
	ds_write2_b32 v169, v20, v21 offset1:1
	ds_write2_b32 v170, v22, v23 offset1:1
	s_waitcnt lgkmcnt(0)
	ds_read_u16 v157, v168 offset:72
	ds_read_u16 v171, v168 offset:108
	ds_read_u16 v172, v168
	ds_read_u16 v176, v168 offset:144
	ds_read_u16 v177, v168 offset:216
	ds_read_u16 v178, v168 offset:252
	ds_read_u16 v179, v168 offset:180
	ds_read_u16 v174, v168 offset:36
	s_waitcnt lgkmcnt(7)
	v_lshlrev_b32_e32 v173, 16, v157
	s_waitcnt lgkmcnt(5)
	v_lshlrev_b32_e32 v172, 16, v172
	v_pk_mul_f32 v[172:173], v[140:141], v[172:173]
	v_lshlrev_b32_e32 v175, 16, v171
	v_and_b32_sdwa v157, v173, v213 dst_sel:DWORD dst_unused:UNUSED_PAD src0_sel:WORD_1 src1_sel:DWORD
	v_and_b32_sdwa v171, v172, v213 dst_sel:DWORD dst_unused:UNUSED_PAD src0_sel:WORD_1 src1_sel:DWORD
	v_add3_u32 v157, v173, v157, s76
	v_add3_u32 v171, v172, v171, s76
	s_waitcnt lgkmcnt(3)
	v_lshlrev_b32_e32 v173, 16, v177
	v_lshlrev_b32_e32 v172, 16, v176
	s_waitcnt lgkmcnt(0)
	v_lshlrev_b32_e32 v174, 16, v174
	v_pk_mul_f32 v[172:173], v[144:145], v[172:173]
	v_lshlrev_b32_e32 v177, 16, v178
	v_lshlrev_b32_e32 v176, 16, v179
	v_pk_mul_f32 v[174:175], v[142:143], v[174:175]
	v_pk_mul_f32 v[176:177], v[146:147], v[176:177]
	v_and_b32_sdwa v178, v173, v213 dst_sel:DWORD dst_unused:UNUSED_PAD src0_sel:WORD_1 src1_sel:DWORD
	v_and_b32_sdwa v179, v172, v213 dst_sel:DWORD dst_unused:UNUSED_PAD src0_sel:WORD_1 src1_sel:DWORD
	v_add3_u32 v182, v173, v178, s76
	v_add3_u32 v172, v172, v179, s76
	v_bfe_u32 v173, v176, 16, 1
	v_bfe_u32 v178, v175, 16, 1
	v_bfe_u32 v179, v174, 16, 1
	v_bfe_u32 v180, v177, 16, 1
	v_lshrrev_b32_e32 v171, 16, v171
	v_lshrrev_b32_e32 v157, 16, v157
	v_lshrrev_b32_e32 v172, 16, v172
	v_add3_u32 v183, v177, v180, s76
	v_add3_u32 v177, v174, v179, s76
	v_add3_u32 v175, v175, v178, s76
	v_add3_u32 v173, v176, v173, s76
	v_and_or_b32 v174, v173, s75, v172
	v_and_or_b32 v173, v175, s75, v157
	v_and_or_b32 v172, v177, s75, v171
	ds_read_u16 v157, v168 offset:1152
	ds_read_u16 v171, v168 offset:1224
	ds_read_u16 v175, v168 offset:1260
	ds_read_u16 v180, v168 offset:1296
	ds_read_u16 v181, v168 offset:1368
	ds_read_u16 v184, v168 offset:1404
	ds_read_u16 v194, v168 offset:1332
	ds_read_u16 v178, v168 offset:1188
	s_waitcnt lgkmcnt(6)
	v_lshlrev_b32_e32 v177, 16, v171
	v_lshlrev_b32_e32 v176, 16, v157
	v_pk_mul_f32 v[176:177], v[148:149], v[176:177]
	s_waitcnt lgkmcnt(5)
	v_lshlrev_b32_e32 v179, 16, v175
	v_and_b32_sdwa v157, v177, v213 dst_sel:DWORD dst_unused:UNUSED_PAD src0_sel:WORD_1 src1_sel:DWORD
	v_and_b32_sdwa v171, v176, v213 dst_sel:DWORD dst_unused:UNUSED_PAD src0_sel:WORD_1 src1_sel:DWORD
	v_add3_u32 v157, v177, v157, s76
	v_add3_u32 v171, v176, v171, s76
	s_waitcnt lgkmcnt(3)
	v_lshlrev_b32_e32 v177, 16, v181
	v_lshlrev_b32_e32 v176, 16, v180
	v_pk_mul_f32 v[176:177], v[152:153], v[176:177]
	s_waitcnt lgkmcnt(2)
	v_lshlrev_b32_e32 v181, 16, v184
	s_waitcnt lgkmcnt(1)
	v_lshlrev_b32_e32 v180, 16, v194
	s_waitcnt lgkmcnt(0)
	v_lshlrev_b32_e32 v178, 16, v178
	v_pk_mul_f32 v[180:181], v[154:155], v[180:181]
	v_and_b32_sdwa v175, v177, v213 dst_sel:DWORD dst_unused:UNUSED_PAD src0_sel:WORD_1 src1_sel:DWORD
	v_and_b32_sdwa v184, v176, v213 dst_sel:DWORD dst_unused:UNUSED_PAD src0_sel:WORD_1 src1_sel:DWORD
	v_pk_mul_f32 v[178:179], v[150:151], v[178:179]
	v_add3_u32 v194, v177, v175, s76
	v_add3_u32 v175, v176, v184, s76
	v_bfe_u32 v176, v180, 16, 1
	v_lshrrev_b32_e32 v175, 16, v175
	v_bfe_u32 v184, v178, 16, 1
	v_add3_u32 v176, v180, v176, s76
	v_add3_u32 v184, v178, v184, s76
	v_and_or_b32 v178, v176, s75, v175
	v_perm_b32 v175, v183, v182, s71
	v_bfe_u32 v177, v179, 16, 1
	v_lshrrev_b32_e32 v157, 16, v157
	v_bfe_u32 v195, v181, 16, 1
	v_add3_u32 v177, v179, v177, s76
	v_lshrrev_b32_e32 v171, 16, v171
	v_add3_u32 v181, v181, v195, s76
	v_and_or_b32 v177, v177, s75, v157
	v_mov_b32_e32 v157, v156
	v_and_or_b32 v176, v184, s75, v171
	v_pk_mul_f32 v[90:91], v[156:157], v[90:91]
	v_pk_mul_f32 v[88:89], v[158:159], v[88:89]
	v_perm_b32 v179, v181, v194, s71
	v_pk_mul_f32 v[94:95], v[156:157], v[94:95]
	v_pk_mul_f32 v[92:93], v[158:159], v[92:93]
	v_pk_mul_f32 v[86:87], v[156:157], v[86:87]
	v_pk_mul_f32 v[84:85], v[158:159], v[84:85]
	v_pk_mul_f32 v[82:83], v[156:157], v[82:83]
	v_pk_mul_f32 v[80:81], v[158:159], v[80:81]
	v_mfma_f32_16x16x32_bf16 v[88:91], v[172:175], v[36:39], v[88:91]
	s_waitcnt lgkmcnt(0)
	s_waitcnt vmcnt(13)
	v_mfma_f32_16x16x32_bf16 v[92:95], v[172:175], v[56:59], v[92:95]
	s_waitcnt vmcnt(11)
	v_mfma_f32_16x16x32_bf16 v[84:87], v[172:175], v[64:67], v[84:87]
	s_waitcnt vmcnt(9)
	v_mfma_f32_16x16x32_bf16 v[80:83], v[172:175], v[72:75], v[80:83]
	v_mfma_f32_16x16x32_bf16 v[88:91], v[176:179], v[44:47], v[88:91]
	v_mfma_f32_16x16x32_bf16 v[92:95], v[176:179], v[60:63], v[92:95]
	v_mfma_f32_16x16x32_bf16 v[84:87], v[176:179], v[68:71], v[84:87]
	s_waitcnt vmcnt(8)
	v_mfma_f32_16x16x32_bf16 v[80:83], v[176:179], v[76:79], v[80:83]

; #define LAS __attribute__((address_space(3)))
; __device__ __forceinline__ f32x4 mfma16(bf16x8 a, bf16x8 b, f32x4 c) { return __builtin_amdgcn_mfma_f32_16x16x32_bf16(a, b, c, 0, 0, 0); }
; __device__ __forceinline__ float rq_max(float v) { v = fmaxf(v, __shfl_xor(v, 16)); v = fmaxf(v, __shfl_xor(v, 32)); return v; }
; __device__ __forceinline__ float fexp2(float x) { return __builtin_amdgcn_exp2f(x); }
; __device__ __forceinline__ void attn_wg_task(const Frame& F, int l, int task) {
;     ...
;             for (int qb = 0; qb < 2; ++qb) {
;                 const float mxr = rq_max(mx[qb]);
;                 const float mn = fmaxf(m_run[qb], mxr); alpha[qb] = fexp2(m_run[qb] - mn);
;                 moved = moved || (mn > m_run[qb]);
;                 float ps = 0.f;
; #pragma unroll
;                 for (int g = 0; g < 2; ++g) {
; #pragma unroll
;                     for (int ab = 0; ab < 2; ++ab)
; #pragma unroll
;                         for (int e = 0; e < 4; ++e) { const float p = fexp2(sa[qb][g][ab][e] - mn); sa[qb][g][ab][e] = p; ps += p; }
;                     Pf[qb][g] = pack8(sa[qb][g][0], sa[qb][g][1]);
;                 }
;                 l_run[qb] = l_run[qb] * alpha[qb] + ps; m_run[qb] = mn;
;             }
;             if (__any(moved)) {
; #pragma unroll
;                 for (int qb = 0; qb < 2; ++qb)
; #pragma unroll
;                     for (int db = 0; db < 8; ++db) O[qb][db] *= alpha[qb];
;             }
; #pragma unroll
;             for (int g = 0; g < 2; ++g)
; #pragma unroll
;                 for (int db = 0; db < 8; ++db) { const bf16x8 vf = *(const LAS bf16x8*)(vb + db * 16 * A_VP + g * 64); O[0][db] = mfma16(vf, Pf[0][g], O[0][db]); O[1][db] = mfma16(vf, Pf[1][g], O[1][db]); }
.LBB0_516:
	v_sub_f32_e32 v65, v72, v64
	v_exp_f32_e32 v71, v65
	v_sub_f32_e32 v65, v73, v64
	v_exp_f32_e32 v99, v65
	v_sub_f32_e32 v65, v74, v64
	v_exp_f32_e32 v101, v65
	v_sub_f32_e32 v65, v75, v64
	v_exp_f32_e32 v103, v65
	v_sub_f32_e32 v65, v84, v64
	v_exp_f32_e32 v105, v65
	v_sub_f32_e32 v65, v85, v64
	v_exp_f32_e32 v107, v65
	v_sub_f32_e32 v65, v86, v64
	v_exp_f32_e32 v85, v65
	v_sub_f32_e32 v65, v87, v64
	v_exp_f32_e32 v87, v65
	s_nop 5
	v_cvt_pk_bf16_f32 v75, v85, v87
	v_sub_f32_e32 v65, v92, v64
	v_exp_f32_e32 v109, v65
	v_sub_f32_e32 v65, v93, v64
	v_exp_f32_e32 v93, v65
	v_sub_f32_e32 v65, v94, v64
	v_exp_f32_e32 v111, v65
	v_sub_f32_e32 v65, v95, v64
	v_exp_f32_e32 v95, v65
	v_sub_f32_e32 v65, v124, v64
	v_exp_f32_e32 v113, v65
	v_sub_f32_e32 v65, v125, v64
	v_exp_f32_e32 v115, v65
	v_sub_f32_e32 v65, v126, v64
	s_nop 0
	v_exp_f32_e32 v117, v65
	v_sub_f32_e32 v64, v127, v64
	s_nop 4
	v_exp_f32_e32 v119, v64
	s_nop 7
	v_cvt_pk_bf16_f32 v74, v105, v107
	v_cvt_pk_bf16_f32 v73, v101, v103
	s_nop 1
	v_cvt_pk_bf16_f32 v72, v71, v99
	s_nop 7
	s_nop 7
	s_nop 1
	v_cvt_pk_bf16_f32 v67, v117, v119
	v_cvt_pk_bf16_f32 v64, v109, v93
	v_sub_f32_e32 v69, v76, v68
	v_cvt_pk_bf16_f32 v66, v113, v115
	v_cvt_pk_bf16_f32 v65, v111, v95
	v_exp_f32_e32 v70, v69
	v_sub_f32_e32 v69, v77, v68
	v_exp_f32_e32 v98, v69
	v_sub_f32_e32 v69, v78, v68
	v_exp_f32_e32 v100, v69
	v_sub_f32_e32 v69, v79, v68
	v_exp_f32_e32 v102, v69
	v_sub_f32_e32 v69, v82, v68
	v_exp_f32_e32 v104, v69
	v_sub_f32_e32 v69, v83, v68
	v_exp_f32_e32 v106, v69
	v_sub_f32_e32 v69, v80, v68
	v_exp_f32_e32 v84, v69
	v_sub_f32_e32 v69, v81, v68
	v_exp_f32_e32 v86, v69
	v_bfe_u32 v79, v70, 16, 1
	s_nop 4
	v_pk_add_f32 v[76:77], v[70:71], 0 op_sel_hi:[1,0]
	v_add3_u32 v70, v70, v79, s76
	v_cvt_pk_bf16_f32 v79, v84, v86
	v_sub_f32_e32 v69, v88, v68
	v_exp_f32_e32 v108, v69
	v_sub_f32_e32 v69, v89, v68
	v_pk_add_f32 v[76:77], v[98:99], v[76:77]
	v_exp_f32_e32 v92, v69
	v_sub_f32_e32 v69, v90, v68
	v_pk_add_f32 v[76:77], v[100:101], v[76:77]
	v_exp_f32_e32 v110, v69
	v_sub_f32_e32 v69, v91, v68
	v_pk_add_f32 v[76:77], v[102:103], v[76:77]
	v_exp_f32_e32 v94, v69
	v_sub_f32_e32 v69, v120, v68
	v_pk_add_f32 v[76:77], v[104:105], v[76:77]
	v_exp_f32_e32 v112, v69
	v_sub_f32_e32 v69, v121, v68
	v_pk_add_f32 v[82:83], v[106:107], v[76:77]
	v_bfe_u32 v77, v98, 16, 1
	v_exp_f32_e32 v114, v69
	v_sub_f32_e32 v69, v122, v68
	v_add3_u32 v80, v98, v77, s76
	s_nop 0
	v_exp_f32_e32 v116, v69
	v_sub_f32_e32 v68, v123, v68
	s_nop 2
	v_exp_f32_e32 v118, v68
	s_nop 4
	v_lshrrev_b32_e32 v70, 16, v70
	s_nop 0
	v_cvt_pk_bf16_f32 v77, v100, v102
	s_nop 0
	v_cvt_pk_bf16_f32 v78, v104, v106
	v_and_or_b32 v76, v80, s75, v70
	s_nop 0
	v_bfe_u32 v71, v110, 16, 1
	s_nop 3
	v_add3_u32 v71, v110, v71, s76
	s_nop 1
	v_lshrrev_b32_e32 v90, 16, v71
	s_nop 1
	v_cvt_pk_bf16_f32 v71, v116, v118
	v_cvt_pk_bf16_f32 v68, v108, v92
	v_pk_add_f32 v[80:81], v[84:85], v[82:83]
	ds_read_b128 v[82:85], v205 offset:53248
	s_waitcnt lgkmcnt(0)
	v_mfma_f32_16x16x32_bf16 v[32:35], v[82:85], v[72:75], v[32:35]
	v_add_f32_e64 v80, v86, v80
	v_add_f32_e64 v81, v87, v81
	v_bfe_u32 v89, v112, 16, 1
	v_pk_add_f32 v[80:81], v[108:109], v[80:81]
	v_mfma_f32_16x16x32_bf16 v[4:7], v[82:85], v[76:79], v[4:7]
	ds_read_b128 v[82:85], v205 offset:55552
	v_pk_add_f32 v[80:81], v[92:93], v[80:81]
	s_nop 0
	s_waitcnt lgkmcnt(0)
	v_mfma_f32_16x16x32_bf16 v[36:39], v[82:85], v[72:75], v[36:39]
	v_add_f32_e64 v80, v110, v80
	v_add_f32_e64 v81, v111, v81
	s_nop 0
	v_pk_add_f32 v[80:81], v[94:95], v[80:81]
	v_mfma_f32_16x16x32_bf16 v[8:11], v[82:85], v[76:79], v[8:11]
	ds_read_b128 v[82:85], v205 offset:57856
	v_pk_add_f32 v[80:81], v[112:113], v[80:81]
	v_add3_u32 v89, v112, v89, s76
	s_waitcnt lgkmcnt(0)
	v_mfma_f32_16x16x32_bf16 v[40:43], v[82:85], v[72:75], v[40:43]
	v_add_f32_e64 v80, v114, v80
	v_add_f32_e64 v81, v115, v81
	s_nop 0
	v_pk_add_f32 v[80:81], v[116:117], v[80:81]
	v_mfma_f32_16x16x32_bf16 v[0:3], v[82:85], v[76:79], v[0:3]
	ds_read_b128 v[82:85], v205 offset:60160
	v_pk_add_f32 v[80:81], v[118:119], v[80:81]
	s_nop 0
	s_waitcnt lgkmcnt(0)
	v_mfma_f32_16x16x32_bf16 v[44:47], v[82:85], v[72:75], v[44:47]
	v_fma_f32 v150, v150, v96, v80
	v_fma_f32 v151, v151, v97, v81
	v_add_u32_e32 v80, 0x8800, v205
	v_lshrrev_b32_e32 v88, 16, v89
	v_mfma_f32_16x16x32_bf16 v[12:15], v[82:85], v[76:79], v[12:15]
	ds_read_b128 v[82:85], v205 offset:62464
	v_cvt_pk_bf16_f32 v69, v110, v94
	v_cvt_pk_bf16_f32 v70, v112, v114
	s_waitcnt lgkmcnt(0)
	v_mfma_f32_16x16x32_bf16 v[48:51], v[82:85], v[72:75], v[48:51]
	v_mfma_f32_16x16x32_bf16 v[16:19], v[82:85], v[76:79], v[16:19]
	ds_read_b128 v[82:85], v205 offset:64768
	s_waitcnt lgkmcnt(0)
	v_mfma_f32_16x16x32_bf16 v[52:55], v[82:85], v[72:75], v[52:55]
	v_mfma_f32_16x16x32_bf16 v[20:23], v[82:85], v[76:79], v[20:23]
	ds_read_b128 v[82:85], v80 offset:32256
	s_waitcnt lgkmcnt(0)
	v_mfma_f32_16x16x32_bf16 v[56:59], v[82:85], v[72:75], v[56:59]
	v_mfma_f32_16x16x32_bf16 v[24:27], v[82:85], v[76:79], v[24:27]
	ds_read_b128 v[82:85], v80 offset:34560
	s_waitcnt lgkmcnt(0)
	v_mfma_f32_16x16x32_bf16 v[60:63], v[82:85], v[72:75], v[60:63]
	ds_read_b128 v[72:75], v205 offset:53312
	s_waitcnt lgkmcnt(0)
	v_mfma_f32_16x16x32_bf16 v[32:35], v[72:75], v[64:67], v[32:35]
	v_mfma_f32_16x16x32_bf16 v[4:7], v[72:75], v[68:71], v[4:7]
	ds_read_b128 v[72:75], v205 offset:55616
	s_waitcnt lgkmcnt(0)
	v_mfma_f32_16x16x32_bf16 v[36:39], v[72:75], v[64:67], v[36:39]
	v_mfma_f32_16x16x32_bf16 v[8:11], v[72:75], v[68:71], v[8:11]
	ds_read_b128 v[72:75], v205 offset:57920
	s_waitcnt lgkmcnt(0)
	v_mfma_f32_16x16x32_bf16 v[40:43], v[72:75], v[64:67], v[40:43]
	v_mfma_f32_16x16x32_bf16 v[0:3], v[72:75], v[68:71], v[0:3]
	ds_read_b128 v[72:75], v205 offset:60224
	s_waitcnt lgkmcnt(0)
	v_mfma_f32_16x16x32_bf16 v[44:47], v[72:75], v[64:67], v[44:47]
	v_mfma_f32_16x16x32_bf16 v[12:15], v[72:75], v[68:71], v[12:15]
	ds_read_b128 v[72:75], v205 offset:62528
	s_waitcnt lgkmcnt(0)
	v_mfma_f32_16x16x32_bf16 v[48:51], v[72:75], v[64:67], v[48:51]
	v_mfma_f32_16x16x32_bf16 v[16:19], v[72:75], v[68:71], v[16:19]
	ds_read_b128 v[72:75], v205 offset:64832
	s_waitcnt lgkmcnt(0)
	v_mfma_f32_16x16x32_bf16 v[52:55], v[72:75], v[64:67], v[52:55]
	v_mfma_f32_16x16x32_bf16 v[20:23], v[72:75], v[68:71], v[20:23]
	ds_read_b128 v[72:75], v80 offset:32320
	s_waitcnt lgkmcnt(0)
	v_mfma_f32_16x16x32_bf16 v[56:59], v[72:75], v[64:67], v[56:59]
	v_mfma_f32_16x16x32_bf16 v[24:27], v[72:75], v[68:71], v[24:27]
	ds_read_b128 v[72:75], v80 offset:34624
	v_mfma_f32_16x16x32_bf16 v[28:31], v[82:85], v[76:79], v[28:31]
	s_waitcnt lgkmcnt(0)
	v_mfma_f32_16x16x32_bf16 v[60:63], v[72:75], v[64:67], v[60:63]
	v_mfma_f32_16x16x32_bf16 v[28:31], v[72:75], v[68:71], v[28:31]
; __device__ __forceinline__ unsigned pk2(float lo, float hi) { return f2bf(lo) | (f2bf(hi) << 16); }
; __device__ __forceinline__ float rq_sum(float v) { v += __shfl_xor(v, 16); v += __shfl_xor(v, 32); return v; }
; __device__ __forceinline__ float frsq(float x) { return __builtin_amdgcn_rsqf(x); }
; __device__ __forceinline__ void attn_wg_task(const Frame& F, int l, int task) {
;     ...
;     for (int qb = 0; qb < 2; ++qb) {
;         const int tq = tq0 + qb * 16;
;         const float inv = 1.0f / rq_sum(l_run[qb]);
;         float ss = 0.f;
; #pragma unroll
;         for (int db = 0; db < 8; ++db) { O[qb][db] *= inv; ss += (O[qb][db][0] * O[qb][db][0] + O[qb][db][1] * O[qb][db][1]) + (O[qb][db][2] * O[qb][db][2] + O[qb][db][3] * O[qb][db][3]); }
;         const float rstd = frsq(rq_sum(ss) * (1.f / HD) + EPS);
; #pragma unroll
;         for (int db = 0; db < 8; ++db) {
;             const int d0 = h * HD + db * 16 + rq * 4;
;             const f32x4 g4 = ld_f4(F.attn_g + l * 1024 + d0);
;             u32x2 o; o.x = pk2(O[qb][db][0] * rstd * g4[0], O[qb][db][1] * rstd * g4[1]); o.y = pk2(O[qb][db][2] * rstd * g4[2], O[qb][db][3] * rstd * g4[3]);
;             st_u2(MIX + (size_t)tq * D + d0, o);
.LBB0_517:
	ds_bpermute_b32 v64, v202, v151
	v_lshl_or_b32 v82, v204, 2, s17
	v_readlane_b32 s2, v251, 53
	v_readlane_b32 s3, v251, 54
	s_waitcnt lgkmcnt(0)
	v_add_f32_e32 v64, v151, v64
	ds_bpermute_b32 v65, v203, v64
	s_barrier
	s_waitcnt lgkmcnt(0)
	v_lshlrev_b32_e32 v184, 1, v82
	v_readlane_b32 s4, v253, 59
	v_add_f32_e32 v64, v64, v65
	v_div_scale_f32 v65, s[0:1], v64, v64, 1.0
	v_rcp_f32_e32 v66, v65
	v_readlane_b32 s5, v253, 60
	v_fma_f32 v67, -v65, v66, 1.0
	v_fmac_f32_e32 v66, v67, v66
	v_div_scale_f32 v67, vcc, 1.0, v64, 1.0
	v_mul_f32_e32 v68, v67, v66
	v_fma_f32 v69, -v65, v68, v67
	v_fmac_f32_e32 v68, v69, v66
	v_fma_f32 v65, -v65, v68, v67
	v_div_fmas_f32 v65, v65, v66, v68
	v_div_fixup_f32 v84, v65, v64, 1.0
	v_pk_mul_f32 v[80:81], v[32:33], v[84:85] op_sel_hi:[1,0]
	v_pk_mul_f32 v[76:77], v[36:37], v[84:85] op_sel_hi:[1,0]
	v_pk_mul_f32 v[78:79], v[34:35], v[84:85] op_sel_hi:[1,0]
	v_pk_mul_f32 v[74:75], v[38:39], v[84:85] op_sel_hi:[1,0]
	v_mov_b32_e32 v34, v81
	v_mov_b32_e32 v35, v77
	v_mov_b32_e32 v32, v80
	v_mov_b32_e32 v33, v76
	v_pk_mul_f32 v[34:35], v[34:35], v[34:35]
	v_mov_b32_e32 v36, v79
	v_mov_b32_e32 v37, v75
	v_pk_fma_f32 v[32:33], v[32:33], v[32:33], v[34:35]
	v_mov_b32_e32 v34, v78
	v_mov_b32_e32 v35, v74
	v_pk_mul_f32 v[36:37], v[36:37], v[36:37]
	v_pk_mul_f32 v[72:73], v[40:41], v[84:85] op_sel_hi:[1,0]
	v_pk_fma_f32 v[34:35], v[34:35], v[34:35], v[36:37]
	v_pk_mul_f32 v[70:71], v[42:43], v[84:85] op_sel_hi:[1,0]
	v_pk_add_f32 v[32:33], v[32:33], v[34:35]
	v_pk_mul_f32 v[34:35], v[70:71], v[70:71]
	v_pk_add_f32 v[32:33], v[32:33], v[32:33] op_sel_hi:[0,1]
	v_pk_mul_f32 v[36:37], v[72:73], v[72:73]
	v_pk_mul_f32 v[68:69], v[44:45], v[84:85] op_sel_hi:[1,0]
	v_pk_mov_b32 v[38:39], v[36:37], v[34:35] op_sel:[1,0]
	v_mov_b32_e32 v37, v35
	v_pk_mul_f32 v[66:67], v[46:47], v[84:85] op_sel_hi:[1,0]
	v_mul_f32_e32 v32, v68, v68
	v_pk_add_f32 v[34:35], v[38:39], v[36:37]
	v_pk_fma_f32 v[36:37], v[68:69], v[68:69], v[32:33] op_sel_hi:[1,1,0]
	v_mul_f32_e32 v32, v66, v66
	v_pk_add_f32 v[34:35], v[34:35], v[34:35] op_sel_hi:[0,1]
	v_pk_fma_f32 v[38:39], v[66:67], v[66:67], v[32:33] op_sel_hi:[1,1,0]
	v_pk_mul_f32 v[50:51], v[50:51], v[84:85] op_sel_hi:[1,0]
	v_pk_mul_f32 v[64:65], v[48:49], v[84:85] op_sel_hi:[1,0]
	v_mul_f32_e32 v34, v50, v50
	v_mul_f32_e32 v36, v64, v64
	v_mul_f32_e32 v38, v65, v65
	v_mul_f32_e32 v32, v51, v51
	v_pk_add_f32 v[36:37], v[36:37], v[38:39]
	v_pk_add_f32 v[32:33], v[34:35], v[32:33]
	v_pk_mul_f32 v[48:49], v[52:53], v[84:85] op_sel_hi:[1,0]
	v_pk_add_f32 v[32:33], v[36:37], v[32:33]
	v_pk_mul_f32 v[46:47], v[54:55], v[84:85] op_sel_hi:[1,0]
	v_pk_add_f32 v[32:33], v[32:33], v[32:33] op_sel_hi:[0,1]
	v_pk_mul_f32 v[34:35], v[46:47], v[46:47]
	v_pk_mul_f32 v[36:37], v[48:49], v[48:49]
	v_pk_mul_f32 v[44:45], v[56:57], v[84:85] op_sel_hi:[1,0]
	v_pk_mov_b32 v[38:39], v[36:37], v[34:35] op_sel:[1,0]
	v_mov_b32_e32 v37, v35
	v_pk_mul_f32 v[42:43], v[58:59], v[84:85] op_sel_hi:[1,0]
	v_mul_f32_e32 v32, v44, v44
	v_pk_add_f32 v[34:35], v[38:39], v[36:37]
	v_pk_fma_f32 v[40:41], v[44:45], v[44:45], v[32:33] op_sel_hi:[1,1,0]
	v_mul_f32_e32 v32, v42, v42
	v_pk_add_f32 v[34:35], v[34:35], v[34:35] op_sel_hi:[0,1]
	v_pk_fma_f32 v[52:53], v[42:43], v[42:43], v[32:33] op_sel_hi:[1,1,0]
	v_pk_mul_f32 v[36:37], v[62:63], v[84:85] op_sel_hi:[1,0]
	v_pk_mul_f32 v[38:39], v[60:61], v[84:85] op_sel_hi:[1,0]
	v_mul_f32_e32 v34, v36, v36
	v_mul_f32_e32 v40, v38, v38
	v_mul_f32_e32 v52, v39, v39
	v_mul_f32_e32 v32, v37, v37
	v_pk_add_f32 v[40:41], v[40:41], v[52:53]
	v_pk_add_f32 v[32:33], v[34:35], v[32:33]
	v_lshlrev_b32_e32 v54, 2, v82
	global_load_dwordx4 v[96:99], v54, s[42:43]
	global_load_dwordx4 v[100:103], v54, s[42:43] offset:64
	global_load_dwordx4 v[104:107], v54, s[42:43] offset:128
	global_load_dwordx4 v[108:111], v54, s[42:43] offset:192
	global_load_dwordx4 v[112:115], v54, s[42:43] offset:256
	global_load_dwordx4 v[116:119], v54, s[42:43] offset:320
	global_load_dwordx4 v[120:123], v54, s[42:43] offset:384
	global_load_dwordx4 v[124:127], v54, s[42:43] offset:448
	v_pk_add_f32 v[32:33], v[40:41], v[32:33]
	v_mov_b32_e32 v56, v80
	v_add_f32_e32 v32, v32, v33
	ds_bpermute_b32 v33, v202, v32
	v_mov_b32_e32 v57, v78
	v_mov_b32_e32 v78, v81
	s_waitcnt lgkmcnt(0)
	v_add_f32_e32 v32, v32, v33
	ds_bpermute_b32 v33, v203, v32
	s_waitcnt lgkmcnt(0)
	v_add_f32_e32 v32, v32, v33
	v_fmamk_f32 v32, v32, 0x3c000000, v214
	v_rsq_f32_e32 v40, v32
	v_lshlrev_b64 v[32:33], 12, v[152:153]
	v_lshl_add_u64 v[52:53], s[2:3], 0, v[32:33]
	s_waitcnt vmcnt(0)
; __device__ __forceinline__ unsigned pk2(float lo, float hi) { return f2bf(lo) | (f2bf(hi) << 16); }
; __device__ __forceinline__ void attn_wg_task(const Frame& F, int l, int task) {
;     ...
; #pragma unroll
;         for (int db = 0; db < 8; ++db) {
;             const int d0 = h * HD + db * 16 + rq * 4;
;             const f32x4 g4 = ld_f4(F.attn_g + l * 1024 + d0);
;             u32x2 o; o.x = pk2(O[qb][db][0] * rstd * g4[0], O[qb][db][1] * rstd * g4[1]); o.y = pk2(O[qb][db][2] * rstd * g4[2], O[qb][db][3] * rstd * g4[3]);
;             st_u2(MIX + (size_t)tq * D + d0, o);
	v_mov_b32_e32 v32, v96
	v_mov_b32_e32 v33, v97
	v_mov_b32_e32 v34, v98
	v_mov_b32_e32 v35, v99
	v_pk_mul_f32 v[56:57], v[56:57], v[40:41] op_sel_hi:[1,0]
	v_mov_b32_e32 v58, v32
	v_mov_b32_e32 v59, v34
	v_pk_mul_f32 v[56:57], v[58:59], v[56:57]
	v_pk_mul_f32 v[58:59], v[78:79], v[40:41] op_sel_hi:[1,0]
	v_mov_b32_e32 v34, v33
	v_pk_mul_f32 v[32:33], v[34:35], v[58:59]
	v_and_b32_sdwa v35, v56, v213 dst_sel:DWORD dst_unused:UNUSED_PAD src0_sel:WORD_1 src1_sel:DWORD
	v_add3_u32 v41, v56, v35, s76
	v_and_b32_sdwa v35, v33, v213 dst_sel:DWORD dst_unused:UNUSED_PAD src0_sel:WORD_1 src1_sel:DWORD
	v_and_b32_sdwa v55, v32, v213 dst_sel:DWORD dst_unused:UNUSED_PAD src0_sel:WORD_1 src1_sel:DWORD
	v_and_b32_sdwa v34, v57, v213 dst_sel:DWORD dst_unused:UNUSED_PAD src0_sel:WORD_1 src1_sel:DWORD
	v_add3_u32 v33, v33, v35, s76
	v_add3_u32 v32, v32, v55, s76
	v_add3_u32 v34, v57, v34, s76
	v_and_b32_e32 v33, 0xffff0000, v33
	v_and_b32_e32 v32, 0xffff0000, v32
	v_or_b32_sdwa v35, v33, v34 dst_sel:DWORD dst_unused:UNUSED_PAD src0_sel:DWORD src1_sel:WORD_1
	v_or_b32_sdwa v34, v32, v41 dst_sel:DWORD dst_unused:UNUSED_PAD src0_sel:DWORD src1_sel:WORD_1
	v_lshl_add_u64 v[32:33], v[52:53], 0, v[184:185]
	global_store_dwordx2 v[32:33], v[34:35], off
	v_mov_b32_e32 v56, v100
	v_mov_b32_e32 v57, v101
	v_mov_b32_e32 v58, v102
	v_mov_b32_e32 v59, v103
	v_mov_b32_e32 v34, v76
	v_mov_b32_e32 v35, v74
	v_pk_mul_f32 v[34:35], v[34:35], v[40:41] op_sel_hi:[1,0]
	v_mov_b32_e32 v74, v77
	v_mov_b32_e32 v52, v56
	v_mov_b32_e32 v53, v58
	v_pk_mul_f32 v[34:35], v[52:53], v[34:35]
	v_pk_mul_f32 v[52:53], v[74:75], v[40:41] op_sel_hi:[1,0]
	v_mov_b32_e32 v58, v57
	v_pk_mul_f32 v[52:53], v[58:59], v[52:53]
	v_and_b32_sdwa v41, v35, v213 dst_sel:DWORD dst_unused:UNUSED_PAD src0_sel:WORD_1 src1_sel:DWORD
	v_and_b32_sdwa v55, v34, v213 dst_sel:DWORD dst_unused:UNUSED_PAD src0_sel:WORD_1 src1_sel:DWORD
	v_add3_u32 v34, v34, v55, s76
	v_add3_u32 v35, v35, v41, s76
	v_and_b32_sdwa v41, v53, v213 dst_sel:DWORD dst_unused:UNUSED_PAD src0_sel:WORD_1 src1_sel:DWORD
	v_and_b32_sdwa v55, v52, v213 dst_sel:DWORD dst_unused:UNUSED_PAD src0_sel:WORD_1 src1_sel:DWORD
	v_add3_u32 v41, v53, v41, s76
	v_add3_u32 v52, v52, v55, s76
	v_and_b32_e32 v41, 0xffff0000, v41
	v_and_b32_e32 v52, 0xffff0000, v52
	v_or_b32_sdwa v35, v41, v35 dst_sel:DWORD dst_unused:UNUSED_PAD src0_sel:DWORD src1_sel:WORD_1
	v_or_b32_sdwa v34, v52, v34 dst_sel:DWORD dst_unused:UNUSED_PAD src0_sel:DWORD src1_sel:WORD_1
	global_store_dwordx2 v[32:33], v[34:35], off offset:32
	v_mov_b32_e32 v56, v104
	v_mov_b32_e32 v57, v105
	v_mov_b32_e32 v58, v106
	v_mov_b32_e32 v59, v107
	v_mov_b32_e32 v34, v72
	v_mov_b32_e32 v35, v70
	v_pk_mul_f32 v[34:35], v[34:35], v[40:41] op_sel_hi:[1,0]
	v_mov_b32_e32 v70, v73
	v_mov_b32_e32 v52, v56
	v_mov_b32_e32 v53, v58
	v_pk_mul_f32 v[34:35], v[52:53], v[34:35]
	v_pk_mul_f32 v[52:53], v[70:71], v[40:41] op_sel_hi:[1,0]
	v_mov_b32_e32 v58, v57
	v_pk_mul_f32 v[52:53], v[58:59], v[52:53]
	v_and_b32_sdwa v41, v35, v213 dst_sel:DWORD dst_unused:UNUSED_PAD src0_sel:WORD_1 src1_sel:DWORD
	v_and_b32_sdwa v55, v34, v213 dst_sel:DWORD dst_unused:UNUSED_PAD src0_sel:WORD_1 src1_sel:DWORD
	v_add3_u32 v34, v34, v55, s76
	v_add3_u32 v35, v35, v41, s76
	v_and_b32_sdwa v41, v53, v213 dst_sel:DWORD dst_unused:UNUSED_PAD src0_sel:WORD_1 src1_sel:DWORD
	v_and_b32_sdwa v55, v52, v213 dst_sel:DWORD dst_unused:UNUSED_PAD src0_sel:WORD_1 src1_sel:DWORD
	v_add3_u32 v41, v53, v41, s76
	v_add3_u32 v52, v52, v55, s76
	v_and_b32_e32 v41, 0xffff0000, v41
	v_and_b32_e32 v52, 0xffff0000, v52
	v_or_b32_sdwa v35, v41, v35 dst_sel:DWORD dst_unused:UNUSED_PAD src0_sel:DWORD src1_sel:WORD_1
	v_or_b32_sdwa v34, v52, v34 dst_sel:DWORD dst_unused:UNUSED_PAD src0_sel:DWORD src1_sel:WORD_1
	global_store_dwordx2 v[32:33], v[34:35], off offset:64
	v_mov_b32_e32 v56, v108
	v_mov_b32_e32 v57, v109
	v_mov_b32_e32 v58, v110
	v_mov_b32_e32 v59, v111
	v_mov_b32_e32 v34, v68
	v_mov_b32_e32 v35, v66
	v_pk_mul_f32 v[34:35], v[34:35], v[40:41] op_sel_hi:[1,0]
	v_mov_b32_e32 v66, v69
	v_mov_b32_e32 v52, v56
	v_mov_b32_e32 v53, v58
	v_pk_mul_f32 v[34:35], v[52:53], v[34:35]
	v_pk_mul_f32 v[52:53], v[66:67], v[40:41] op_sel_hi:[1,0]
	v_mov_b32_e32 v58, v57
	v_pk_mul_f32 v[52:53], v[58:59], v[52:53]
	v_and_b32_sdwa v41, v35, v213 dst_sel:DWORD dst_unused:UNUSED_PAD src0_sel:WORD_1 src1_sel:DWORD
	v_and_b32_sdwa v55, v34, v213 dst_sel:DWORD dst_unused:UNUSED_PAD src0_sel:WORD_1 src1_sel:DWORD
	v_add3_u32 v34, v34, v55, s76
	v_add3_u32 v35, v35, v41, s76
	v_and_b32_sdwa v41, v53, v213 dst_sel:DWORD dst_unused:UNUSED_PAD src0_sel:WORD_1 src1_sel:DWORD
	v_and_b32_sdwa v55, v52, v213 dst_sel:DWORD dst_unused:UNUSED_PAD src0_sel:WORD_1 src1_sel:DWORD
	v_add3_u32 v41, v53, v41, s76
	v_add3_u32 v52, v52, v55, s76
	v_and_b32_e32 v41, 0xffff0000, v41
	v_and_b32_e32 v52, 0xffff0000, v52
	v_or_b32_sdwa v35, v41, v35 dst_sel:DWORD dst_unused:UNUSED_PAD src0_sel:DWORD src1_sel:WORD_1
	v_or_b32_sdwa v34, v52, v34 dst_sel:DWORD dst_unused:UNUSED_PAD src0_sel:DWORD src1_sel:WORD_1
	global_store_dwordx2 v[32:33], v[34:35], off offset:96
	v_mov_b32_e32 v56, v112
	v_mov_b32_e32 v57, v113
	v_mov_b32_e32 v58, v114
	v_mov_b32_e32 v59, v115
	v_mov_b32_e32 v34, v64
	v_mov_b32_e32 v35, v50
	v_pk_mul_f32 v[34:35], v[34:35], v[40:41] op_sel_hi:[1,0]
	v_mov_b32_e32 v50, v65
	v_pk_mul_f32 v[50:51], v[50:51], v[40:41] op_sel_hi:[1,0]
	v_mov_b32_e32 v52, v56
	v_mov_b32_e32 v53, v58
	v_pk_mul_f32 v[34:35], v[52:53], v[34:35]
	v_mov_b32_e32 v58, v57
	v_pk_mul_f32 v[50:51], v[58:59], v[50:51]
	v_and_b32_sdwa v41, v35, v213 dst_sel:DWORD dst_unused:UNUSED_PAD src0_sel:WORD_1 src1_sel:DWORD
; __device__ __forceinline__ unsigned pk2(float lo, float hi) { return f2bf(lo) | (f2bf(hi) << 16); }
; __device__ __forceinline__ void attn_wg_task(const Frame& F, int l, int task) {
;     ...
; #pragma unroll
;         for (int db = 0; db < 8; ++db) {
;             const int d0 = h * HD + db * 16 + rq * 4;
;             const f32x4 g4 = ld_f4(F.attn_g + l * 1024 + d0);
;             u32x2 o; o.x = pk2(O[qb][db][0] * rstd * g4[0], O[qb][db][1] * rstd * g4[1]); o.y = pk2(O[qb][db][2] * rstd * g4[2], O[qb][db][3] * rstd * g4[3]);
;             st_u2(MIX + (size_t)tq * D + d0, o);
	v_and_b32_sdwa v52, v34, v213 dst_sel:DWORD dst_unused:UNUSED_PAD src0_sel:WORD_1 src1_sel:DWORD
	v_add3_u32 v34, v34, v52, s76
	v_add3_u32 v35, v35, v41, s76
	v_and_b32_sdwa v41, v51, v213 dst_sel:DWORD dst_unused:UNUSED_PAD src0_sel:WORD_1 src1_sel:DWORD
	v_and_b32_sdwa v52, v50, v213 dst_sel:DWORD dst_unused:UNUSED_PAD src0_sel:WORD_1 src1_sel:DWORD
	v_add3_u32 v41, v51, v41, s76
	v_add3_u32 v50, v50, v52, s76
	v_and_b32_e32 v41, 0xffff0000, v41
	v_and_b32_e32 v50, 0xffff0000, v50
	v_or_b32_sdwa v35, v41, v35 dst_sel:DWORD dst_unused:UNUSED_PAD src0_sel:DWORD src1_sel:WORD_1
	v_or_b32_sdwa v34, v50, v34 dst_sel:DWORD dst_unused:UNUSED_PAD src0_sel:DWORD src1_sel:WORD_1
	global_store_dwordx2 v[32:33], v[34:35], off offset:128
	v_mov_b32_e32 v50, v116
	v_mov_b32_e32 v51, v117
	v_mov_b32_e32 v52, v118
	v_mov_b32_e32 v53, v119
	v_mov_b32_e32 v34, v48
	v_mov_b32_e32 v35, v46
	v_pk_mul_f32 v[34:35], v[34:35], v[40:41] op_sel_hi:[1,0]
	v_mov_b32_e32 v46, v49
	v_pk_mul_f32 v[46:47], v[46:47], v[40:41] op_sel_hi:[1,0]
	v_mov_b32_e32 v56, v50
	v_mov_b32_e32 v57, v52
	v_pk_mul_f32 v[34:35], v[56:57], v[34:35]
	v_mov_b32_e32 v52, v51
	v_pk_mul_f32 v[46:47], v[52:53], v[46:47]
	v_and_b32_sdwa v41, v35, v213 dst_sel:DWORD dst_unused:UNUSED_PAD src0_sel:WORD_1 src1_sel:DWORD
	v_and_b32_sdwa v48, v34, v213 dst_sel:DWORD dst_unused:UNUSED_PAD src0_sel:WORD_1 src1_sel:DWORD
	v_add3_u32 v34, v34, v48, s76
	v_add3_u32 v35, v35, v41, s76
	v_and_b32_sdwa v41, v47, v213 dst_sel:DWORD dst_unused:UNUSED_PAD src0_sel:WORD_1 src1_sel:DWORD
	v_and_b32_sdwa v48, v46, v213 dst_sel:DWORD dst_unused:UNUSED_PAD src0_sel:WORD_1 src1_sel:DWORD
	v_add3_u32 v41, v47, v41, s76
	v_add3_u32 v46, v46, v48, s76
	v_and_b32_e32 v41, 0xffff0000, v41
	v_and_b32_e32 v46, 0xffff0000, v46
	v_or_b32_sdwa v35, v41, v35 dst_sel:DWORD dst_unused:UNUSED_PAD src0_sel:DWORD src1_sel:WORD_1
	v_or_b32_sdwa v34, v46, v34 dst_sel:DWORD dst_unused:UNUSED_PAD src0_sel:DWORD src1_sel:WORD_1
	global_store_dwordx2 v[32:33], v[34:35], off offset:160
	v_mov_b32_e32 v46, v120
	v_mov_b32_e32 v47, v121
	v_mov_b32_e32 v48, v122
	v_mov_b32_e32 v49, v123
	v_mov_b32_e32 v34, v44
	v_mov_b32_e32 v35, v42
	v_pk_mul_f32 v[34:35], v[34:35], v[40:41] op_sel_hi:[1,0]
	v_mov_b32_e32 v42, v45
	v_pk_mul_f32 v[42:43], v[42:43], v[40:41] op_sel_hi:[1,0]
	v_mov_b32_e32 v50, v46
	v_mov_b32_e32 v51, v48
	v_pk_mul_f32 v[34:35], v[50:51], v[34:35]
	v_mov_b32_e32 v48, v47
	v_pk_mul_f32 v[42:43], v[48:49], v[42:43]
	v_and_b32_sdwa v41, v35, v213 dst_sel:DWORD dst_unused:UNUSED_PAD src0_sel:WORD_1 src1_sel:DWORD
	v_and_b32_sdwa v44, v34, v213 dst_sel:DWORD dst_unused:UNUSED_PAD src0_sel:WORD_1 src1_sel:DWORD
	v_add3_u32 v34, v34, v44, s76
	v_add3_u32 v35, v35, v41, s76
	v_and_b32_sdwa v41, v43, v213 dst_sel:DWORD dst_unused:UNUSED_PAD src0_sel:WORD_1 src1_sel:DWORD
	v_and_b32_sdwa v44, v42, v213 dst_sel:DWORD dst_unused:UNUSED_PAD src0_sel:WORD_1 src1_sel:DWORD
	v_add3_u32 v41, v43, v41, s76
	v_add3_u32 v42, v42, v44, s76
	v_and_b32_e32 v41, 0xffff0000, v41
	v_and_b32_e32 v42, 0xffff0000, v42
	v_or_b32_sdwa v35, v41, v35 dst_sel:DWORD dst_unused:UNUSED_PAD src0_sel:DWORD src1_sel:WORD_1
	v_or_b32_sdwa v34, v42, v34 dst_sel:DWORD dst_unused:UNUSED_PAD src0_sel:DWORD src1_sel:WORD_1
	global_store_dwordx2 v[32:33], v[34:35], off offset:192
	v_mov_b32_e32 v42, v124
	v_mov_b32_e32 v43, v125
	v_mov_b32_e32 v44, v126
	v_mov_b32_e32 v45, v127
	v_mov_b32_e32 v34, v38
	v_mov_b32_e32 v35, v36
	v_pk_mul_f32 v[34:35], v[34:35], v[40:41] op_sel_hi:[1,0]
	v_mov_b32_e32 v36, v39
	v_pk_mul_f32 v[36:37], v[36:37], v[40:41] op_sel_hi:[1,0]
	v_mov_b32_e32 v46, v42
	v_mov_b32_e32 v47, v44
	v_pk_mul_f32 v[34:35], v[46:47], v[34:35]
	v_mov_b32_e32 v44, v43
	v_pk_mul_f32 v[36:37], v[44:45], v[36:37]
	v_and_b32_sdwa v38, v35, v213 dst_sel:DWORD dst_unused:UNUSED_PAD src0_sel:WORD_1 src1_sel:DWORD
	v_and_b32_sdwa v39, v34, v213 dst_sel:DWORD dst_unused:UNUSED_PAD src0_sel:WORD_1 src1_sel:DWORD
	v_add3_u32 v34, v34, v39, s76
	v_add3_u32 v35, v35, v38, s76
	v_and_b32_sdwa v38, v37, v213 dst_sel:DWORD dst_unused:UNUSED_PAD src0_sel:WORD_1 src1_sel:DWORD
	v_and_b32_sdwa v39, v36, v213 dst_sel:DWORD dst_unused:UNUSED_PAD src0_sel:WORD_1 src1_sel:DWORD
	v_add3_u32 v37, v37, v38, s76
	v_add3_u32 v36, v36, v39, s76
	v_and_b32_e32 v37, 0xffff0000, v37
	v_and_b32_e32 v36, 0xffff0000, v36
	v_or_b32_sdwa v35, v37, v35 dst_sel:DWORD dst_unused:UNUSED_PAD src0_sel:DWORD src1_sel:WORD_1
	v_or_b32_sdwa v34, v36, v34 dst_sel:DWORD dst_unused:UNUSED_PAD src0_sel:DWORD src1_sel:WORD_1
	global_store_dwordx2 v[32:33], v[34:35], off offset:224
	ds_bpermute_b32 v32, v202, v150
	s_waitcnt lgkmcnt(0)
	v_add_f32_e32 v32, v150, v32
	ds_bpermute_b32 v33, v203, v32
	s_waitcnt lgkmcnt(0)
; __device__ __forceinline__ unsigned pk2(float lo, float hi) { return f2bf(lo) | (f2bf(hi) << 16); }
; __device__ __forceinline__ float rq_sum(float v) { v += __shfl_xor(v, 16); v += __shfl_xor(v, 32); return v; }
; __device__ __forceinline__ float frsq(float x) { return __builtin_amdgcn_rsqf(x); }
; __device__ __forceinline__ void attn_wg_task(const Frame& F, int l, int task) {
;     ...
;     for (int qb = 0; qb < 2; ++qb) {
;         const int tq = tq0 + qb * 16;
;         const float inv = 1.0f / rq_sum(l_run[qb]);
;         float ss = 0.f;
; #pragma unroll
;         for (int db = 0; db < 8; ++db) { O[qb][db] *= inv; ss += (O[qb][db][0] * O[qb][db][0] + O[qb][db][1] * O[qb][db][1]) + (O[qb][db][2] * O[qb][db][2] + O[qb][db][3] * O[qb][db][3]); }
;         const float rstd = frsq(rq_sum(ss) * (1.f / HD) + EPS);
; #pragma unroll
;         for (int db = 0; db < 8; ++db) {
;             const int d0 = h * HD + db * 16 + rq * 4;
;             const f32x4 g4 = ld_f4(F.attn_g + l * 1024 + d0);
;             u32x2 o; o.x = pk2(O[qb][db][0] * rstd * g4[0], O[qb][db][1] * rstd * g4[1]); o.y = pk2(O[qb][db][2] * rstd * g4[2], O[qb][db][3] * rstd * g4[3]);
;             st_u2(MIX + (size_t)tq * D + d0, o);
	v_add_f32_e32 v32, v32, v33
	v_div_scale_f32 v33, s[0:1], v32, v32, 1.0
	v_rcp_f32_e32 v34, v33
	s_nop 0
	v_fma_f32 v35, -v33, v34, 1.0
	v_fmac_f32_e32 v34, v35, v34
	v_div_scale_f32 v35, vcc, 1.0, v32, 1.0
	v_mul_f32_e32 v36, v35, v34
	v_fma_f32 v37, -v33, v36, v35
	v_fmac_f32_e32 v36, v37, v34
	v_fma_f32 v33, -v33, v36, v35
	v_div_fmas_f32 v33, v33, v34, v36
	v_div_fixup_f32 v48, v33, v32, 1.0
	v_pk_mul_f32 v[46:47], v[4:5], v[48:49] op_sel_hi:[1,0]
	v_pk_mul_f32 v[42:43], v[8:9], v[48:49] op_sel_hi:[1,0]
	v_pk_mul_f32 v[44:45], v[6:7], v[48:49] op_sel_hi:[1,0]
	v_pk_mul_f32 v[36:37], v[10:11], v[48:49] op_sel_hi:[1,0]
	v_mov_b32_e32 v6, v47
	v_mov_b32_e32 v7, v43
	v_mov_b32_e32 v4, v46
	v_mov_b32_e32 v5, v42
	v_pk_mul_f32 v[6:7], v[6:7], v[6:7]
	v_mov_b32_e32 v8, v45
	v_mov_b32_e32 v9, v37
	v_pk_fma_f32 v[4:5], v[4:5], v[4:5], v[6:7]
	v_mov_b32_e32 v6, v44
	v_mov_b32_e32 v7, v36
	v_pk_mul_f32 v[8:9], v[8:9], v[8:9]
	v_pk_mul_f32 v[40:41], v[0:1], v[48:49] op_sel_hi:[1,0]
	v_pk_mul_f32 v[38:39], v[2:3], v[48:49] op_sel_hi:[1,0]
	v_pk_fma_f32 v[6:7], v[6:7], v[6:7], v[8:9]
	v_pk_mul_f32 v[0:1], v[38:39], v[38:39]
	v_pk_mul_f32 v[2:3], v[40:41], v[40:41]
	v_pk_add_f32 v[4:5], v[4:5], v[6:7]
	v_pk_mov_b32 v[6:7], v[2:3], v[0:1] op_sel:[1,0]
	v_mov_b32_e32 v3, v1
	v_pk_add_f32 v[0:1], v[6:7], v[2:3]
	v_pk_mul_f32 v[34:35], v[12:13], v[48:49] op_sel_hi:[1,0]
	v_pk_add_f32 v[0:1], v[0:1], v[0:1] op_sel_hi:[0,1]
	v_pk_mul_f32 v[32:33], v[14:15], v[48:49] op_sel_hi:[1,0]
	v_mul_f32_e32 v0, v34, v34
	v_pk_fma_f32 v[2:3], v[34:35], v[34:35], v[0:1] op_sel_hi:[1,1,0]
	v_mul_f32_e32 v0, v32, v32
	v_pk_add_f32 v[4:5], v[4:5], v[4:5] op_sel_hi:[0,1]
	v_pk_fma_f32 v[6:7], v[32:33], v[32:33], v[0:1] op_sel_hi:[1,1,0]
	v_pk_mul_f32 v[14:15], v[18:19], v[48:49] op_sel_hi:[1,0]
	v_pk_mul_f32 v[16:17], v[16:17], v[48:49] op_sel_hi:[1,0]
	v_mul_f32_e32 v0, v14, v14
	v_mul_f32_e32 v2, v16, v16
	v_mul_f32_e32 v6, v17, v17
	v_mul_f32_e32 v4, v15, v15
	v_pk_add_f32 v[2:3], v[2:3], v[6:7]
	v_pk_add_f32 v[0:1], v[0:1], v[4:5]
	v_pk_mul_f32 v[12:13], v[20:21], v[48:49] op_sel_hi:[1,0]
	v_pk_add_f32 v[0:1], v[2:3], v[0:1]
	v_pk_mul_f32 v[10:11], v[22:23], v[48:49] op_sel_hi:[1,0]
	v_pk_add_f32 v[4:5], v[0:1], v[0:1] op_sel_hi:[0,1]
	v_pk_mul_f32 v[0:1], v[10:11], v[10:11]
	v_pk_mul_f32 v[2:3], v[12:13], v[12:13]
	v_pk_mul_f32 v[8:9], v[24:25], v[48:49] op_sel_hi:[1,0]
	v_pk_mov_b32 v[6:7], v[2:3], v[0:1] op_sel:[1,0]
	v_mov_b32_e32 v3, v1
	v_pk_add_f32 v[0:1], v[6:7], v[2:3]
	v_pk_mul_f32 v[6:7], v[26:27], v[48:49] op_sel_hi:[1,0]
	v_pk_add_f32 v[18:19], v[0:1], v[0:1] op_sel_hi:[0,1]
	v_mul_f32_e32 v0, v8, v8
	v_pk_fma_f32 v[20:21], v[8:9], v[8:9], v[0:1] op_sel_hi:[1,1,0]
	v_mul_f32_e32 v0, v6, v6
	v_pk_fma_f32 v[22:23], v[6:7], v[6:7], v[0:1] op_sel_hi:[1,1,0]
	v_pk_mul_f32 v[0:1], v[30:31], v[48:49] op_sel_hi:[1,0]
	v_pk_mul_f32 v[2:3], v[28:29], v[48:49] op_sel_hi:[1,0]
	v_mul_f32_e32 v18, v0, v0
	v_mul_f32_e32 v20, v2, v2
	v_mul_f32_e32 v22, v3, v3
	v_mul_f32_e32 v4, v1, v1
	v_pk_add_f32 v[20:21], v[20:21], v[22:23]
	v_pk_add_f32 v[4:5], v[18:19], v[4:5]
	v_mov_b32_e32 v24, v46
	v_pk_add_f32 v[4:5], v[20:21], v[4:5]
	v_mov_b32_e32 v20, v96
	v_mov_b32_e32 v21, v97
	v_mov_b32_e32 v22, v98
	v_mov_b32_e32 v23, v99
	v_add_f32_e32 v4, v4, v5
	ds_bpermute_b32 v5, v202, v4
	v_mov_b32_e32 v25, v44
	v_mov_b32_e32 v44, v47
	v_lshlrev_b64 v[18:19], 12, v[148:149]
	v_lshl_add_u64 v[18:19], s[2:3], 0, v[18:19]
	s_waitcnt lgkmcnt(0)
	v_add_f32_e32 v4, v4, v5
	ds_bpermute_b32 v5, v203, v4
	v_lshl_add_u64 v[18:19], v[18:19], 0, v[184:185]
	s_add_i32 s2, s16, 1
	s_cmp_lt_u32 s16, 2
	s_cselect_b64 s[0:1], -1, 0
	s_waitcnt lgkmcnt(0)
	v_add_f32_e32 v4, v4, v5
	v_fmamk_f32 v4, v4, 0x3c000000, v214
	v_rsq_f32_e32 v4, v4
	s_and_b64 s[0:1], s[4:5], s[0:1]
	s_andn2_b64 vcc, exec, s[0:1]
	s_mov_b32 s16, s2
	v_pk_mul_f32 v[24:25], v[24:25], v[4:5] op_sel_hi:[1,0]
	v_mov_b32_e32 v26, v20
	v_mov_b32_e32 v27, v22
	v_pk_mul_f32 v[24:25], v[26:27], v[24:25]
	v_pk_mul_f32 v[26:27], v[44:45], v[4:5] op_sel_hi:[1,0]
	v_mov_b32_e32 v22, v21
	v_pk_mul_f32 v[20:21], v[22:23], v[26:27]
	v_and_b32_sdwa v22, v24, v213 dst_sel:DWORD dst_unused:UNUSED_PAD src0_sel:WORD_1 src1_sel:DWORD
	v_add3_u32 v22, v24, v22, s76
	v_and_b32_sdwa v23, v21, v213 dst_sel:DWORD dst_unused:UNUSED_PAD src0_sel:WORD_1 src1_sel:DWORD
	v_and_b32_sdwa v24, v20, v213 dst_sel:DWORD dst_unused:UNUSED_PAD src0_sel:WORD_1 src1_sel:DWORD
	v_and_b32_sdwa v5, v25, v213 dst_sel:DWORD dst_unused:UNUSED_PAD src0_sel:WORD_1 src1_sel:DWORD
	v_add3_u32 v21, v21, v23, s76
	v_add3_u32 v20, v20, v24, s76
	v_add3_u32 v5, v25, v5, s76
	v_and_b32_e32 v21, 0xffff0000, v21
	v_and_b32_e32 v20, 0xffff0000, v20
	v_or_b32_sdwa v21, v21, v5 dst_sel:DWORD dst_unused:UNUSED_PAD src0_sel:DWORD src1_sel:WORD_1
	v_or_b32_sdwa v20, v20, v22 dst_sel:DWORD dst_unused:UNUSED_PAD src0_sel:DWORD src1_sel:WORD_1
	global_store_dwordx2 v[18:19], v[20:21], off
	v_mov_b32_e32 v20, v100
	v_mov_b32_e32 v21, v101
	v_mov_b32_e32 v22, v102
	v_mov_b32_e32 v23, v103
	v_mov_b32_e32 v24, v42
	v_mov_b32_e32 v25, v36
	v_pk_mul_f32 v[24:25], v[24:25], v[4:5] op_sel_hi:[1,0]
	v_mov_b32_e32 v36, v43
	v_mov_b32_e32 v26, v20
	v_mov_b32_e32 v27, v22
	v_pk_mul_f32 v[24:25], v[26:27], v[24:25]
	v_pk_mul_f32 v[26:27], v[36:37], v[4:5] op_sel_hi:[1,0]
	v_mov_b32_e32 v22, v21
	v_pk_mul_f32 v[20:21], v[22:23], v[26:27]
	v_and_b32_sdwa v22, v24, v213 dst_sel:DWORD dst_unused:UNUSED_PAD src0_sel:WORD_1 src1_sel:DWORD
	v_add3_u32 v22, v24, v22, s76
	v_and_b32_sdwa v23, v21, v213 dst_sel:DWORD dst_unused:UNUSED_PAD src0_sel:WORD_1 src1_sel:DWORD
; __device__ __forceinline__ unsigned pk2(float lo, float hi) { return f2bf(lo) | (f2bf(hi) << 16); }
; __device__ __forceinline__ void attn_wg_task(const Frame& F, int l, int task) {
;     ...
; #pragma unroll
;         for (int db = 0; db < 8; ++db) {
;             const int d0 = h * HD + db * 16 + rq * 4;
;             const f32x4 g4 = ld_f4(F.attn_g + l * 1024 + d0);
;             u32x2 o; o.x = pk2(O[qb][db][0] * rstd * g4[0], O[qb][db][1] * rstd * g4[1]); o.y = pk2(O[qb][db][2] * rstd * g4[2], O[qb][db][3] * rstd * g4[3]);
;             st_u2(MIX + (size_t)tq * D + d0, o);
	v_and_b32_sdwa v24, v20, v213 dst_sel:DWORD dst_unused:UNUSED_PAD src0_sel:WORD_1 src1_sel:DWORD
	v_and_b32_sdwa v5, v25, v213 dst_sel:DWORD dst_unused:UNUSED_PAD src0_sel:WORD_1 src1_sel:DWORD
	v_add3_u32 v21, v21, v23, s76
	v_add3_u32 v20, v20, v24, s76
	v_add3_u32 v5, v25, v5, s76
	v_and_b32_e32 v21, 0xffff0000, v21
	v_and_b32_e32 v20, 0xffff0000, v20
	v_or_b32_sdwa v21, v21, v5 dst_sel:DWORD dst_unused:UNUSED_PAD src0_sel:DWORD src1_sel:WORD_1
	v_or_b32_sdwa v20, v20, v22 dst_sel:DWORD dst_unused:UNUSED_PAD src0_sel:DWORD src1_sel:WORD_1
	global_store_dwordx2 v[18:19], v[20:21], off offset:32
	v_mov_b32_e32 v20, v104
	v_mov_b32_e32 v21, v105
	v_mov_b32_e32 v22, v106
	v_mov_b32_e32 v23, v107
	v_mov_b32_e32 v24, v40
	v_mov_b32_e32 v25, v38
	v_pk_mul_f32 v[24:25], v[24:25], v[4:5] op_sel_hi:[1,0]
	v_mov_b32_e32 v38, v41
	v_mov_b32_e32 v26, v20
	v_mov_b32_e32 v27, v22
	v_pk_mul_f32 v[24:25], v[26:27], v[24:25]
	v_pk_mul_f32 v[26:27], v[38:39], v[4:5] op_sel_hi:[1,0]
	v_mov_b32_e32 v22, v21
	v_pk_mul_f32 v[20:21], v[22:23], v[26:27]
	v_and_b32_sdwa v22, v24, v213 dst_sel:DWORD dst_unused:UNUSED_PAD src0_sel:WORD_1 src1_sel:DWORD
	v_add3_u32 v22, v24, v22, s76
	v_and_b32_sdwa v23, v21, v213 dst_sel:DWORD dst_unused:UNUSED_PAD src0_sel:WORD_1 src1_sel:DWORD
	v_and_b32_sdwa v24, v20, v213 dst_sel:DWORD dst_unused:UNUSED_PAD src0_sel:WORD_1 src1_sel:DWORD
	v_and_b32_sdwa v5, v25, v213 dst_sel:DWORD dst_unused:UNUSED_PAD src0_sel:WORD_1 src1_sel:DWORD
	v_add3_u32 v21, v21, v23, s76
	v_add3_u32 v20, v20, v24, s76
	v_add3_u32 v5, v25, v5, s76
	v_and_b32_e32 v21, 0xffff0000, v21
	v_and_b32_e32 v20, 0xffff0000, v20
	v_or_b32_sdwa v21, v21, v5 dst_sel:DWORD dst_unused:UNUSED_PAD src0_sel:DWORD src1_sel:WORD_1
	v_or_b32_sdwa v20, v20, v22 dst_sel:DWORD dst_unused:UNUSED_PAD src0_sel:DWORD src1_sel:WORD_1
	global_store_dwordx2 v[18:19], v[20:21], off offset:64
	v_mov_b32_e32 v20, v108
	v_mov_b32_e32 v21, v109
	v_mov_b32_e32 v22, v110
	v_mov_b32_e32 v23, v111
	v_mov_b32_e32 v24, v34
	v_mov_b32_e32 v25, v32
	v_pk_mul_f32 v[24:25], v[24:25], v[4:5] op_sel_hi:[1,0]
	v_mov_b32_e32 v32, v35
	v_mov_b32_e32 v26, v20
	v_mov_b32_e32 v27, v22
	v_pk_mul_f32 v[24:25], v[26:27], v[24:25]
	v_pk_mul_f32 v[26:27], v[32:33], v[4:5] op_sel_hi:[1,0]
	v_mov_b32_e32 v22, v21
	v_pk_mul_f32 v[20:21], v[22:23], v[26:27]
	v_and_b32_sdwa v22, v24, v213 dst_sel:DWORD dst_unused:UNUSED_PAD src0_sel:WORD_1 src1_sel:DWORD
	v_add3_u32 v22, v24, v22, s76
	v_and_b32_sdwa v23, v21, v213 dst_sel:DWORD dst_unused:UNUSED_PAD src0_sel:WORD_1 src1_sel:DWORD
	v_and_b32_sdwa v24, v20, v213 dst_sel:DWORD dst_unused:UNUSED_PAD src0_sel:WORD_1 src1_sel:DWORD
	v_and_b32_sdwa v5, v25, v213 dst_sel:DWORD dst_unused:UNUSED_PAD src0_sel:WORD_1 src1_sel:DWORD
	v_add3_u32 v21, v21, v23, s76
	v_add3_u32 v20, v20, v24, s76
	v_add3_u32 v5, v25, v5, s76
	v_and_b32_e32 v21, 0xffff0000, v21
	v_and_b32_e32 v20, 0xffff0000, v20
	v_or_b32_sdwa v21, v21, v5 dst_sel:DWORD dst_unused:UNUSED_PAD src0_sel:DWORD src1_sel:WORD_1
	v_or_b32_sdwa v20, v20, v22 dst_sel:DWORD dst_unused:UNUSED_PAD src0_sel:DWORD src1_sel:WORD_1
	global_store_dwordx2 v[18:19], v[20:21], off offset:96
	v_mov_b32_e32 v20, v112
	v_mov_b32_e32 v21, v113
	v_mov_b32_e32 v22, v114
	v_mov_b32_e32 v23, v115
	v_mov_b32_e32 v25, v14
	v_mov_b32_e32 v14, v17
	v_mov_b32_e32 v24, v16
	v_pk_mul_f32 v[14:15], v[14:15], v[4:5] op_sel_hi:[1,0]
	v_pk_mul_f32 v[24:25], v[24:25], v[4:5] op_sel_hi:[1,0]
	v_mov_b32_e32 v27, v22
	v_mov_b32_e32 v22, v21
	v_mov_b32_e32 v26, v20
	v_pk_mul_f32 v[14:15], v[22:23], v[14:15]
	v_pk_mul_f32 v[24:25], v[26:27], v[24:25]
	v_and_b32_sdwa v17, v15, v213 dst_sel:DWORD dst_unused:UNUSED_PAD src0_sel:WORD_1 src1_sel:DWORD
	v_and_b32_sdwa v20, v14, v213 dst_sel:DWORD dst_unused:UNUSED_PAD src0_sel:WORD_1 src1_sel:DWORD
	v_and_b32_sdwa v5, v25, v213 dst_sel:DWORD dst_unused:UNUSED_PAD src0_sel:WORD_1 src1_sel:DWORD
	v_and_b32_sdwa v16, v24, v213 dst_sel:DWORD dst_unused:UNUSED_PAD src0_sel:WORD_1 src1_sel:DWORD
	v_add3_u32 v15, v15, v17, s76
	v_add3_u32 v14, v14, v20, s76
	v_add3_u32 v16, v24, v16, s76
	v_add3_u32 v5, v25, v5, s76
; __device__ __forceinline__ unsigned pk2(float lo, float hi) { return f2bf(lo) | (f2bf(hi) << 16); }
; __device__ __forceinline__ void attn_wg_task(const Frame& F, int l, int task) {
;     ...
; #pragma unroll
;         for (int db = 0; db < 8; ++db) {
;             const int d0 = h * HD + db * 16 + rq * 4;
;             const f32x4 g4 = ld_f4(F.attn_g + l * 1024 + d0);
;             u32x2 o; o.x = pk2(O[qb][db][0] * rstd * g4[0], O[qb][db][1] * rstd * g4[1]); o.y = pk2(O[qb][db][2] * rstd * g4[2], O[qb][db][3] * rstd * g4[3]);
;             st_u2(MIX + (size_t)tq * D + d0, o);
	v_and_b32_e32 v15, 0xffff0000, v15
	v_and_b32_e32 v14, 0xffff0000, v14
	v_or_b32_sdwa v15, v15, v5 dst_sel:DWORD dst_unused:UNUSED_PAD src0_sel:DWORD src1_sel:WORD_1
	v_or_b32_sdwa v14, v14, v16 dst_sel:DWORD dst_unused:UNUSED_PAD src0_sel:DWORD src1_sel:WORD_1
	global_store_dwordx2 v[18:19], v[14:15], off offset:128
	v_mov_b32_e32 v14, v116
	v_mov_b32_e32 v15, v117
	v_mov_b32_e32 v16, v118
	v_mov_b32_e32 v17, v119
	v_mov_b32_e32 v21, v10
	v_mov_b32_e32 v10, v13
	v_mov_b32_e32 v20, v12
	v_pk_mul_f32 v[10:11], v[10:11], v[4:5] op_sel_hi:[1,0]
	v_pk_mul_f32 v[20:21], v[20:21], v[4:5] op_sel_hi:[1,0]
	v_mov_b32_e32 v23, v16
	v_mov_b32_e32 v16, v15
	v_mov_b32_e32 v22, v14
	v_pk_mul_f32 v[10:11], v[16:17], v[10:11]
	v_pk_mul_f32 v[20:21], v[22:23], v[20:21]
	v_and_b32_sdwa v13, v11, v213 dst_sel:DWORD dst_unused:UNUSED_PAD src0_sel:WORD_1 src1_sel:DWORD
	v_and_b32_sdwa v14, v10, v213 dst_sel:DWORD dst_unused:UNUSED_PAD src0_sel:WORD_1 src1_sel:DWORD
	v_and_b32_sdwa v5, v21, v213 dst_sel:DWORD dst_unused:UNUSED_PAD src0_sel:WORD_1 src1_sel:DWORD
	v_and_b32_sdwa v12, v20, v213 dst_sel:DWORD dst_unused:UNUSED_PAD src0_sel:WORD_1 src1_sel:DWORD
	v_add3_u32 v11, v11, v13, s76
	v_add3_u32 v10, v10, v14, s76
	v_add3_u32 v12, v20, v12, s76
	v_add3_u32 v5, v21, v5, s76
	v_and_b32_e32 v11, 0xffff0000, v11
	v_and_b32_e32 v10, 0xffff0000, v10
	v_or_b32_sdwa v11, v11, v5 dst_sel:DWORD dst_unused:UNUSED_PAD src0_sel:DWORD src1_sel:WORD_1
	v_or_b32_sdwa v10, v10, v12 dst_sel:DWORD dst_unused:UNUSED_PAD src0_sel:DWORD src1_sel:WORD_1
	global_store_dwordx2 v[18:19], v[10:11], off offset:160
	v_mov_b32_e32 v10, v120
	v_mov_b32_e32 v11, v121
	v_mov_b32_e32 v12, v122
	v_mov_b32_e32 v13, v123
	v_mov_b32_e32 v15, v6
	v_mov_b32_e32 v6, v9
	v_mov_b32_e32 v14, v8
	v_pk_mul_f32 v[6:7], v[6:7], v[4:5] op_sel_hi:[1,0]
	v_pk_mul_f32 v[14:15], v[14:15], v[4:5] op_sel_hi:[1,0]
	v_mov_b32_e32 v17, v12
	v_mov_b32_e32 v12, v11
	v_mov_b32_e32 v16, v10
	v_pk_mul_f32 v[6:7], v[12:13], v[6:7]
	v_pk_mul_f32 v[14:15], v[16:17], v[14:15]
	v_and_b32_sdwa v9, v7, v213 dst_sel:DWORD dst_unused:UNUSED_PAD src0_sel:WORD_1 src1_sel:DWORD
	v_and_b32_sdwa v10, v6, v213 dst_sel:DWORD dst_unused:UNUSED_PAD src0_sel:WORD_1 src1_sel:DWORD
	v_and_b32_sdwa v5, v15, v213 dst_sel:DWORD dst_unused:UNUSED_PAD src0_sel:WORD_1 src1_sel:DWORD
	v_and_b32_sdwa v8, v14, v213 dst_sel:DWORD dst_unused:UNUSED_PAD src0_sel:WORD_1 src1_sel:DWORD
	v_add3_u32 v7, v7, v9, s76
	v_add3_u32 v6, v6, v10, s76
	v_add3_u32 v8, v14, v8, s76
	v_add3_u32 v5, v15, v5, s76
	v_and_b32_e32 v7, 0xffff0000, v7
	v_and_b32_e32 v6, 0xffff0000, v6
	v_or_b32_sdwa v7, v7, v5 dst_sel:DWORD dst_unused:UNUSED_PAD src0_sel:DWORD src1_sel:WORD_1
	v_or_b32_sdwa v6, v6, v8 dst_sel:DWORD dst_unused:UNUSED_PAD src0_sel:DWORD src1_sel:WORD_1
	global_store_dwordx2 v[18:19], v[6:7], off offset:192
	v_mov_b32_e32 v6, v124
	v_mov_b32_e32 v7, v125
	v_mov_b32_e32 v8, v126
	v_mov_b32_e32 v9, v127
	v_mov_b32_e32 v11, v0
	v_mov_b32_e32 v0, v3
	v_mov_b32_e32 v10, v2
	v_pk_mul_f32 v[0:1], v[0:1], v[4:5] op_sel_hi:[1,0]
	v_pk_mul_f32 v[10:11], v[10:11], v[4:5] op_sel_hi:[1,0]
	v_mov_b32_e32 v13, v8
	v_mov_b32_e32 v8, v7
	v_mov_b32_e32 v12, v6
	v_pk_mul_f32 v[0:1], v[8:9], v[0:1]
	v_pk_mul_f32 v[10:11], v[12:13], v[10:11]
	v_and_b32_sdwa v4, v1, v213 dst_sel:DWORD dst_unused:UNUSED_PAD src0_sel:WORD_1 src1_sel:DWORD
	v_and_b32_sdwa v5, v0, v213 dst_sel:DWORD dst_unused:UNUSED_PAD src0_sel:WORD_1 src1_sel:DWORD
	v_and_b32_sdwa v2, v11, v213 dst_sel:DWORD dst_unused:UNUSED_PAD src0_sel:WORD_1 src1_sel:DWORD
	v_and_b32_sdwa v3, v10, v213 dst_sel:DWORD dst_unused:UNUSED_PAD src0_sel:WORD_1 src1_sel:DWORD
	v_add3_u32 v1, v1, v4, s76
	v_add3_u32 v0, v0, v5, s76
	v_add3_u32 v3, v10, v3, s76
	v_add3_u32 v2, v11, v2, s76
	v_and_b32_e32 v1, 0xffff0000, v1
	v_and_b32_e32 v0, 0xffff0000, v0
	v_or_b32_sdwa v1, v1, v2 dst_sel:DWORD dst_unused:UNUSED_PAD src0_sel:DWORD src1_sel:WORD_1
	v_or_b32_sdwa v0, v0, v3 dst_sel:DWORD dst_unused:UNUSED_PAD src0_sel:DWORD src1_sel:WORD_1
	global_store_dwordx2 v[18:19], v[0:1], off offset:224
	s_cbranch_vccnz .LBB0_577

; #define GAS __attribute__((address_space(1)))
; __device__ __forceinline__ void attn_wg_task(const Frame& F, int l, int task) {
;     ...
;     const int tq0 = b * S + (4 * cq + wch) * CH + qi0;
;     bf16x8 Qf[2][4];
; #pragma unroll
;     for (int qb = 0; qb < 2; ++qb) {
;         const int tq = tq0 + qb * 16;
;         float ssq = 0.f;
; #pragma unroll
;         for (int w = 0; w < 4; ++w) ssq += *(const GAS float*)(SSQ + (size_t)((0 * 8 + h) * 4 + w) * T + tq);
;         const float rs = frsq(ssq * (1.f / HD) + EPS) * (pg8::KSCALE * LOG2E);
; #pragma unroll
;         for (int ks = 0; ks < 4; ++ks) {
;             const float* gp = F.qa_g + l * HD + ks * 32 + rq * 8; const float* kp = F.ka_g + l * HD + ks * 32 + rq * 8;
;             const f32x4 a0 = ld_f4(gp), a1 = ld_f4(gp + 4), b0 = ld_f4(kp), b1 = ld_f4(kp + 4);
;             const u32x4 raw = ld_u4(TOK + (size_t)tq * TOKP + TK_QA + h * HD + ks * 32 + rq * 8);
;             u32x4 o;
;             o.x = pk2(bf_lo(raw.x) * rs * (a0[0] * b0[0]), bf_hi(raw.x) * rs * (a0[1] * b0[1])); o.y = pk2(bf_lo(raw.y) * rs * (a0[2] * b0[2]), bf_hi(raw.y) * rs * (a0[3] * b0[3]));
;             o.z = pk2(bf_lo(raw.z) * rs * (a1[0] * b1[0]), bf_hi(raw.z) * rs * (a1[1] * b1[1])); o.w = pk2(bf_lo(raw.w) * rs * (a1[2] * b1[2]), bf_hi(raw.w) * rs * (a1[3] * b1[3]));
;             Qf[qb][ks] = __builtin_bit_cast(bf16x8, o);
;         }
;     }
;     float m_run[2] = {-1e30f, -1e30f}, l_run[2] = {0.f, 0.f};
;     f32x4 O[2][8];
; #pragma unroll
;     for (int qb = 0; qb < 2; ++qb)
; #pragma unroll
;         for (int db = 0; db < 8; ++db) O[qb][db] = (f32x4){0.f, 0.f, 0.f, 0.f};
;     const int p0 = tid, p1 = tid + 512;
;     const int kr0 = p0 >> 4, kr1 = p1 >> 4;
;     const int kl0 = (kr0 & 32) + ((kr0 >> 2) & 1) * 16 + ((kr0 >> 3) & 3) * 4 + (kr0 & 3), kl1 = (kr1 & 32) + ((kr1 >> 2) & 1) * 16 + ((kr1 >> 3) & 3) * 4 + (kr1 & 3);
;     const bf16* gk0 = TOK + (size_t)(b * S + kr0) * TOKP + TK_KA + h * HD + (p0 & 15) * 8; const bf16* gk1 = TOK + (size_t)(b * S + kr1) * TOKP + TK_KA + h * HD + (p1 & 15) * 8;
;     const bf16* gv0 = SWP + (size_t)(SW_VA + h * HD + (p0 >> 3)) * SWPP + b * S + (p0 & 7) * 8; const bf16* gv1 = SWP + (size_t)(SW_VA + h * HD + (p1 >> 3)) * SWPP + b * S + (p1 & 7) * 8;
;     const int lk0 = A_KBUF + kl0 * A_KP + (p0 & 15) * 16, lk1 = A_KBUF + kl1 * A_KP + (p1 & 15) * 16;
.LBB0_521:
	s_lshl_b32 s1, s19, 2
	s_and_b32 s21, s1, 28
	s_lshl_b32 s20, s19, 5
	s_add_i32 s1, s21, s25
	s_waitcnt vmcnt(0)
	v_mov_b32_e32 v123, v212
	s_bfe_u32 s4, s19, 0x30003
	s_and_b32 s0, s20, 0xfffff800
	s_lshl_b32 s1, s1, 6
	s_add_i32 s1, s1, s0
	v_and_b32_e32 v122, 15, v123
	s_lshl_b32 s17, s4, 7
	s_lshl_b32 s96, s4, 8
	v_or_b32_e32 v207, s66, v122
	s_add_u32 s2, s80, s96
	v_or_b32_e32 v152, s1, v207
	s_addc_u32 s3, s81, 0
	v_and_b32_e32 v184, 48, v123
	s_waitcnt lgkmcnt(0)
	v_lshl_add_u64 v[0:1], s[2:3], 0, v[184:185]
	v_ashrrev_i32_e32 v153, 31, v152
	s_lshl_b32 s2, s4, 18
	v_bfe_u32 v204, v123, 4, 2
	v_lshl_add_u64 v[2:3], v[152:153], 2, s[88:89]
	s_mov_b32 s3, s97
	s_or_b32 s8, s2, 0x10000
	s_mov_b32 s9, s97
	s_or_b32 s14, s2, 0x20000
	s_mov_b32 s15, s97
	s_or_b32 s22, s2, 0x30000
	s_mov_b32 s23, s97
	v_lshlrev_b32_e32 v206, 5, v204
	v_lshl_add_u64 v[4:5], v[2:3], 0, s[2:3]
	v_lshl_add_u64 v[6:7], v[2:3], 0, s[8:9]
	v_lshl_add_u64 v[8:9], v[2:3], 0, s[14:15]
	v_lshl_add_u64 v[2:3], v[2:3], 0, s[22:23]
	s_movk_i32 s1, 0x2900
	global_load_dword v64, v[4:5], off
	global_load_dword v65, v[6:7], off
	global_load_dword v70, v[8:9], off
	global_load_dword v71, v[2:3], off
	v_mad_i64_i32 v[2:3], s[12:13], v152, s1, v[0:1]
	global_load_dwordx4 v[84:87], v206, s[38:39] offset:16
	global_load_dwordx4 v[92:95], v206, s[38:39]
	global_load_dwordx4 v[88:91], v206, s[40:41] offset:16
	global_load_dwordx4 v[96:99], v206, s[40:41]
	global_load_dwordx4 v[56:59], v206, s[38:39] offset:144
	global_load_dwordx4 v[72:75], v206, s[38:39] offset:128
	global_load_dwordx4 v[60:63], v206, s[40:41] offset:144
	global_load_dwordx4 v[76:79], v206, s[40:41] offset:128
	global_load_dwordx4 v[80:83], v[2:3], off
	global_load_dwordx4 v[52:55], v[2:3], off offset:64
	global_load_dwordx4 v[32:35], v206, s[38:39] offset:272
	global_load_dwordx4 v[40:43], v206, s[38:39] offset:256
	global_load_dwordx4 v[36:39], v206, s[40:41] offset:272
	global_load_dwordx4 v[44:47], v206, s[40:41] offset:256
	global_load_dwordx4 v[8:11], v206, s[38:39] offset:400
	global_load_dwordx4 v[16:19], v206, s[38:39] offset:384
	s_waitcnt lgkmcnt(0)
	global_load_dwordx4 v[12:15], v206, s[40:41] offset:400
	global_load_dwordx4 v[20:23], v206, s[40:41] offset:384
	global_load_dwordx4 v[28:31], v[2:3], off offset:128
	global_load_dwordx4 v[4:7], v[2:3], off offset:192
	v_add_u32_e32 v110, 0x200, v123
	s_waitcnt vmcnt(32)
	v_ashrrev_i32_e32 v132, 4, v123
	v_ashrrev_i32_e32 v131, 4, v110
	v_add_u32_e32 v128, s0, v132
	v_mov_b64_e32 v[100:101], s[80:81]
	v_add_u32_e32 v129, s0, v131
	v_or_b32_e32 v148, 16, v152
	s_add_u32 s12, s88, s2
	v_mad_i64_i32 v[102:103], s[2:3], v128, s1, v[100:101]
	v_mad_i64_i32 v[100:101], s[2:3], v129, s1, v[100:101]
	v_ashrrev_i32_e32 v149, 31, v148
	v_lshl_add_u64 v[102:103], v[102:103], 0, s[96:97]
	v_lshlrev_b32_e32 v116, 4, v122
	v_mov_b32_e32 v117, v185
	v_lshl_add_u64 v[100:101], v[100:101], 0, s[96:97]
	v_ashrrev_i32_e32 v133, 3, v123
	v_lshlrev_b64 v[2:3], 2, v[148:149]
	v_lshl_add_u64 v[102:103], v[102:103], 0, v[116:117]
	v_lshl_add_u64 v[100:101], v[100:101], 0, v[116:117]
	v_add_u32_e32 v117, s17, v133
	v_mov_b64_e32 v[104:105], s[64:65]
	s_mov_b32 s5, 0x8100
	v_ashrrev_i32_e32 v134, 3, v110
	v_lshl_add_u64 v[24:25], s[88:89], 0, v[2:3]
	s_addc_u32 s13, s89, 0
	v_mad_i64_i32 v[0:1], s[2:3], v148, s1, v[0:1]
	v_mad_i64_i32 v[106:107], s[2:3], v117, s5, v[104:105]
	s_ashr_i32 s1, s0, 31
	v_add_u32_e32 v130, s17, v134
	v_lshl_add_u64 v[26:27], v[24:25], 0, s[8:9]
	s_lshl_b64 s[2:3], s[0:1], 1
	v_and_b32_e32 v108, 7, v123
	v_mad_i64_i32 v[104:105], s[8:9], v130, s5, v[104:105]
	v_lshlrev_b32_e32 v118, 4, v108
	v_mov_b32_e32 v119, v185
	v_lshl_add_u64 v[104:105], v[104:105], 0, s[2:3]
	v_lshl_add_u64 v[110:111], v[104:105], 0, v[118:119]
	v_sub_u32_e64 v104, 8, s21 clamp
	v_lshl_add_u64 v[48:49], v[24:25], 0, s[14:15]
	v_readfirstlane_b32 s18, v104
	s_add_i32 s5, s21, s18
	s_lshl_b32 s5, s5, 6
	s_add_i32 s14, s5, 0xfffffe00
	v_lshl_add_u64 v[2:3], s[12:13], 0, v[2:3]
	v_lshl_add_u64 v[24:25], v[24:25], 0, s[22:23]
	v_lshl_add_u64 v[106:107], v[106:107], 0, s[2:3]
	s_ashr_i32 s15, s14, 31
	v_mad_i64_i32 v[102:103], s[8:9], s14, v223, v[102:103]
	v_mad_i64_i32 v[100:101], s[8:9], s14, v223, v[100:101]
	global_load_dword v124, v[2:3], off
	global_load_dword v125, v[26:27], off
	global_load_dword v126, v[48:49], off
	global_load_dword v127, v[24:25], off
	global_load_dwordx4 v[66:69], v[0:1], off
	s_nop 0
	global_load_dwordx4 v[48:51], v[0:1], off offset:64
	global_load_dwordx4 v[24:27], v[0:1], off offset:128
	s_nop 0
	global_load_dwordx4 v[0:3], v[0:1], off offset:192
	v_lshl_add_u64 v[108:109], v[106:107], 0, v[118:119]
	s_lshl_b64 s[8:9], s[14:15], 1
	v_lshl_add_u64 v[108:109], v[108:109], 0, s[8:9]
	v_lshl_add_u64 v[110:111], v[110:111], 0, s[8:9]
	s_barrier
	global_load_dwordx4 v[104:107], v[102:103], off offset:2048
	s_nop 0
	global_load_dwordx4 v[100:103], v[100:101], off offset:2048
	s_nop 0
	global_load_dwordx4 v[112:115], v[108:109], off
	s_nop 0
	global_load_dwordx4 v[108:111], v[110:111], off
	v_and_b32_e32 v119, 63, v123
	v_mov_b32_e32 v228, 0
	v_cmp_gt_i32_e64 s[34:35], 64, v123
	v_lshlrev_b32_e32 v120, 2, v119
	s_and_saveexec_b64 s[8:9], s[34:35]
	s_cbranch_execz .LBB0_523
	s_lshl_b64 s[22:23], s[0:1], 2
	s_add_u32 s12, s12, s22
	s_addc_u32 s13, s13, s23
	v_mov_b32_e32 v121, v185
	v_lshl_add_u64 v[136:137], s[12:13], 0, v[120:121]
	v_lshl_add_u64 v[136:137], s[14:15], 2, v[136:137]
	v_add_co_u32_e32 v138, vcc, 0x200000, v136
	s_nop 1
	v_addc_co_u32_e32 v139, vcc, 0, v137, vcc
	global_load_dword v119, v[138:139], off
	v_add_co_u32_e32 v138, vcc, 0x210000, v136
	s_nop 1
	v_addc_co_u32_e32 v139, vcc, 0, v137, vcc
	global_load_dword v121, v[138:139], off
	v_add_co_u32_e32 v138, vcc, 0x220000, v136
	s_nop 1
	v_addc_co_u32_e32 v139, vcc, 0, v137, vcc
	global_load_dword v240, v[138:139], off
	v_add_co_u32_e32 v136, vcc, 0x230000, v136
	s_nop 1
	v_addc_co_u32_e32 v137, vcc, 0, v137, vcc
	global_load_dword v241, v[136:137], off
	s_waitcnt vmcnt(0)
	v_add_f32_e32 v119, 0, v119
	v_add_f32_e32 v119, v119, v121
	s_nop 0
	v_add_f32_e32 v119, v119, v240
	s_nop 0
	v_add_f32_e32 v119, v119, v241
	v_fmamk_f32 v119, v119, 0x3c000000, v214
	v_rsq_f32_e32 v228, v119

; #define A_GLOAD(j) do { const int ko = (kc0 + (j)) * CH; r0 = ld_u4(gk0 + (size_t)ko * TOKP); r1 = ld_u4(gk1 + (size_t)ko * TOKP); r2 = ld_u4(gv0 + ko); r3 = ld_u4(gv1 + ko); \
;         if (tid < 64) { float s_ = 0.f; _Pragma("unroll") for (int w = 0; w < 4; ++w) s_ += *(const GAS float*)(gss + (size_t)w * T + ko); rkv = frsq(s_ * (1.f / HD) + EPS); } } while (0)
; __device__ __forceinline__ void attn_wg_task(const Frame& F, int l, int task) {
;     ...
;         if (j < 11) A_GLOAD(j + 1);
.LBB0_526:
	v_lshl_add_u64 v[96:97], s[62:63], 0, v[162:163]
	v_lshl_add_u64 v[98:99], s[62:63], 0, v[160:161]
	v_lshl_add_u64 v[100:101], s[62:63], 0, v[154:155]
	v_lshl_add_u64 v[102:103], s[62:63], 0, v[156:157]
	global_load_dwordx4 v[104:107], v[96:97], off
	s_nop 0
	global_load_dwordx4 v[96:99], v[98:99], off
	s_nop 0
	global_load_dwordx4 v[108:111], v[100:101], off
	s_nop 0
	global_load_dwordx4 v[100:103], v[102:103], off
	s_and_saveexec_b64 s[0:1], s[34:35]
	s_cbranch_execz .LBB0_528
	v_lshl_add_u64 v[112:113], s[62:63], 0, v[158:159]
	v_add_co_u32_e32 v114, vcc, 0x700000, v112
	s_nop 1
	v_addc_co_u32_e32 v115, vcc, 0, v113, vcc
	global_load_dword v240, v[114:115], off
	v_add_co_u32_e32 v114, vcc, 0x710000, v112
	s_nop 1
	v_addc_co_u32_e32 v115, vcc, 0, v113, vcc
	global_load_dword v241, v[114:115], off
	v_add_co_u32_e32 v114, vcc, 0x720000, v112
	s_nop 1
	v_addc_co_u32_e32 v115, vcc, 0, v113, vcc
	global_load_dword v242, v[114:115], off
	v_add_co_u32_e32 v114, vcc, 0x730000, v112
	s_nop 1
	v_addc_co_u32_e32 v115, vcc, 0, v113, vcc
	global_load_dword v243, v[114:115], off

; __device__ __forceinline__ float rq_max(float v) { v = fmaxf(v, __shfl_xor(v, 16)); v = fmaxf(v, __shfl_xor(v, 32)); return v; }
; __device__ __forceinline__ float fexp2(float x) { return __builtin_amdgcn_exp2f(x); }
; __device__ __forceinline__ void attn_wg_task(const Frame& F, int l, int task) {
;     ...
;             for (int qb = 0; qb < 2; ++qb) {
;                 const float mxr = rq_max(mx[qb]);
;                 const float mn = fmaxf(m_run[qb], mxr); alpha[qb] = fexp2(m_run[qb] - mn);
;                 moved = moved || (mn > m_run[qb]);
;                 float ps = 0.f;
; #pragma unroll
;                 for (int g = 0; g < 2; ++g) {
; #pragma unroll
;                     for (int ab = 0; ab < 2; ++ab)
; #pragma unroll
;                         for (int e = 0; e < 4; ++e) { const float p = fexp2(sa[qb][g][ab][e] - mn); sa[qb][g][ab][e] = p; ps += p; }
;                     Pf[qb][g] = pack8(sa[qb][g][0], sa[qb][g][1]);
;                 }
;                 l_run[qb] = l_run[qb] * alpha[qb] + ps; m_run[qb] = mn;
;             }
.LBB0_535:
	v_sub_f32_e32 v112, v166, v130
	v_exp_f32_e32 v117, v112
	v_sub_f32_e32 v112, v167, v130
	v_exp_f32_e32 v119, v112
	v_sub_f32_e32 v112, v170, v130
	v_exp_f32_e32 v133, v112
	v_sub_f32_e32 v112, v171, v130
	v_exp_f32_e32 v135, v112
	v_sub_f32_e32 v112, v172, v130
	v_exp_f32_e32 v137, v112
	v_sub_f32_e32 v112, v173, v130
	v_exp_f32_e32 v139, v112
	v_sub_f32_e32 v112, v174, v130
	v_exp_f32_e32 v141, v112
	v_sub_f32_e32 v112, v175, v130
	v_exp_f32_e32 v143, v112
	s_nop 5
	v_cvt_pk_bf16_f32 v123, v141, v143
	v_sub_f32_e32 v112, v180, v130
	v_exp_f32_e32 v167, v112
	v_sub_f32_e32 v112, v181, v130
	v_exp_f32_e32 v171, v112
	v_sub_f32_e32 v112, v182, v130
	v_exp_f32_e32 v173, v112
	v_sub_f32_e32 v112, v183, v130
	v_exp_f32_e32 v175, v112
	v_sub_f32_e32 v112, v196, v130
	v_exp_f32_e32 v181, v112
	v_sub_f32_e32 v112, v197, v130
	s_nop 1
	v_exp_f32_e32 v183, v112
	v_sub_f32_e32 v112, v198, v130
	s_nop 3
	v_exp_f32_e32 v197, v112
	v_sub_f32_e32 v112, v199, v130
	s_nop 3
	v_cvt_pk_bf16_f32 v121, v133, v135
	v_exp_f32_e32 v199, v112
	s_nop 7
	v_cvt_pk_bf16_f32 v122, v137, v139
	v_cvt_pk_bf16_f32 v120, v117, v119
	s_nop 7
	v_sub_f32_e32 v124, v168, v131
	s_nop 3
	v_exp_f32_e32 v132, v124
	v_sub_f32_e32 v124, v169, v131
	s_nop 3
	v_exp_f32_e32 v134, v124
	v_sub_f32_e32 v124, v144, v131
	v_cvt_pk_bf16_f32 v115, v197, v199
	v_cvt_pk_bf16_f32 v114, v181, v183
	v_cvt_pk_bf16_f32 v113, v173, v175
	v_cvt_pk_bf16_f32 v112, v167, v171
	v_sub_f32_e32 v116, v164, v131
	v_sub_f32_e32 v118, v165, v131
	v_exp_f32_e32 v136, v124
	v_sub_f32_e32 v124, v145, v131
	v_exp_f32_e32 v116, v116
	v_exp_f32_e32 v118, v118
	v_exp_f32_e32 v138, v124
	v_sub_f32_e32 v124, v146, v131
	v_exp_f32_e32 v140, v124
	v_sub_f32_e32 v124, v147, v131
	v_exp_f32_e32 v142, v124
	v_bfe_u32 v127, v118, 16, 1
	v_bfe_u32 v146, v116, 16, 1
	v_add3_u32 v144, v118, v127, s76
	v_bfe_u32 v127, v132, 16, 1
	s_nop 0
	v_add3_u32 v146, v116, v146, s76
	v_pk_add_f32 v[116:117], v[116:117], 0 op_sel_hi:[1,0]
	s_nop 1
	v_add3_u32 v127, v132, v127, s76
	v_pk_add_f32 v[116:117], v[118:119], v[116:117]
	s_nop 0
	v_lshrrev_b32_e32 v164, 16, v127
	s_nop 0
	v_lshrrev_b32_e32 v145, 16, v146
	v_pk_add_f32 v[116:117], v[132:133], v[116:117]
	v_cvt_pk_bf16_f32 v127, v140, v142
	v_and_or_b32 v124, v144, s75, v145
	v_sub_f32_e32 v144, v176, v131
	v_pk_add_f32 v[116:117], v[134:135], v[116:117]
	v_exp_f32_e32 v166, v144
	v_pk_add_f32 v[116:117], v[136:137], v[116:117]
	v_bfe_u32 v125, v134, 16, 1
	v_pk_add_f32 v[116:117], v[138:139], v[116:117]
	v_bfe_u32 v147, v136, 16, 1
	v_pk_add_f32 v[116:117], v[140:141], v[116:117]
	v_add3_u32 v125, v134, v125, s76
	v_pk_add_f32 v[116:117], v[142:143], v[116:117]
	v_add3_u32 v147, v136, v147, s76
	v_pk_add_f32 v[132:133], v[166:167], v[116:117]
	v_sub_f32_e32 v116, v177, v131
	v_exp_f32_e32 v170, v116
	v_sub_f32_e32 v116, v178, v131
	v_exp_f32_e32 v172, v116
	v_sub_f32_e32 v116, v179, v131
	v_exp_f32_e32 v174, v116
	v_sub_f32_e32 v116, v194, v131
	v_exp_f32_e32 v180, v116
	v_sub_f32_e32 v116, v195, v131
	v_exp_f32_e32 v182, v116
	v_sub_f32_e32 v116, v200, v131
	v_pk_add_f32 v[132:133], v[170:171], v[132:133]
	v_exp_f32_e32 v196, v116
	v_sub_f32_e32 v116, v201, v131
	v_pk_add_f32 v[132:133], v[172:173], v[132:133]
	v_exp_f32_e32 v198, v116
	v_pk_add_f32 v[132:133], v[174:175], v[132:133]
	s_nop 0
	v_pk_add_f32 v[132:133], v[180:181], v[132:133]
	s_nop 0
	v_pk_add_f32 v[132:133], v[182:183], v[132:133]
	v_bfe_u32 v119, v172, 16, 1
	s_nop 1
	v_pk_add_f32 v[132:133], v[196:197], v[132:133]
	v_bfe_u32 v126, v138, 16, 1
	s_nop 1
	v_add3_u32 v119, v172, v119, s76
	s_nop 0
	v_pk_add_f32 v[132:133], v[198:199], v[132:133]
	s_mul_i32 s0, s3, 0x4800
	v_add3_u32 v126, v138, v126, s76
	s_nop 0
	v_lshrrev_b32_e32 v138, 16, v119
	s_nop 1
	v_pk_fma_f32 v[150:151], v[150:151], v[128:129], v[132:133]
	v_add_u32_e32 v128, s0, v205
	v_cvt_pk_bf16_f32 v119, v196, v198
	v_cvt_pk_bf16_f32 v116, v166, v170
	ds_read_b128 v[132:135], v128 offset:34816
	v_lshrrev_b32_e32 v146, 16, v147
	v_and_or_b32 v125, v125, s75, v164
	v_and_or_b32 v126, v126, s75, v146
	s_waitcnt lgkmcnt(0)
; #define LAS __attribute__((address_space(3)))
; __device__ __forceinline__ f32x4 mfma16(bf16x8 a, bf16x8 b, f32x4 c) { return __builtin_amdgcn_mfma_f32_16x16x32_bf16(a, b, c, 0, 0, 0); }
; __device__ __forceinline__ void attn_wg_task(const Frame& F, int l, int task) {
;     ...
;                     Pf[qb][g] = pack8(sa[qb][g][0], sa[qb][g][1]);
;                 }
;                 l_run[qb] = l_run[qb] * alpha[qb] + ps; m_run[qb] = mn;
;             }
;             if (__any(moved)) {
; #pragma unroll
;                 for (int qb = 0; qb < 2; ++qb)
; #pragma unroll
;                     for (int db = 0; db < 8; ++db) O[qb][db] *= alpha[qb];
;             }
; #pragma unroll
;             for (int g = 0; g < 2; ++g)
; #pragma unroll
;                 for (int db = 0; db < 8; ++db) { const bf16x8 vf = *(const LAS bf16x8*)(vb + db * 16 * A_VP + g * 64); O[0][db] = mfma16(vf, Pf[0][g], O[0][db]); O[1][db] = mfma16(vf, Pf[1][g], O[1][db]); }
	v_mfma_f32_16x16x32_bf16 v[32:35], v[132:135], v[120:123], v[32:35]
	v_bfe_u32 v137, v180, 16, 1
	s_nop 1
	v_mfma_f32_16x16x32_bf16 v[4:7], v[132:135], v[124:127], v[4:7]
	ds_read_b128 v[132:135], v128 offset:37120
	v_add3_u32 v137, v180, v137, s76
	s_nop 0
	s_waitcnt lgkmcnt(0)
	v_mfma_f32_16x16x32_bf16 v[36:39], v[132:135], v[120:123], v[36:39]
	s_nop 0
	v_lshrrev_b32_e32 v136, 16, v137
	v_cvt_pk_bf16_f32 v117, v172, v174
	v_mfma_f32_16x16x32_bf16 v[8:11], v[132:135], v[124:127], v[8:11]
	ds_read_b128 v[132:135], v128 offset:39424
	v_cvt_pk_bf16_f32 v118, v180, v182
	v_mov_b32_e32 v232, v131
	s_waitcnt lgkmcnt(0)
	v_mfma_f32_16x16x32_bf16 v[40:43], v[132:135], v[120:123], v[40:43]
	v_mfma_f32_16x16x32_bf16 v[0:3], v[132:135], v[124:127], v[0:3]
	ds_read_b128 v[132:135], v128 offset:41728
	s_waitcnt lgkmcnt(0)
	v_mfma_f32_16x16x32_bf16 v[44:47], v[132:135], v[120:123], v[44:47]
	v_mfma_f32_16x16x32_bf16 v[12:15], v[132:135], v[124:127], v[12:15]
	ds_read_b128 v[132:135], v128 offset:44032
	s_waitcnt lgkmcnt(0)
	v_mfma_f32_16x16x32_bf16 v[48:51], v[132:135], v[120:123], v[48:51]
	v_mfma_f32_16x16x32_bf16 v[16:19], v[132:135], v[124:127], v[16:19]
	ds_read_b128 v[132:135], v128 offset:46336
	s_waitcnt lgkmcnt(0)
	v_mfma_f32_16x16x32_bf16 v[52:55], v[132:135], v[120:123], v[52:55]
	v_mfma_f32_16x16x32_bf16 v[20:23], v[132:135], v[124:127], v[20:23]
	ds_read_b128 v[132:135], v128 offset:48640
	s_waitcnt lgkmcnt(0)
	v_mfma_f32_16x16x32_bf16 v[56:59], v[132:135], v[120:123], v[56:59]
	v_mfma_f32_16x16x32_bf16 v[24:27], v[132:135], v[124:127], v[24:27]
	ds_read_b128 v[132:135], v128 offset:50944
	s_waitcnt lgkmcnt(0)
	v_mfma_f32_16x16x32_bf16 v[60:63], v[132:135], v[120:123], v[60:63]
	ds_read_b128 v[120:123], v128 offset:34880
	s_waitcnt lgkmcnt(0)
	v_mfma_f32_16x16x32_bf16 v[32:35], v[120:123], v[112:115], v[32:35]
	v_mfma_f32_16x16x32_bf16 v[4:7], v[120:123], v[116:119], v[4:7]
	ds_read_b128 v[120:123], v128 offset:37184
	s_waitcnt lgkmcnt(0)
	v_mfma_f32_16x16x32_bf16 v[36:39], v[120:123], v[112:115], v[36:39]
	v_mfma_f32_16x16x32_bf16 v[8:11], v[120:123], v[116:119], v[8:11]
	ds_read_b128 v[120:123], v128 offset:39488
	s_waitcnt lgkmcnt(0)
	v_mfma_f32_16x16x32_bf16 v[40:43], v[120:123], v[112:115], v[40:43]
	v_mfma_f32_16x16x32_bf16 v[0:3], v[120:123], v[116:119], v[0:3]
	ds_read_b128 v[120:123], v128 offset:41792
	s_waitcnt lgkmcnt(0)
	v_mfma_f32_16x16x32_bf16 v[44:47], v[120:123], v[112:115], v[44:47]
	v_mfma_f32_16x16x32_bf16 v[12:15], v[120:123], v[116:119], v[12:15]
	ds_read_b128 v[120:123], v128 offset:44096
	s_waitcnt lgkmcnt(0)
	v_mfma_f32_16x16x32_bf16 v[48:51], v[120:123], v[112:115], v[48:51]
	v_mfma_f32_16x16x32_bf16 v[16:19], v[120:123], v[116:119], v[16:19]
	ds_read_b128 v[120:123], v128 offset:46400
	s_waitcnt lgkmcnt(0)
	v_mfma_f32_16x16x32_bf16 v[52:55], v[120:123], v[112:115], v[52:55]
	v_mfma_f32_16x16x32_bf16 v[20:23], v[120:123], v[116:119], v[20:23]
	ds_read_b128 v[120:123], v128 offset:48704
	s_waitcnt lgkmcnt(0)
	v_mfma_f32_16x16x32_bf16 v[56:59], v[120:123], v[112:115], v[56:59]
	v_mfma_f32_16x16x32_bf16 v[24:27], v[120:123], v[116:119], v[24:27]
	ds_read_b128 v[120:123], v128 offset:51008
	v_mfma_f32_16x16x32_bf16 v[28:31], v[132:135], v[124:127], v[28:31]
	s_waitcnt lgkmcnt(0)
	v_mfma_f32_16x16x32_bf16 v[60:63], v[120:123], v[112:115], v[60:63]
	v_mfma_f32_16x16x32_bf16 v[28:31], v[120:123], v[116:119], v[28:31]
	s_branch .LBB0_537

.LBB0_537:
	s_xor_b32 s3, s3, 1
	s_mul_i32 s0, s3, 0x4400
	v_add_u32_e32 v112, s0, v209
	s_waitcnt vmcnt(3)
	ds_write_b128 v112, v[104:107]
	v_add_u32_e32 v104, s0, v210
	s_mul_i32 s0, s3, 0x4800
	s_waitcnt vmcnt(2)
	ds_write_b128 v104, v[96:99]
	v_add_u32_e32 v96, s0, v226
	s_waitcnt vmcnt(1)
	ds_write_b128 v96, v[108:111] offset:34816
	v_add_u32_e32 v96, s0, v227
	s_waitcnt vmcnt(0)
	ds_write_b128 v96, v[100:103] offset:34816
	s_and_saveexec_b64 s[0:1], s[34:35]
	v_add_f32_e32 v240, 0, v240
	v_lshl_add_u32 v96, s3, 8, v230
	v_add_f32_e32 v240, v240, v241
	s_nop 0
	v_add_f32_e32 v240, v240, v242
	s_nop 0
	v_add_f32_e32 v240, v240, v243
	s_nop 0
	v_fmamk_f32 v240, v240, 0x3c000000, v214
	s_nop 0
	v_rsq_f32_e32 v228, v240
	s_nop 1
	ds_write_b32 v96, v228
	s_or_b64 exec, exec, s[0:1]
	s_sub_i32 s2, s2, 64
	s_add_i32 s18, s18, 1
	s_add_i32 s0, s9, s2
	s_mov_b64 s[4:5], 0xa4000
	v_lshl_add_u64 v[154:155], v[154:155], 0, s[46:47]
	v_lshl_add_u64 v[156:157], v[156:157], 0, s[46:47]
	v_lshl_add_u64 v[158:159], v[158:159], 0, s[10:11]
	v_lshl_add_u64 v[160:161], v[160:161], 0, s[4:5]
	s_cmpk_eq_i32 s0, 0xff40
	v_lshl_add_u64 v[162:163], v[162:163], 0, s[4:5]
	s_waitcnt lgkmcnt(0)
	s_barrier
	s_cbranch_scc1 .LBB0_541
	v_mov_b32_e32 v233, v130
	s_branch .LBB0_526

; __device__ __forceinline__ unsigned pk2(float lo, float hi) { return f2bf(lo) | (f2bf(hi) << 16); }
; __device__ __forceinline__ float rq_sum(float v) { v += __shfl_xor(v, 16); v += __shfl_xor(v, 32); return v; }
; __device__ __forceinline__ float frsq(float x) { return __builtin_amdgcn_rsqf(x); }
; __device__ __forceinline__ void attn_wg_task(const Frame& F, int l, int task) {
;     ...
;     for (int qb = 0; qb < 2; ++qb) {
;         const int tq = tq0 + qb * 16;
;         const float inv = 1.0f / rq_sum(l_run[qb]);
;         float ss = 0.f;
; #pragma unroll
;         for (int db = 0; db < 8; ++db) { O[qb][db] *= inv; ss += (O[qb][db][0] * O[qb][db][0] + O[qb][db][1] * O[qb][db][1]) + (O[qb][db][2] * O[qb][db][2] + O[qb][db][3] * O[qb][db][3]); }
;         const float rstd = frsq(rq_sum(ss) * (1.f / HD) + EPS);
; #pragma unroll
;         for (int db = 0; db < 8; ++db) {
;             const int d0 = h * HD + db * 16 + rq * 4;
;             const f32x4 g4 = ld_f4(F.attn_g + l * 1024 + d0);
;             u32x2 o; o.x = pk2(O[qb][db][0] * rstd * g4[0], O[qb][db][1] * rstd * g4[1]); o.y = pk2(O[qb][db][2] * rstd * g4[2], O[qb][db][3] * rstd * g4[3]);
;             st_u2(MIX + (size_t)tq * D + d0, o);
.LBB0_549:
	ds_bpermute_b32 v64, v202, v151
	v_lshl_or_b32 v82, v204, 2, s19
	v_readlane_b32 s2, v251, 53
	v_readlane_b32 s3, v251, 54
	s_waitcnt lgkmcnt(0)
	v_add_f32_e32 v64, v151, v64
	ds_bpermute_b32 v65, v203, v64
	s_barrier
	s_waitcnt lgkmcnt(0)
	v_lshlrev_b32_e32 v184, 1, v82
	s_add_i32 s18, s18, s87
	v_add_f32_e32 v64, v64, v65
	v_div_scale_f32 v65, s[0:1], v64, v64, 1.0
	v_rcp_f32_e32 v66, v65
	s_nop 0
	v_fma_f32 v67, -v65, v66, 1.0
	v_fmac_f32_e32 v66, v67, v66
	v_div_scale_f32 v67, vcc, 1.0, v64, 1.0
	v_mul_f32_e32 v68, v67, v66
	v_fma_f32 v69, -v65, v68, v67
	v_fmac_f32_e32 v68, v69, v66
	v_fma_f32 v65, -v65, v68, v67
	v_div_fmas_f32 v65, v65, v66, v68
	v_div_fixup_f32 v84, v65, v64, 1.0
	v_pk_mul_f32 v[80:81], v[32:33], v[84:85] op_sel_hi:[1,0]
	v_pk_mul_f32 v[76:77], v[36:37], v[84:85] op_sel_hi:[1,0]
	v_pk_mul_f32 v[78:79], v[34:35], v[84:85] op_sel_hi:[1,0]
	v_pk_mul_f32 v[74:75], v[38:39], v[84:85] op_sel_hi:[1,0]
	v_mov_b32_e32 v34, v81
	v_mov_b32_e32 v35, v77
	v_mov_b32_e32 v32, v80
	v_mov_b32_e32 v33, v76
	v_pk_mul_f32 v[34:35], v[34:35], v[34:35]
	v_mov_b32_e32 v36, v79
	v_mov_b32_e32 v37, v75
	v_pk_fma_f32 v[32:33], v[32:33], v[32:33], v[34:35]
	v_mov_b32_e32 v34, v78
	v_mov_b32_e32 v35, v74
	v_pk_mul_f32 v[36:37], v[36:37], v[36:37]
	v_pk_mul_f32 v[72:73], v[40:41], v[84:85] op_sel_hi:[1,0]
	v_pk_fma_f32 v[34:35], v[34:35], v[34:35], v[36:37]
	v_pk_mul_f32 v[70:71], v[42:43], v[84:85] op_sel_hi:[1,0]
	v_pk_add_f32 v[32:33], v[32:33], v[34:35]
	v_pk_mul_f32 v[34:35], v[70:71], v[70:71]
	v_pk_add_f32 v[32:33], v[32:33], v[32:33] op_sel_hi:[0,1]
	v_pk_mul_f32 v[36:37], v[72:73], v[72:73]
	v_pk_mul_f32 v[68:69], v[44:45], v[84:85] op_sel_hi:[1,0]
	v_pk_mov_b32 v[38:39], v[36:37], v[34:35] op_sel:[1,0]
	v_mov_b32_e32 v37, v35
	v_pk_mul_f32 v[66:67], v[46:47], v[84:85] op_sel_hi:[1,0]
	v_mul_f32_e32 v32, v68, v68
	v_pk_add_f32 v[34:35], v[38:39], v[36:37]
	v_pk_fma_f32 v[36:37], v[68:69], v[68:69], v[32:33] op_sel_hi:[1,1,0]
	v_mul_f32_e32 v32, v66, v66
	v_pk_add_f32 v[34:35], v[34:35], v[34:35] op_sel_hi:[0,1]
	v_pk_fma_f32 v[38:39], v[66:67], v[66:67], v[32:33] op_sel_hi:[1,1,0]
	v_pk_mul_f32 v[50:51], v[50:51], v[84:85] op_sel_hi:[1,0]
	v_pk_mul_f32 v[64:65], v[48:49], v[84:85] op_sel_hi:[1,0]
	v_mul_f32_e32 v34, v50, v50
	v_mul_f32_e32 v36, v64, v64
	v_mul_f32_e32 v38, v65, v65
	v_mul_f32_e32 v32, v51, v51
	v_pk_add_f32 v[36:37], v[36:37], v[38:39]
	v_pk_add_f32 v[32:33], v[34:35], v[32:33]
	v_pk_mul_f32 v[48:49], v[52:53], v[84:85] op_sel_hi:[1,0]
	v_pk_add_f32 v[32:33], v[36:37], v[32:33]
	v_pk_mul_f32 v[46:47], v[54:55], v[84:85] op_sel_hi:[1,0]
	v_pk_add_f32 v[32:33], v[32:33], v[32:33] op_sel_hi:[0,1]
	v_pk_mul_f32 v[34:35], v[46:47], v[46:47]
	v_pk_mul_f32 v[36:37], v[48:49], v[48:49]
	v_pk_mul_f32 v[44:45], v[56:57], v[84:85] op_sel_hi:[1,0]
	v_pk_mov_b32 v[38:39], v[36:37], v[34:35] op_sel:[1,0]
	v_mov_b32_e32 v37, v35
	v_pk_mul_f32 v[42:43], v[58:59], v[84:85] op_sel_hi:[1,0]
	v_mul_f32_e32 v32, v44, v44
	v_pk_add_f32 v[34:35], v[38:39], v[36:37]
	v_pk_fma_f32 v[40:41], v[44:45], v[44:45], v[32:33] op_sel_hi:[1,1,0]
	v_mul_f32_e32 v32, v42, v42
	v_pk_add_f32 v[34:35], v[34:35], v[34:35] op_sel_hi:[0,1]
	v_pk_fma_f32 v[52:53], v[42:43], v[42:43], v[32:33] op_sel_hi:[1,1,0]
	v_pk_mul_f32 v[36:37], v[62:63], v[84:85] op_sel_hi:[1,0]
	v_pk_mul_f32 v[38:39], v[60:61], v[84:85] op_sel_hi:[1,0]
	v_mul_f32_e32 v34, v36, v36
	v_mul_f32_e32 v40, v38, v38
	v_mul_f32_e32 v52, v39, v39
	v_mul_f32_e32 v32, v37, v37
	v_pk_add_f32 v[40:41], v[40:41], v[52:53]
	v_pk_add_f32 v[32:33], v[34:35], v[32:33]
	v_lshlrev_b32_e32 v54, 2, v82
	global_load_dwordx4 v[96:99], v54, s[42:43]
	global_load_dwordx4 v[100:103], v54, s[42:43] offset:64
	global_load_dwordx4 v[104:107], v54, s[42:43] offset:128
	global_load_dwordx4 v[108:111], v54, s[42:43] offset:192
	global_load_dwordx4 v[112:115], v54, s[42:43] offset:256
	global_load_dwordx4 v[116:119], v54, s[42:43] offset:320
	global_load_dwordx4 v[120:123], v54, s[42:43] offset:384
	global_load_dwordx4 v[124:127], v54, s[42:43] offset:448
	v_pk_add_f32 v[32:33], v[40:41], v[32:33]
	v_mov_b32_e32 v56, v80
	v_add_f32_e32 v32, v32, v33
	ds_bpermute_b32 v33, v202, v32
	v_mov_b32_e32 v57, v78
	v_mov_b32_e32 v78, v81
	s_waitcnt lgkmcnt(0)
	v_add_f32_e32 v32, v32, v33
	ds_bpermute_b32 v33, v203, v32
	s_waitcnt lgkmcnt(0)
	v_add_f32_e32 v32, v32, v33
	v_fmamk_f32 v32, v32, 0x3c000000, v214
	v_rsq_f32_e32 v40, v32
	v_lshlrev_b64 v[32:33], 12, v[152:153]
	v_lshl_add_u64 v[52:53], s[2:3], 0, v[32:33]
	s_waitcnt vmcnt(0)
; __device__ __forceinline__ unsigned pk2(float lo, float hi) { return f2bf(lo) | (f2bf(hi) << 16); }
; __device__ __forceinline__ void attn_wg_task(const Frame& F, int l, int task) {
;     ...
; #pragma unroll
;         for (int db = 0; db < 8; ++db) {
;             const int d0 = h * HD + db * 16 + rq * 4;
;             const f32x4 g4 = ld_f4(F.attn_g + l * 1024 + d0);
;             u32x2 o; o.x = pk2(O[qb][db][0] * rstd * g4[0], O[qb][db][1] * rstd * g4[1]); o.y = pk2(O[qb][db][2] * rstd * g4[2], O[qb][db][3] * rstd * g4[3]);
;             st_u2(MIX + (size_t)tq * D + d0, o);
	v_mov_b32_e32 v32, v96
	v_mov_b32_e32 v33, v97
	v_mov_b32_e32 v34, v98
	v_mov_b32_e32 v35, v99
	v_pk_mul_f32 v[56:57], v[56:57], v[40:41] op_sel_hi:[1,0]
	v_mov_b32_e32 v58, v32
	v_mov_b32_e32 v59, v34
	v_pk_mul_f32 v[56:57], v[58:59], v[56:57]
	v_pk_mul_f32 v[58:59], v[78:79], v[40:41] op_sel_hi:[1,0]
	v_mov_b32_e32 v34, v33
	v_pk_mul_f32 v[32:33], v[34:35], v[58:59]
	v_and_b32_sdwa v35, v56, v213 dst_sel:DWORD dst_unused:UNUSED_PAD src0_sel:WORD_1 src1_sel:DWORD
	v_add3_u32 v41, v56, v35, s76
	v_and_b32_sdwa v35, v33, v213 dst_sel:DWORD dst_unused:UNUSED_PAD src0_sel:WORD_1 src1_sel:DWORD
	v_and_b32_sdwa v55, v32, v213 dst_sel:DWORD dst_unused:UNUSED_PAD src0_sel:WORD_1 src1_sel:DWORD
	v_and_b32_sdwa v34, v57, v213 dst_sel:DWORD dst_unused:UNUSED_PAD src0_sel:WORD_1 src1_sel:DWORD
	v_add3_u32 v33, v33, v35, s76
	v_add3_u32 v32, v32, v55, s76
	v_add3_u32 v34, v57, v34, s76
	v_and_b32_e32 v33, 0xffff0000, v33
	v_and_b32_e32 v32, 0xffff0000, v32
	v_or_b32_sdwa v35, v33, v34 dst_sel:DWORD dst_unused:UNUSED_PAD src0_sel:DWORD src1_sel:WORD_1
	v_or_b32_sdwa v34, v32, v41 dst_sel:DWORD dst_unused:UNUSED_PAD src0_sel:DWORD src1_sel:WORD_1
	v_lshl_add_u64 v[32:33], v[52:53], 0, v[184:185]
	global_store_dwordx2 v[32:33], v[34:35], off
	v_mov_b32_e32 v56, v100
	v_mov_b32_e32 v57, v101
	v_mov_b32_e32 v58, v102
	v_mov_b32_e32 v59, v103
	v_mov_b32_e32 v34, v76
	v_mov_b32_e32 v35, v74
	v_pk_mul_f32 v[34:35], v[34:35], v[40:41] op_sel_hi:[1,0]
	v_mov_b32_e32 v74, v77
	v_mov_b32_e32 v52, v56
	v_mov_b32_e32 v53, v58
	v_pk_mul_f32 v[34:35], v[52:53], v[34:35]
	v_pk_mul_f32 v[52:53], v[74:75], v[40:41] op_sel_hi:[1,0]
	v_mov_b32_e32 v58, v57
	v_pk_mul_f32 v[52:53], v[58:59], v[52:53]
	v_and_b32_sdwa v41, v35, v213 dst_sel:DWORD dst_unused:UNUSED_PAD src0_sel:WORD_1 src1_sel:DWORD
	v_and_b32_sdwa v55, v34, v213 dst_sel:DWORD dst_unused:UNUSED_PAD src0_sel:WORD_1 src1_sel:DWORD
	v_add3_u32 v34, v34, v55, s76
	v_add3_u32 v35, v35, v41, s76
	v_and_b32_sdwa v41, v53, v213 dst_sel:DWORD dst_unused:UNUSED_PAD src0_sel:WORD_1 src1_sel:DWORD
	v_and_b32_sdwa v55, v52, v213 dst_sel:DWORD dst_unused:UNUSED_PAD src0_sel:WORD_1 src1_sel:DWORD
	v_add3_u32 v41, v53, v41, s76
	v_add3_u32 v52, v52, v55, s76
	v_and_b32_e32 v41, 0xffff0000, v41
	v_and_b32_e32 v52, 0xffff0000, v52
	v_or_b32_sdwa v35, v41, v35 dst_sel:DWORD dst_unused:UNUSED_PAD src0_sel:DWORD src1_sel:WORD_1
	v_or_b32_sdwa v34, v52, v34 dst_sel:DWORD dst_unused:UNUSED_PAD src0_sel:DWORD src1_sel:WORD_1
	global_store_dwordx2 v[32:33], v[34:35], off offset:32
	v_mov_b32_e32 v56, v104
	v_mov_b32_e32 v57, v105
	v_mov_b32_e32 v58, v106
	v_mov_b32_e32 v59, v107
	v_mov_b32_e32 v34, v72
	v_mov_b32_e32 v35, v70
	v_pk_mul_f32 v[34:35], v[34:35], v[40:41] op_sel_hi:[1,0]
	v_mov_b32_e32 v70, v73
	v_mov_b32_e32 v52, v56
	v_mov_b32_e32 v53, v58
	v_pk_mul_f32 v[34:35], v[52:53], v[34:35]
	v_pk_mul_f32 v[52:53], v[70:71], v[40:41] op_sel_hi:[1,0]
	v_mov_b32_e32 v58, v57
	v_pk_mul_f32 v[52:53], v[58:59], v[52:53]
	v_and_b32_sdwa v41, v35, v213 dst_sel:DWORD dst_unused:UNUSED_PAD src0_sel:WORD_1 src1_sel:DWORD
	v_and_b32_sdwa v55, v34, v213 dst_sel:DWORD dst_unused:UNUSED_PAD src0_sel:WORD_1 src1_sel:DWORD
	v_add3_u32 v34, v34, v55, s76
	v_add3_u32 v35, v35, v41, s76
	v_and_b32_sdwa v41, v53, v213 dst_sel:DWORD dst_unused:UNUSED_PAD src0_sel:WORD_1 src1_sel:DWORD
	v_and_b32_sdwa v55, v52, v213 dst_sel:DWORD dst_unused:UNUSED_PAD src0_sel:WORD_1 src1_sel:DWORD
	v_add3_u32 v41, v53, v41, s76
	v_add3_u32 v52, v52, v55, s76
	v_and_b32_e32 v41, 0xffff0000, v41
	v_and_b32_e32 v52, 0xffff0000, v52
	v_or_b32_sdwa v35, v41, v35 dst_sel:DWORD dst_unused:UNUSED_PAD src0_sel:DWORD src1_sel:WORD_1
	v_or_b32_sdwa v34, v52, v34 dst_sel:DWORD dst_unused:UNUSED_PAD src0_sel:DWORD src1_sel:WORD_1
	global_store_dwordx2 v[32:33], v[34:35], off offset:64
	v_mov_b32_e32 v56, v108
	v_mov_b32_e32 v57, v109
	v_mov_b32_e32 v58, v110
	v_mov_b32_e32 v59, v111
	v_mov_b32_e32 v34, v68
	v_mov_b32_e32 v35, v66
	v_pk_mul_f32 v[34:35], v[34:35], v[40:41] op_sel_hi:[1,0]
	v_mov_b32_e32 v66, v69
	v_mov_b32_e32 v52, v56
	v_mov_b32_e32 v53, v58
	v_pk_mul_f32 v[34:35], v[52:53], v[34:35]
	v_pk_mul_f32 v[52:53], v[66:67], v[40:41] op_sel_hi:[1,0]
	v_mov_b32_e32 v58, v57
	v_pk_mul_f32 v[52:53], v[58:59], v[52:53]
	v_and_b32_sdwa v41, v35, v213 dst_sel:DWORD dst_unused:UNUSED_PAD src0_sel:WORD_1 src1_sel:DWORD
	v_and_b32_sdwa v55, v34, v213 dst_sel:DWORD dst_unused:UNUSED_PAD src0_sel:WORD_1 src1_sel:DWORD
	v_add3_u32 v34, v34, v55, s76
	v_add3_u32 v35, v35, v41, s76
	v_and_b32_sdwa v41, v53, v213 dst_sel:DWORD dst_unused:UNUSED_PAD src0_sel:WORD_1 src1_sel:DWORD
	v_and_b32_sdwa v55, v52, v213 dst_sel:DWORD dst_unused:UNUSED_PAD src0_sel:WORD_1 src1_sel:DWORD
	v_add3_u32 v41, v53, v41, s76
	v_add3_u32 v52, v52, v55, s76
	v_and_b32_e32 v41, 0xffff0000, v41
	v_and_b32_e32 v52, 0xffff0000, v52
	v_or_b32_sdwa v35, v41, v35 dst_sel:DWORD dst_unused:UNUSED_PAD src0_sel:DWORD src1_sel:WORD_1
	v_or_b32_sdwa v34, v52, v34 dst_sel:DWORD dst_unused:UNUSED_PAD src0_sel:DWORD src1_sel:WORD_1
	global_store_dwordx2 v[32:33], v[34:35], off offset:96
	v_mov_b32_e32 v56, v112
	v_mov_b32_e32 v57, v113
	v_mov_b32_e32 v58, v114
	v_mov_b32_e32 v59, v115
	v_mov_b32_e32 v34, v64
	v_mov_b32_e32 v35, v50
	v_pk_mul_f32 v[34:35], v[34:35], v[40:41] op_sel_hi:[1,0]
	v_mov_b32_e32 v50, v65
	v_pk_mul_f32 v[50:51], v[50:51], v[40:41] op_sel_hi:[1,0]
	v_mov_b32_e32 v52, v56
	v_mov_b32_e32 v53, v58
	v_pk_mul_f32 v[34:35], v[52:53], v[34:35]
	v_mov_b32_e32 v58, v57
	v_pk_mul_f32 v[50:51], v[58:59], v[50:51]
	v_and_b32_sdwa v41, v35, v213 dst_sel:DWORD dst_unused:UNUSED_PAD src0_sel:WORD_1 src1_sel:DWORD
; __device__ __forceinline__ unsigned pk2(float lo, float hi) { return f2bf(lo) | (f2bf(hi) << 16); }
; __device__ __forceinline__ void attn_wg_task(const Frame& F, int l, int task) {
;     ...
; #pragma unroll
;         for (int db = 0; db < 8; ++db) {
;             const int d0 = h * HD + db * 16 + rq * 4;
;             const f32x4 g4 = ld_f4(F.attn_g + l * 1024 + d0);
;             u32x2 o; o.x = pk2(O[qb][db][0] * rstd * g4[0], O[qb][db][1] * rstd * g4[1]); o.y = pk2(O[qb][db][2] * rstd * g4[2], O[qb][db][3] * rstd * g4[3]);
;             st_u2(MIX + (size_t)tq * D + d0, o);
	v_and_b32_sdwa v52, v34, v213 dst_sel:DWORD dst_unused:UNUSED_PAD src0_sel:WORD_1 src1_sel:DWORD
	v_add3_u32 v34, v34, v52, s76
	v_add3_u32 v35, v35, v41, s76
	v_and_b32_sdwa v41, v51, v213 dst_sel:DWORD dst_unused:UNUSED_PAD src0_sel:WORD_1 src1_sel:DWORD
	v_and_b32_sdwa v52, v50, v213 dst_sel:DWORD dst_unused:UNUSED_PAD src0_sel:WORD_1 src1_sel:DWORD
	v_add3_u32 v41, v51, v41, s76
	v_add3_u32 v50, v50, v52, s76
	v_and_b32_e32 v41, 0xffff0000, v41
	v_and_b32_e32 v50, 0xffff0000, v50
	v_or_b32_sdwa v35, v41, v35 dst_sel:DWORD dst_unused:UNUSED_PAD src0_sel:DWORD src1_sel:WORD_1
	v_or_b32_sdwa v34, v50, v34 dst_sel:DWORD dst_unused:UNUSED_PAD src0_sel:DWORD src1_sel:WORD_1
	global_store_dwordx2 v[32:33], v[34:35], off offset:128
	v_mov_b32_e32 v50, v116
	v_mov_b32_e32 v51, v117
	v_mov_b32_e32 v52, v118
	v_mov_b32_e32 v53, v119
	v_mov_b32_e32 v34, v48
	v_mov_b32_e32 v35, v46
	v_pk_mul_f32 v[34:35], v[34:35], v[40:41] op_sel_hi:[1,0]
	v_mov_b32_e32 v46, v49
	v_pk_mul_f32 v[46:47], v[46:47], v[40:41] op_sel_hi:[1,0]
	v_mov_b32_e32 v56, v50
	v_mov_b32_e32 v57, v52
	v_pk_mul_f32 v[34:35], v[56:57], v[34:35]
	v_mov_b32_e32 v52, v51
	v_pk_mul_f32 v[46:47], v[52:53], v[46:47]
	v_and_b32_sdwa v41, v35, v213 dst_sel:DWORD dst_unused:UNUSED_PAD src0_sel:WORD_1 src1_sel:DWORD
	v_and_b32_sdwa v48, v34, v213 dst_sel:DWORD dst_unused:UNUSED_PAD src0_sel:WORD_1 src1_sel:DWORD
	v_add3_u32 v34, v34, v48, s76
	v_add3_u32 v35, v35, v41, s76
	v_and_b32_sdwa v41, v47, v213 dst_sel:DWORD dst_unused:UNUSED_PAD src0_sel:WORD_1 src1_sel:DWORD
	v_and_b32_sdwa v48, v46, v213 dst_sel:DWORD dst_unused:UNUSED_PAD src0_sel:WORD_1 src1_sel:DWORD
	v_add3_u32 v41, v47, v41, s76
	v_add3_u32 v46, v46, v48, s76
	v_and_b32_e32 v41, 0xffff0000, v41
	v_and_b32_e32 v46, 0xffff0000, v46
	v_or_b32_sdwa v35, v41, v35 dst_sel:DWORD dst_unused:UNUSED_PAD src0_sel:DWORD src1_sel:WORD_1
	v_or_b32_sdwa v34, v46, v34 dst_sel:DWORD dst_unused:UNUSED_PAD src0_sel:DWORD src1_sel:WORD_1
	global_store_dwordx2 v[32:33], v[34:35], off offset:160
	v_mov_b32_e32 v46, v120
	v_mov_b32_e32 v47, v121
	v_mov_b32_e32 v48, v122
	v_mov_b32_e32 v49, v123
	v_mov_b32_e32 v34, v44
	v_mov_b32_e32 v35, v42
	v_pk_mul_f32 v[34:35], v[34:35], v[40:41] op_sel_hi:[1,0]
	v_mov_b32_e32 v42, v45
	v_pk_mul_f32 v[42:43], v[42:43], v[40:41] op_sel_hi:[1,0]
	v_mov_b32_e32 v50, v46
	v_mov_b32_e32 v51, v48
	v_pk_mul_f32 v[34:35], v[50:51], v[34:35]
	v_mov_b32_e32 v48, v47
	v_pk_mul_f32 v[42:43], v[48:49], v[42:43]
	v_and_b32_sdwa v41, v35, v213 dst_sel:DWORD dst_unused:UNUSED_PAD src0_sel:WORD_1 src1_sel:DWORD
	v_and_b32_sdwa v44, v34, v213 dst_sel:DWORD dst_unused:UNUSED_PAD src0_sel:WORD_1 src1_sel:DWORD
	v_add3_u32 v34, v34, v44, s76
	v_add3_u32 v35, v35, v41, s76
	v_and_b32_sdwa v41, v43, v213 dst_sel:DWORD dst_unused:UNUSED_PAD src0_sel:WORD_1 src1_sel:DWORD
	v_and_b32_sdwa v44, v42, v213 dst_sel:DWORD dst_unused:UNUSED_PAD src0_sel:WORD_1 src1_sel:DWORD
	v_add3_u32 v41, v43, v41, s76
	v_add3_u32 v42, v42, v44, s76
	v_and_b32_e32 v41, 0xffff0000, v41
	v_and_b32_e32 v42, 0xffff0000, v42
	v_or_b32_sdwa v35, v41, v35 dst_sel:DWORD dst_unused:UNUSED_PAD src0_sel:DWORD src1_sel:WORD_1
	v_or_b32_sdwa v34, v42, v34 dst_sel:DWORD dst_unused:UNUSED_PAD src0_sel:DWORD src1_sel:WORD_1
	global_store_dwordx2 v[32:33], v[34:35], off offset:192
	v_mov_b32_e32 v42, v124
	v_mov_b32_e32 v43, v125
	v_mov_b32_e32 v44, v126
	v_mov_b32_e32 v45, v127
	v_mov_b32_e32 v34, v38
	v_mov_b32_e32 v35, v36
	v_pk_mul_f32 v[34:35], v[34:35], v[40:41] op_sel_hi:[1,0]
	v_mov_b32_e32 v36, v39
	v_pk_mul_f32 v[36:37], v[36:37], v[40:41] op_sel_hi:[1,0]
	v_mov_b32_e32 v46, v42
	v_mov_b32_e32 v47, v44
	v_pk_mul_f32 v[34:35], v[46:47], v[34:35]
	v_mov_b32_e32 v44, v43
	v_pk_mul_f32 v[36:37], v[44:45], v[36:37]
	v_and_b32_sdwa v38, v35, v213 dst_sel:DWORD dst_unused:UNUSED_PAD src0_sel:WORD_1 src1_sel:DWORD
	v_and_b32_sdwa v39, v34, v213 dst_sel:DWORD dst_unused:UNUSED_PAD src0_sel:WORD_1 src1_sel:DWORD
	v_add3_u32 v34, v34, v39, s76
	v_add3_u32 v35, v35, v38, s76
	v_and_b32_sdwa v38, v37, v213 dst_sel:DWORD dst_unused:UNUSED_PAD src0_sel:WORD_1 src1_sel:DWORD
	v_and_b32_sdwa v39, v36, v213 dst_sel:DWORD dst_unused:UNUSED_PAD src0_sel:WORD_1 src1_sel:DWORD
	v_add3_u32 v37, v37, v38, s76
	v_add3_u32 v36, v36, v39, s76
	v_and_b32_e32 v37, 0xffff0000, v37
	v_and_b32_e32 v36, 0xffff0000, v36
	v_or_b32_sdwa v35, v37, v35 dst_sel:DWORD dst_unused:UNUSED_PAD src0_sel:DWORD src1_sel:WORD_1
	v_or_b32_sdwa v34, v36, v34 dst_sel:DWORD dst_unused:UNUSED_PAD src0_sel:DWORD src1_sel:WORD_1
	global_store_dwordx2 v[32:33], v[34:35], off offset:224
	ds_bpermute_b32 v32, v202, v150
	s_waitcnt lgkmcnt(0)
	v_add_f32_e32 v32, v150, v32
	ds_bpermute_b32 v33, v203, v32
	s_waitcnt lgkmcnt(0)
; __device__ __forceinline__ unsigned pk2(float lo, float hi) { return f2bf(lo) | (f2bf(hi) << 16); }
; __device__ __forceinline__ float rq_sum(float v) { v += __shfl_xor(v, 16); v += __shfl_xor(v, 32); return v; }
; __device__ __forceinline__ float frsq(float x) { return __builtin_amdgcn_rsqf(x); }
; __device__ __forceinline__ void attn_wg_task(const Frame& F, int l, int task) {
;     ...
;     for (int qb = 0; qb < 2; ++qb) {
;         const int tq = tq0 + qb * 16;
;         const float inv = 1.0f / rq_sum(l_run[qb]);
;         float ss = 0.f;
; #pragma unroll
;         for (int db = 0; db < 8; ++db) { O[qb][db] *= inv; ss += (O[qb][db][0] * O[qb][db][0] + O[qb][db][1] * O[qb][db][1]) + (O[qb][db][2] * O[qb][db][2] + O[qb][db][3] * O[qb][db][3]); }
;         const float rstd = frsq(rq_sum(ss) * (1.f / HD) + EPS);
; #pragma unroll
;         for (int db = 0; db < 8; ++db) {
;             const int d0 = h * HD + db * 16 + rq * 4;
;             const f32x4 g4 = ld_f4(F.attn_g + l * 1024 + d0);
;             u32x2 o; o.x = pk2(O[qb][db][0] * rstd * g4[0], O[qb][db][1] * rstd * g4[1]); o.y = pk2(O[qb][db][2] * rstd * g4[2], O[qb][db][3] * rstd * g4[3]);
;             st_u2(MIX + (size_t)tq * D + d0, o);
	v_add_f32_e32 v32, v32, v33
	v_div_scale_f32 v33, s[0:1], v32, v32, 1.0
	v_rcp_f32_e32 v34, v33
	v_readlane_b32 s0, v250, 0
	s_add_i32 s17, s17, s0
	v_readlane_b32 s0, v250, 2
	v_fma_f32 v35, -v33, v34, 1.0
	v_fmac_f32_e32 v34, v35, v34
	v_div_scale_f32 v35, vcc, 1.0, v32, 1.0
	v_mul_f32_e32 v36, v35, v34
	v_fma_f32 v37, -v33, v36, v35
	v_fmac_f32_e32 v36, v37, v34
	v_fma_f32 v33, -v33, v36, v35
	v_div_fmas_f32 v33, v33, v34, v36
	v_div_fixup_f32 v48, v33, v32, 1.0
	v_pk_mul_f32 v[46:47], v[4:5], v[48:49] op_sel_hi:[1,0]
	v_pk_mul_f32 v[42:43], v[8:9], v[48:49] op_sel_hi:[1,0]
	v_pk_mul_f32 v[44:45], v[6:7], v[48:49] op_sel_hi:[1,0]
	v_pk_mul_f32 v[36:37], v[10:11], v[48:49] op_sel_hi:[1,0]
	v_mov_b32_e32 v6, v47
	v_mov_b32_e32 v7, v43
	v_mov_b32_e32 v4, v46
	v_mov_b32_e32 v5, v42
	v_pk_mul_f32 v[6:7], v[6:7], v[6:7]
	v_mov_b32_e32 v8, v45
	v_mov_b32_e32 v9, v37
	v_pk_fma_f32 v[4:5], v[4:5], v[4:5], v[6:7]
	v_mov_b32_e32 v6, v44
	v_mov_b32_e32 v7, v36
	v_pk_mul_f32 v[8:9], v[8:9], v[8:9]
	v_pk_mul_f32 v[40:41], v[0:1], v[48:49] op_sel_hi:[1,0]
	v_pk_mul_f32 v[38:39], v[2:3], v[48:49] op_sel_hi:[1,0]
	v_pk_fma_f32 v[6:7], v[6:7], v[6:7], v[8:9]
	v_pk_mul_f32 v[0:1], v[38:39], v[38:39]
	v_pk_mul_f32 v[2:3], v[40:41], v[40:41]
	v_pk_add_f32 v[4:5], v[4:5], v[6:7]
	v_pk_mov_b32 v[6:7], v[2:3], v[0:1] op_sel:[1,0]
	v_mov_b32_e32 v3, v1
	v_pk_add_f32 v[0:1], v[6:7], v[2:3]
	v_pk_mul_f32 v[34:35], v[12:13], v[48:49] op_sel_hi:[1,0]
	v_pk_add_f32 v[0:1], v[0:1], v[0:1] op_sel_hi:[0,1]
	v_pk_mul_f32 v[32:33], v[14:15], v[48:49] op_sel_hi:[1,0]
	v_mul_f32_e32 v0, v34, v34
	v_pk_fma_f32 v[2:3], v[34:35], v[34:35], v[0:1] op_sel_hi:[1,1,0]
	v_mul_f32_e32 v0, v32, v32
	v_pk_add_f32 v[4:5], v[4:5], v[4:5] op_sel_hi:[0,1]
	v_pk_fma_f32 v[6:7], v[32:33], v[32:33], v[0:1] op_sel_hi:[1,1,0]
	v_pk_mul_f32 v[14:15], v[18:19], v[48:49] op_sel_hi:[1,0]
	v_pk_mul_f32 v[16:17], v[16:17], v[48:49] op_sel_hi:[1,0]
	v_mul_f32_e32 v0, v14, v14
	v_mul_f32_e32 v2, v16, v16
	v_mul_f32_e32 v6, v17, v17
	v_mul_f32_e32 v4, v15, v15
	v_pk_add_f32 v[2:3], v[2:3], v[6:7]
	v_pk_add_f32 v[0:1], v[0:1], v[4:5]
	v_pk_mul_f32 v[12:13], v[20:21], v[48:49] op_sel_hi:[1,0]
	v_pk_add_f32 v[0:1], v[2:3], v[0:1]
	v_pk_mul_f32 v[10:11], v[22:23], v[48:49] op_sel_hi:[1,0]
	v_pk_add_f32 v[4:5], v[0:1], v[0:1] op_sel_hi:[0,1]
	v_pk_mul_f32 v[0:1], v[10:11], v[10:11]
	v_pk_mul_f32 v[2:3], v[12:13], v[12:13]
	v_pk_mul_f32 v[8:9], v[24:25], v[48:49] op_sel_hi:[1,0]
	v_pk_mov_b32 v[6:7], v[2:3], v[0:1] op_sel:[1,0]
	v_mov_b32_e32 v3, v1
	v_pk_add_f32 v[0:1], v[6:7], v[2:3]
	v_pk_mul_f32 v[6:7], v[26:27], v[48:49] op_sel_hi:[1,0]
	v_pk_add_f32 v[18:19], v[0:1], v[0:1] op_sel_hi:[0,1]
	v_mul_f32_e32 v0, v8, v8
	v_pk_fma_f32 v[20:21], v[8:9], v[8:9], v[0:1] op_sel_hi:[1,1,0]
	v_mul_f32_e32 v0, v6, v6
	v_pk_fma_f32 v[22:23], v[6:7], v[6:7], v[0:1] op_sel_hi:[1,1,0]
	v_pk_mul_f32 v[0:1], v[30:31], v[48:49] op_sel_hi:[1,0]
	v_pk_mul_f32 v[2:3], v[28:29], v[48:49] op_sel_hi:[1,0]
	v_mul_f32_e32 v18, v0, v0
	v_mul_f32_e32 v20, v2, v2
	v_mul_f32_e32 v22, v3, v3
	v_mul_f32_e32 v4, v1, v1
	v_pk_add_f32 v[20:21], v[20:21], v[22:23]
	v_pk_add_f32 v[4:5], v[18:19], v[4:5]
	v_mov_b32_e32 v24, v46
	v_pk_add_f32 v[4:5], v[20:21], v[4:5]
	v_mov_b32_e32 v20, v96
	v_mov_b32_e32 v21, v97
	v_mov_b32_e32 v22, v98
	v_mov_b32_e32 v23, v99
	v_add_f32_e32 v4, v4, v5
	ds_bpermute_b32 v5, v202, v4
	v_mov_b32_e32 v25, v44
	v_mov_b32_e32 v44, v47
	v_lshlrev_b64 v[18:19], 12, v[148:149]
	v_lshl_add_u64 v[18:19], s[2:3], 0, v[18:19]
	s_waitcnt lgkmcnt(0)
	v_add_f32_e32 v4, v4, v5
	ds_bpermute_b32 v5, v203, v4
	v_lshl_add_u64 v[18:19], v[18:19], 0, v[184:185]
	s_add_i32 s16, s16, s0
	s_cmpk_lt_i32 s18, 0x200
	s_waitcnt lgkmcnt(0)
	v_add_f32_e32 v4, v4, v5
	v_fmamk_f32 v4, v4, 0x3c000000, v214
	v_rsq_f32_e32 v4, v4
	v_mov_b32_e32 v26, v20
	v_pk_mul_f32 v[24:25], v[24:25], v[4:5] op_sel_hi:[1,0]
	v_mov_b32_e32 v27, v22
	v_pk_mul_f32 v[24:25], v[26:27], v[24:25]
	v_pk_mul_f32 v[26:27], v[44:45], v[4:5] op_sel_hi:[1,0]
	v_mov_b32_e32 v22, v21
	v_pk_mul_f32 v[20:21], v[22:23], v[26:27]
	v_and_b32_sdwa v22, v24, v213 dst_sel:DWORD dst_unused:UNUSED_PAD src0_sel:WORD_1 src1_sel:DWORD
	v_add3_u32 v22, v24, v22, s76
	v_and_b32_sdwa v23, v21, v213 dst_sel:DWORD dst_unused:UNUSED_PAD src0_sel:WORD_1 src1_sel:DWORD
	v_and_b32_sdwa v24, v20, v213 dst_sel:DWORD dst_unused:UNUSED_PAD src0_sel:WORD_1 src1_sel:DWORD
	v_and_b32_sdwa v5, v25, v213 dst_sel:DWORD dst_unused:UNUSED_PAD src0_sel:WORD_1 src1_sel:DWORD
	v_add3_u32 v21, v21, v23, s76
	v_add3_u32 v20, v20, v24, s76
	v_add3_u32 v5, v25, v5, s76
	v_and_b32_e32 v21, 0xffff0000, v21
	v_and_b32_e32 v20, 0xffff0000, v20
	v_or_b32_sdwa v21, v21, v5 dst_sel:DWORD dst_unused:UNUSED_PAD src0_sel:DWORD src1_sel:WORD_1
	v_or_b32_sdwa v20, v20, v22 dst_sel:DWORD dst_unused:UNUSED_PAD src0_sel:DWORD src1_sel:WORD_1
	global_store_dwordx2 v[18:19], v[20:21], off
	v_mov_b32_e32 v20, v100
	v_mov_b32_e32 v21, v101
	v_mov_b32_e32 v22, v102
	v_mov_b32_e32 v23, v103
	v_mov_b32_e32 v24, v42
	v_mov_b32_e32 v25, v36
	v_pk_mul_f32 v[24:25], v[24:25], v[4:5] op_sel_hi:[1,0]
	v_mov_b32_e32 v36, v43
	v_mov_b32_e32 v26, v20
	v_mov_b32_e32 v27, v22
	v_pk_mul_f32 v[24:25], v[26:27], v[24:25]
	v_pk_mul_f32 v[26:27], v[36:37], v[4:5] op_sel_hi:[1,0]
	v_mov_b32_e32 v22, v21
	v_pk_mul_f32 v[20:21], v[22:23], v[26:27]
	v_and_b32_sdwa v22, v24, v213 dst_sel:DWORD dst_unused:UNUSED_PAD src0_sel:WORD_1 src1_sel:DWORD
	v_add3_u32 v22, v24, v22, s76
	v_and_b32_sdwa v23, v21, v213 dst_sel:DWORD dst_unused:UNUSED_PAD src0_sel:WORD_1 src1_sel:DWORD
	v_and_b32_sdwa v24, v20, v213 dst_sel:DWORD dst_unused:UNUSED_PAD src0_sel:WORD_1 src1_sel:DWORD
; __device__ __forceinline__ unsigned pk2(float lo, float hi) { return f2bf(lo) | (f2bf(hi) << 16); }
; __device__ __forceinline__ void attn_wg_task(const Frame& F, int l, int task) {
;     ...
;         for (int db = 0; db < 8; ++db) {
;             const int d0 = h * HD + db * 16 + rq * 4;
;             const f32x4 g4 = ld_f4(F.attn_g + l * 1024 + d0);
;             u32x2 o; o.x = pk2(O[qb][db][0] * rstd * g4[0], O[qb][db][1] * rstd * g4[1]); o.y = pk2(O[qb][db][2] * rstd * g4[2], O[qb][db][3] * rstd * g4[3]);
;             st_u2(MIX + (size_t)tq * D + d0, o);
	v_and_b32_sdwa v5, v25, v213 dst_sel:DWORD dst_unused:UNUSED_PAD src0_sel:WORD_1 src1_sel:DWORD
	v_add3_u32 v21, v21, v23, s76
	v_add3_u32 v20, v20, v24, s76
	v_add3_u32 v5, v25, v5, s76
	v_and_b32_e32 v21, 0xffff0000, v21
	v_and_b32_e32 v20, 0xffff0000, v20
	v_or_b32_sdwa v21, v21, v5 dst_sel:DWORD dst_unused:UNUSED_PAD src0_sel:DWORD src1_sel:WORD_1
	v_or_b32_sdwa v20, v20, v22 dst_sel:DWORD dst_unused:UNUSED_PAD src0_sel:DWORD src1_sel:WORD_1
	global_store_dwordx2 v[18:19], v[20:21], off offset:32
	v_mov_b32_e32 v20, v104
	v_mov_b32_e32 v21, v105
	v_mov_b32_e32 v22, v106
	v_mov_b32_e32 v23, v107
	v_mov_b32_e32 v24, v40
	v_mov_b32_e32 v25, v38
	v_pk_mul_f32 v[24:25], v[24:25], v[4:5] op_sel_hi:[1,0]
	v_mov_b32_e32 v38, v41
	v_mov_b32_e32 v26, v20
	v_mov_b32_e32 v27, v22
	v_pk_mul_f32 v[24:25], v[26:27], v[24:25]
	v_pk_mul_f32 v[26:27], v[38:39], v[4:5] op_sel_hi:[1,0]
	v_mov_b32_e32 v22, v21
	v_pk_mul_f32 v[20:21], v[22:23], v[26:27]
	v_and_b32_sdwa v22, v24, v213 dst_sel:DWORD dst_unused:UNUSED_PAD src0_sel:WORD_1 src1_sel:DWORD
	v_add3_u32 v22, v24, v22, s76
	v_and_b32_sdwa v23, v21, v213 dst_sel:DWORD dst_unused:UNUSED_PAD src0_sel:WORD_1 src1_sel:DWORD
	v_and_b32_sdwa v24, v20, v213 dst_sel:DWORD dst_unused:UNUSED_PAD src0_sel:WORD_1 src1_sel:DWORD
	v_and_b32_sdwa v5, v25, v213 dst_sel:DWORD dst_unused:UNUSED_PAD src0_sel:WORD_1 src1_sel:DWORD
	v_add3_u32 v21, v21, v23, s76
	v_add3_u32 v20, v20, v24, s76
	v_add3_u32 v5, v25, v5, s76
	v_and_b32_e32 v21, 0xffff0000, v21
	v_and_b32_e32 v20, 0xffff0000, v20
	v_or_b32_sdwa v21, v21, v5 dst_sel:DWORD dst_unused:UNUSED_PAD src0_sel:DWORD src1_sel:WORD_1
	v_or_b32_sdwa v20, v20, v22 dst_sel:DWORD dst_unused:UNUSED_PAD src0_sel:DWORD src1_sel:WORD_1
	global_store_dwordx2 v[18:19], v[20:21], off offset:64
	v_mov_b32_e32 v20, v108
	v_mov_b32_e32 v21, v109
	v_mov_b32_e32 v22, v110
	v_mov_b32_e32 v23, v111
	v_mov_b32_e32 v24, v34
	v_mov_b32_e32 v25, v32
	v_pk_mul_f32 v[24:25], v[24:25], v[4:5] op_sel_hi:[1,0]
	v_mov_b32_e32 v32, v35
	v_mov_b32_e32 v26, v20
	v_mov_b32_e32 v27, v22
	v_pk_mul_f32 v[24:25], v[26:27], v[24:25]
	v_pk_mul_f32 v[26:27], v[32:33], v[4:5] op_sel_hi:[1,0]
	v_mov_b32_e32 v22, v21
	v_pk_mul_f32 v[20:21], v[22:23], v[26:27]
	v_and_b32_sdwa v22, v24, v213 dst_sel:DWORD dst_unused:UNUSED_PAD src0_sel:WORD_1 src1_sel:DWORD
	v_add3_u32 v22, v24, v22, s76
	v_and_b32_sdwa v23, v21, v213 dst_sel:DWORD dst_unused:UNUSED_PAD src0_sel:WORD_1 src1_sel:DWORD
	v_and_b32_sdwa v24, v20, v213 dst_sel:DWORD dst_unused:UNUSED_PAD src0_sel:WORD_1 src1_sel:DWORD
	v_and_b32_sdwa v5, v25, v213 dst_sel:DWORD dst_unused:UNUSED_PAD src0_sel:WORD_1 src1_sel:DWORD
	v_add3_u32 v21, v21, v23, s76
	v_add3_u32 v20, v20, v24, s76
	v_add3_u32 v5, v25, v5, s76
	v_and_b32_e32 v21, 0xffff0000, v21
	v_and_b32_e32 v20, 0xffff0000, v20
	v_or_b32_sdwa v21, v21, v5 dst_sel:DWORD dst_unused:UNUSED_PAD src0_sel:DWORD src1_sel:WORD_1
	v_or_b32_sdwa v20, v20, v22 dst_sel:DWORD dst_unused:UNUSED_PAD src0_sel:DWORD src1_sel:WORD_1
	global_store_dwordx2 v[18:19], v[20:21], off offset:96
	v_mov_b32_e32 v20, v112
	v_mov_b32_e32 v21, v113
	v_mov_b32_e32 v22, v114
	v_mov_b32_e32 v23, v115
	v_mov_b32_e32 v25, v14
	v_mov_b32_e32 v14, v17
	v_mov_b32_e32 v24, v16
	v_pk_mul_f32 v[14:15], v[14:15], v[4:5] op_sel_hi:[1,0]
	v_pk_mul_f32 v[24:25], v[24:25], v[4:5] op_sel_hi:[1,0]
	v_mov_b32_e32 v27, v22
	v_mov_b32_e32 v22, v21
	v_mov_b32_e32 v26, v20
	v_pk_mul_f32 v[14:15], v[22:23], v[14:15]
	v_pk_mul_f32 v[24:25], v[26:27], v[24:25]
	v_and_b32_sdwa v17, v15, v213 dst_sel:DWORD dst_unused:UNUSED_PAD src0_sel:WORD_1 src1_sel:DWORD
	v_and_b32_sdwa v20, v14, v213 dst_sel:DWORD dst_unused:UNUSED_PAD src0_sel:WORD_1 src1_sel:DWORD
	v_and_b32_sdwa v5, v25, v213 dst_sel:DWORD dst_unused:UNUSED_PAD src0_sel:WORD_1 src1_sel:DWORD
	v_and_b32_sdwa v16, v24, v213 dst_sel:DWORD dst_unused:UNUSED_PAD src0_sel:WORD_1 src1_sel:DWORD
	v_add3_u32 v15, v15, v17, s76
	v_add3_u32 v14, v14, v20, s76
	v_add3_u32 v16, v24, v16, s76
	v_add3_u32 v5, v25, v5, s76
	v_and_b32_e32 v15, 0xffff0000, v15
	v_and_b32_e32 v14, 0xffff0000, v14
	v_or_b32_sdwa v15, v15, v5 dst_sel:DWORD dst_unused:UNUSED_PAD src0_sel:DWORD src1_sel:WORD_1
	v_or_b32_sdwa v14, v14, v16 dst_sel:DWORD dst_unused:UNUSED_PAD src0_sel:DWORD src1_sel:WORD_1
	global_store_dwordx2 v[18:19], v[14:15], off offset:128
	v_mov_b32_e32 v14, v116
	v_mov_b32_e32 v15, v117
	v_mov_b32_e32 v16, v118
	v_mov_b32_e32 v17, v119
	v_mov_b32_e32 v21, v10
	v_mov_b32_e32 v10, v13
	v_mov_b32_e32 v20, v12
	v_pk_mul_f32 v[10:11], v[10:11], v[4:5] op_sel_hi:[1,0]
	v_pk_mul_f32 v[20:21], v[20:21], v[4:5] op_sel_hi:[1,0]
	v_mov_b32_e32 v23, v16
	v_mov_b32_e32 v16, v15
	v_mov_b32_e32 v22, v14
	v_pk_mul_f32 v[10:11], v[16:17], v[10:11]
	v_pk_mul_f32 v[20:21], v[22:23], v[20:21]
	v_and_b32_sdwa v13, v11, v213 dst_sel:DWORD dst_unused:UNUSED_PAD src0_sel:WORD_1 src1_sel:DWORD
	v_and_b32_sdwa v14, v10, v213 dst_sel:DWORD dst_unused:UNUSED_PAD src0_sel:WORD_1 src1_sel:DWORD
	v_and_b32_sdwa v5, v21, v213 dst_sel:DWORD dst_unused:UNUSED_PAD src0_sel:WORD_1 src1_sel:DWORD
	v_and_b32_sdwa v12, v20, v213 dst_sel:DWORD dst_unused:UNUSED_PAD src0_sel:WORD_1 src1_sel:DWORD
	v_add3_u32 v11, v11, v13, s76
	v_add3_u32 v10, v10, v14, s76
	v_add3_u32 v12, v20, v12, s76
	v_add3_u32 v5, v21, v5, s76
	v_and_b32_e32 v11, 0xffff0000, v11
	v_and_b32_e32 v10, 0xffff0000, v10
	v_or_b32_sdwa v11, v11, v5 dst_sel:DWORD dst_unused:UNUSED_PAD src0_sel:DWORD src1_sel:WORD_1
	v_or_b32_sdwa v10, v10, v12 dst_sel:DWORD dst_unused:UNUSED_PAD src0_sel:DWORD src1_sel:WORD_1
	global_store_dwordx2 v[18:19], v[10:11], off offset:160
	v_mov_b32_e32 v10, v120
; __device__ __forceinline__ unsigned pk2(float lo, float hi) { return f2bf(lo) | (f2bf(hi) << 16); }
; __device__ __forceinline__ void attn_wg_task(const Frame& F, int l, int task) {
;     ...
;         for (int db = 0; db < 8; ++db) {
;             const int d0 = h * HD + db * 16 + rq * 4;
;             const f32x4 g4 = ld_f4(F.attn_g + l * 1024 + d0);
;             u32x2 o; o.x = pk2(O[qb][db][0] * rstd * g4[0], O[qb][db][1] * rstd * g4[1]); o.y = pk2(O[qb][db][2] * rstd * g4[2], O[qb][db][3] * rstd * g4[3]);
;             st_u2(MIX + (size_t)tq * D + d0, o);
;         }
	v_mov_b32_e32 v11, v121
	v_mov_b32_e32 v12, v122
	v_mov_b32_e32 v13, v123
	v_mov_b32_e32 v15, v6
	v_mov_b32_e32 v6, v9
	v_mov_b32_e32 v14, v8
	v_pk_mul_f32 v[6:7], v[6:7], v[4:5] op_sel_hi:[1,0]
	v_pk_mul_f32 v[14:15], v[14:15], v[4:5] op_sel_hi:[1,0]
	v_mov_b32_e32 v17, v12
	v_mov_b32_e32 v12, v11
	v_mov_b32_e32 v16, v10
	v_pk_mul_f32 v[6:7], v[12:13], v[6:7]
	v_pk_mul_f32 v[14:15], v[16:17], v[14:15]
	v_and_b32_sdwa v9, v7, v213 dst_sel:DWORD dst_unused:UNUSED_PAD src0_sel:WORD_1 src1_sel:DWORD
	v_and_b32_sdwa v10, v6, v213 dst_sel:DWORD dst_unused:UNUSED_PAD src0_sel:WORD_1 src1_sel:DWORD
	v_and_b32_sdwa v5, v15, v213 dst_sel:DWORD dst_unused:UNUSED_PAD src0_sel:WORD_1 src1_sel:DWORD
	v_and_b32_sdwa v8, v14, v213 dst_sel:DWORD dst_unused:UNUSED_PAD src0_sel:WORD_1 src1_sel:DWORD
	v_add3_u32 v7, v7, v9, s76
	v_add3_u32 v6, v6, v10, s76
	v_add3_u32 v8, v14, v8, s76
	v_add3_u32 v5, v15, v5, s76
	v_and_b32_e32 v7, 0xffff0000, v7
	v_and_b32_e32 v6, 0xffff0000, v6
	v_or_b32_sdwa v7, v7, v5 dst_sel:DWORD dst_unused:UNUSED_PAD src0_sel:DWORD src1_sel:WORD_1
	v_or_b32_sdwa v6, v6, v8 dst_sel:DWORD dst_unused:UNUSED_PAD src0_sel:DWORD src1_sel:WORD_1
	global_store_dwordx2 v[18:19], v[6:7], off offset:192
	v_mov_b32_e32 v6, v124
	v_mov_b32_e32 v7, v125
	v_mov_b32_e32 v8, v126
	v_mov_b32_e32 v9, v127
	v_mov_b32_e32 v11, v0
	v_mov_b32_e32 v0, v3
	v_mov_b32_e32 v10, v2
	v_pk_mul_f32 v[0:1], v[0:1], v[4:5] op_sel_hi:[1,0]
	v_pk_mul_f32 v[10:11], v[10:11], v[4:5] op_sel_hi:[1,0]
	v_mov_b32_e32 v13, v8
	v_mov_b32_e32 v8, v7
	v_mov_b32_e32 v12, v6
	v_pk_mul_f32 v[0:1], v[8:9], v[0:1]
	v_pk_mul_f32 v[10:11], v[12:13], v[10:11]
	v_and_b32_sdwa v4, v1, v213 dst_sel:DWORD dst_unused:UNUSED_PAD src0_sel:WORD_1 src1_sel:DWORD
	v_and_b32_sdwa v5, v0, v213 dst_sel:DWORD dst_unused:UNUSED_PAD src0_sel:WORD_1 src1_sel:DWORD
	v_and_b32_sdwa v2, v11, v213 dst_sel:DWORD dst_unused:UNUSED_PAD src0_sel:WORD_1 src1_sel:DWORD
	v_and_b32_sdwa v3, v10, v213 dst_sel:DWORD dst_unused:UNUSED_PAD src0_sel:WORD_1 src1_sel:DWORD
	v_add3_u32 v1, v1, v4, s76
	v_add3_u32 v0, v0, v5, s76
	v_add3_u32 v3, v10, v3, s76
	v_add3_u32 v2, v11, v2, s76
	v_and_b32_e32 v1, 0xffff0000, v1
	v_and_b32_e32 v0, 0xffff0000, v0
	v_or_b32_sdwa v1, v1, v2 dst_sel:DWORD dst_unused:UNUSED_PAD src0_sel:DWORD src1_sel:WORD_1
	v_or_b32_sdwa v0, v0, v3 dst_sel:DWORD dst_unused:UNUSED_PAD src0_sel:DWORD src1_sel:WORD_1
	global_store_dwordx2 v[18:19], v[0:1], off offset:224
	s_cbranch_scc0 .LBB0_479
; #define GAS __attribute__((address_space(1)))
; #define LAS __attribute__((address_space(3)))
; __device__ __forceinline__ void attn_wg_task(const Frame& F, int l, int task) {
;     int tid = F.wave * 64 + lane_id(); asm volatile("" : "+v"(tid));
;     const int lane = tid & 63, c = lane & 15, rq = lane >> 4, wave = F.wave;
;     const int cq = task & 7, h = (task >> 3) & 7, b = task >> 6;
;     const bf16* TOK = (const bf16*)(F.ws + WS_TOK); const bf16* SWP = (const bf16*)(F.ws + WS_SWP); const float* SSQ = (const float*)(F.ws + WS_SSQ);
;     bf16* MIX = (bf16*)(F.ws + WS_MIX);
;     LAS unsigned char* lds = F.lds + RING_OFF;
;     const LAS float* bh = (const LAS float*)(lds + A_BIAS) + h * 257;
;     const int wch = wave >> 1;
;     const int qi0 = (wave & 1) * 32 + c;
;     const int tq0 = b * S + (4 * cq + wch) * CH + qi0;
;     bf16x8 Qf[2][4];
; #pragma unroll
;     for (int qb = 0; qb < 2; ++qb) {
;         const int tq = tq0 + qb * 16;
;         float ssq = 0.f;
; #pragma unroll
;         for (int w = 0; w < 4; ++w) ssq += *(const GAS float*)(SSQ + (size_t)((0 * 8 + h) * 4 + w) * T + tq);
;         const float rs = frsq(ssq * (1.f / HD) + EPS) * (pg8::KSCALE * LOG2E);
; #pragma unroll
;         for (int ks = 0; ks < 4; ++ks) {
;             const float* gp = F.qa_g + l * HD + ks * 32 + rq * 8; const float* kp = F.ka_g + l * HD + ks * 32 + rq * 8;
;             const f32x4 a0 = ld_f4(gp), a1 = ld_f4(gp + 4), b0 = ld_f4(kp), b1 = ld_f4(kp + 4);
;             const u32x4 raw = ld_u4(TOK + (size_t)tq * TOKP + TK_QA + h * HD + ks * 32 + rq * 8);
;             u32x4 o;
;             o.x = pk2(bf_lo(raw.x) * rs * (a0[0] * b0[0]), bf_hi(raw.x) * rs * (a0[1] * b0[1])); o.y = pk2(bf_lo(raw.y) * rs * (a0[2] * b0[2]), bf_hi(raw.y) * rs * (a0[3] * b0[3]));
;             o.z = pk2(bf_lo(raw.z) * rs * (a1[0] * b1[0]), bf_hi(raw.z) * rs * (a1[1] * b1[1])); o.w = pk2(bf_lo(raw.w) * rs * (a1[2] * b1[2]), bf_hi(raw.w) * rs * (a1[3] * b1[3]));
;             Qf[qb][ks] = __builtin_bit_cast(bf16x8, o);
;         }
;     }
;     float m_run[2] = {-1e30f, -1e30f}, l_run[2] = {0.f, 0.f};
;     f32x4 O[2][8];
; #pragma unroll
;     for (int qb = 0; qb < 2; ++qb)
; #pragma unroll
;         for (int db = 0; db < 8; ++db) O[qb][db] = (f32x4){0.f, 0.f, 0.f, 0.f};
;     const int p0 = tid, p1 = tid + 512;
;     const int kr0 = p0 >> 4, kr1 = p1 >> 4;
.LBB0_550:
	s_lshl_b32 s1, s18, 2
	s_and_b32 s22, s1, 28
	s_lshl_b32 s0, s18, 5
	s_add_i32 s1, s22, s25
	s_waitcnt vmcnt(0)
	v_mov_b32_e32 v116, v212
	s_bfe_u32 s20, s18, 0x30003
	s_and_b32 s0, s0, 0xfffff800
	s_lshl_b32 s1, s1, 6
	s_add_i32 s1, s1, s0
	v_and_b32_e32 v117, 15, v116
	s_lshl_b32 s19, s20, 7
	s_lshl_b32 s96, s20, 8
	v_or_b32_e32 v207, s66, v117
	s_add_u32 s2, s80, s96
	v_or_b32_e32 v152, s1, v207
	s_addc_u32 s3, s81, 0
	v_and_b32_e32 v184, 48, v116
	s_waitcnt lgkmcnt(0)
	v_lshl_add_u64 v[0:1], s[2:3], 0, v[184:185]
	v_ashrrev_i32_e32 v153, 31, v152
	s_lshl_b32 s2, s20, 18
	v_bfe_u32 v204, v116, 4, 2
	v_lshl_add_u64 v[2:3], v[152:153], 2, s[88:89]
	s_mov_b32 s3, s97
	s_or_b32 s4, s2, 0x10000
	s_mov_b32 s5, s97
	s_or_b32 s12, s2, 0x20000
	s_mov_b32 s13, s97
	s_or_b32 s14, s2, 0x30000
	s_mov_b32 s15, s97
	v_lshlrev_b32_e32 v206, 5, v204
	v_lshl_add_u64 v[4:5], v[2:3], 0, s[2:3]
	v_lshl_add_u64 v[6:7], v[2:3], 0, s[4:5]
	v_lshl_add_u64 v[8:9], v[2:3], 0, s[12:13]
	v_lshl_add_u64 v[2:3], v[2:3], 0, s[14:15]
	s_movk_i32 s1, 0x2900
	global_load_dword v123, v[4:5], off
	global_load_dword v124, v[6:7], off
	global_load_dword v125, v[8:9], off
	global_load_dword v126, v[2:3], off
	v_mad_i64_i32 v[2:3], s[8:9], v152, s1, v[0:1]
	global_load_dwordx4 v[84:87], v206, s[38:39] offset:16
	global_load_dwordx4 v[92:95], v206, s[38:39]
	global_load_dwordx4 v[88:91], v206, s[40:41] offset:16
	global_load_dwordx4 v[96:99], v206, s[40:41]
	global_load_dwordx4 v[56:59], v206, s[38:39] offset:144
	global_load_dwordx4 v[72:75], v206, s[38:39] offset:128
	global_load_dwordx4 v[60:63], v206, s[40:41] offset:144
	global_load_dwordx4 v[76:79], v206, s[40:41] offset:128
	global_load_dwordx4 v[80:83], v[2:3], off
	global_load_dwordx4 v[52:55], v[2:3], off offset:64
	global_load_dwordx4 v[32:35], v206, s[38:39] offset:272
	global_load_dwordx4 v[40:43], v206, s[38:39] offset:256
	global_load_dwordx4 v[36:39], v206, s[40:41] offset:272
	global_load_dwordx4 v[44:47], v206, s[40:41] offset:256
	global_load_dwordx4 v[8:11], v206, s[38:39] offset:400
	global_load_dwordx4 v[16:19], v206, s[38:39] offset:384
	s_waitcnt lgkmcnt(0)
	global_load_dwordx4 v[12:15], v206, s[40:41] offset:400
	global_load_dwordx4 v[20:23], v206, s[40:41] offset:384
	global_load_dwordx4 v[28:31], v[2:3], off offset:128
	global_load_dwordx4 v[4:7], v[2:3], off offset:192
	v_add_u32_e32 v110, 0x200, v116
	v_or_b32_e32 v148, 16, v152
	v_ashrrev_i32_e32 v118, 4, v116
	v_ashrrev_i32_e32 v119, 4, v110
	v_ashrrev_i32_e32 v149, 31, v148
	s_waitcnt vmcnt(35)
	v_add_u32_e32 v64, s0, v118
	s_waitcnt vmcnt(34)
	v_mov_b64_e32 v[70:71], s[80:81]
	v_add_u32_e32 v102, s0, v119
	v_lshlrev_b64 v[2:3], 2, v[148:149]
	s_add_u32 s8, s88, s2
	v_mad_i64_i32 v[64:65], s[2:3], v64, s1, v[70:71]
	v_mad_i64_i32 v[70:71], s[2:3], v102, s1, v[70:71]
	v_lshl_add_u64 v[24:25], s[88:89], 0, v[2:3]
	v_lshl_add_u64 v[100:101], v[64:65], 0, s[96:97]
	v_lshlrev_b32_e32 v64, 4, v117
	v_mov_b32_e32 v65, v185
	v_lshl_add_u64 v[70:71], v[70:71], 0, s[96:97]
	v_ashrrev_i32_e32 v121, 3, v116
	v_lshl_add_u64 v[26:27], v[24:25], 0, s[4:5]
	v_lshl_add_u64 v[100:101], v[100:101], 0, v[64:65]
	v_lshl_add_u64 v[102:103], v[70:71], 0, v[64:65]
	v_add_u32_e32 v65, s19, v121
	v_mov_b64_e32 v[104:105], s[64:65]
	s_mov_b32 s4, 0x8100
	s_addc_u32 s9, s89, 0
	v_mad_i64_i32 v[0:1], s[2:3], v148, s1, v[0:1]
	v_mad_i64_i32 v[70:71], s[2:3], v65, s4, v[104:105]
	s_ashr_i32 s1, s0, 31
	s_lshl_b64 s[2:3], s[0:1], 1
	v_and_b32_e32 v65, 7, v116
	v_ashrrev_i32_e32 v120, 3, v110
	v_lshl_add_u64 v[106:107], v[70:71], 0, s[2:3]
	v_lshlrev_b32_e32 v70, 4, v65
	v_add_u32_e32 v65, s19, v120
	v_mad_i64_i32 v[104:105], s[4:5], v65, s4, v[104:105]
	v_sub_u32_e64 v65, 8, s22 clamp
	v_lshl_add_u64 v[104:105], v[104:105], 0, s[2:3]
	v_readfirstlane_b32 s21, v65
	s_add_i32 s22, s22, s21
	s_lshl_b32 s2, s22, 6
	s_waitcnt vmcnt(33)
	v_lshl_add_u64 v[48:49], v[24:25], 0, s[12:13]
	s_add_i32 s12, s2, 0xfffffe00
	v_lshl_add_u64 v[2:3], s[8:9], 0, v[2:3]
	v_lshl_add_u64 v[24:25], v[24:25], 0, s[14:15]
	v_mov_b32_e32 v71, v185
	s_ashr_i32 s13, s12, 31
	v_mad_i64_i32 v[100:101], s[2:3], s12, v223, v[100:101]
	v_mad_i64_i32 v[102:103], s[2:3], s12, v223, v[102:103]
	global_load_dword v127, v[2:3], off
	global_load_dword v128, v[26:27], off
	global_load_dword v129, v[48:49], off
	global_load_dword v130, v[24:25], off
	global_load_dwordx4 v[66:69], v[0:1], off
	s_nop 0
	global_load_dwordx4 v[48:51], v[0:1], off offset:64
	global_load_dwordx4 v[24:27], v[0:1], off offset:128
	s_nop 0
	global_load_dwordx4 v[0:3], v[0:1], off offset:192
	v_lshl_add_u64 v[108:109], v[106:107], 0, v[70:71]
	v_lshl_add_u64 v[110:111], v[104:105], 0, v[70:71]
	s_lshl_b64 s[2:3], s[12:13], 1
	v_lshl_add_u64 v[108:109], v[108:109], 0, s[2:3]
	v_lshl_add_u64 v[110:111], v[110:111], 0, s[2:3]
	s_barrier
	global_load_dwordx4 v[104:107], v[100:101], off offset:2048
	s_nop 0
	global_load_dwordx4 v[100:103], v[102:103], off offset:2048
	s_nop 0
	global_load_dwordx4 v[112:115], v[108:109], off
	s_nop 0
	global_load_dwordx4 v[108:111], v[110:111], off
	v_and_b32_e32 v122, 63, v116
	v_mov_b32_e32 v228, 0
	v_cmp_gt_i32_e64 s[34:35], 64, v116
	s_and_saveexec_b64 s[2:3], s[34:35]
	s_cbranch_execz .LBB0_552
	s_lshl_b64 s[0:1], s[0:1], 2
	s_add_u32 s0, s8, s0
	s_addc_u32 s1, s9, s1
	s_waitcnt vmcnt(44)
	v_lshlrev_b32_e32 v132, 2, v122
	v_mov_b32_e32 v133, v185
	v_lshl_add_u64 v[132:133], s[0:1], 0, v[132:133]
	v_lshl_add_u64 v[132:133], s[12:13], 2, v[132:133]
	v_add_co_u32_e32 v134, vcc, 0x200000, v132
	s_nop 1
	v_addc_co_u32_e32 v135, vcc, 0, v133, vcc
	global_load_dword v65, v[134:135], off
	v_add_co_u32_e32 v134, vcc, 0x210000, v132
	s_nop 1
	v_addc_co_u32_e32 v135, vcc, 0, v133, vcc
	global_load_dword v71, v[134:135], off
	v_add_co_u32_e32 v134, vcc, 0x220000, v132
	s_nop 1
	v_addc_co_u32_e32 v135, vcc, 0, v133, vcc
	global_load_dword v240, v[134:135], off
	v_add_co_u32_e32 v132, vcc, 0x230000, v132
	s_nop 1
	v_addc_co_u32_e32 v133, vcc, 0, v133, vcc
	global_load_dword v241, v[132:133], off
	s_waitcnt vmcnt(0)
	v_add_f32_e32 v65, 0, v65
	v_add_f32_e32 v65, v65, v71
	s_nop 0
	v_add_f32_e32 v65, v65, v240
	s_nop 0
	v_add_f32_e32 v65, v65, v241
	v_fmamk_f32 v65, v65, 0x3c000000, v214
	v_rsq_f32_e32 v228, v65

; #define A_LSTORE(bf) do { *(LAS u32x4*)(lds + lk0 + (bf) * 64 * A_KP) = r0; *(LAS u32x4*)(lds + lk1 + (bf) * 64 * A_KP) = r1; *(LAS u32x4*)(lds + lv0 + (bf) * 128 * A_VP) = r2; *(LAS u32x4*)(lds + lv1 + (bf) * 128 * A_VP) = r3; \
;         if (tid < 64) ((LAS float*)(lds + A_RK))[(bf) * 64 + tid] = rkv; } while (0)
; __device__ __forceinline__ void attn_wg_task(const Frame& F, int l, int task) {
;     ...
;         if (j < 11) A_LSTORE((j + 1) & 1);
;         __syncthreads();
.LBB0_566:
	s_xor_b32 s3, s3, 1
	s_mul_i32 s0, s3, 0x4400
	v_add_u32_e32 v112, s0, v209
	s_waitcnt vmcnt(3)
	ds_write_b128 v112, v[104:107]
	v_add_u32_e32 v104, s0, v210
	s_mul_i32 s0, s3, 0x4800
	s_waitcnt vmcnt(2)
	ds_write_b128 v104, v[96:99]
	v_add_u32_e32 v96, s0, v226
	s_waitcnt vmcnt(1)
	ds_write_b128 v96, v[108:111] offset:34816
	v_add_u32_e32 v96, s0, v227
	s_waitcnt vmcnt(0)
	ds_write_b128 v96, v[100:103] offset:34816
	s_and_saveexec_b64 s[0:1], s[34:35]
	v_add_f32_e32 v240, 0, v240
	v_lshl_add_u32 v96, s3, 8, v230
	v_add_f32_e32 v240, v240, v241
	s_nop 0
	v_add_f32_e32 v240, v240, v242
	s_nop 0
	v_add_f32_e32 v240, v240, v243
	s_nop 0
	v_fmamk_f32 v240, v240, 0x3c000000, v214
	s_nop 0
	v_rsq_f32_e32 v228, v240
	s_nop 1
	ds_write_b32 v96, v228
	s_or_b64 exec, exec, s[0:1]
	s_sub_i32 s2, s2, 64
	s_add_i32 s21, s21, 1
	s_add_i32 s0, s22, s2
	s_mov_b64 s[4:5], 0xa4000
	v_lshl_add_u64 v[154:155], v[154:155], 0, s[46:47]
	v_lshl_add_u64 v[156:157], v[156:157], 0, s[46:47]
	v_lshl_add_u64 v[158:159], v[158:159], 0, s[44:45]
	v_lshl_add_u64 v[160:161], v[160:161], 0, s[4:5]
	s_cmpk_eq_i32 s0, 0xff40
	v_lshl_add_u64 v[162:163], v[162:163], 0, s[4:5]
	s_waitcnt lgkmcnt(0)
	s_barrier
	s_cbranch_scc1 .LBB0_570
	v_mov_b32_e32 v233, v130
	s_branch .LBB0_555

; __device__ __forceinline__ f32x4 mfma16(bf16x8 a, bf16x8 b, f32x4 c) { return __builtin_amdgcn_mfma_f32_16x16x32_bf16(a, b, c, 0, 0, 0); }
; __device__ __forceinline__ float fexp2(float x) { return __builtin_amdgcn_exp2f(x); }
; __device__ __forceinline__ void ret_task(const Frame& F, int l, int task) {
;     ...
;     const int qb2 = task & 1, n = (task >> 1) & 31, h = (task >> 6) & 7, b = task >> 9, bhh = b * NH + h;
;     const bf16* TOK = (const bf16*)(F.ws + WS_TOK); const bf16* SWP = (const bf16*)(F.ws + WS_SWP); const bf16* ST = (const bf16*)(F.ws + WS_ST);
;     bf16* MIX = (bf16*)(F.ws + WS_MIX);
;     const int tc0 = b * S + n * CH, tq0 = tc0 + qb2 * 32;
;     const float lg = pg8::lg2gamma(h);
;     bf16x8 Qf[2][4], Kf[2][2][4];
; #pragma unroll
;     for (int qb = 0; qb < 2; ++qb)
; #pragma unroll
;         for (int ks = 0; ks < 4; ++ks) Qf[qb][ks] = ld_b8(TOK + (size_t)(tq0 + qb * 16 + c) * TOKP + TK_QR + h * HD + ks * 32 + rq * 8);
; #pragma unroll
;     for (int g = 0; g < 2; ++g)
; #pragma unroll
;         for (int ab = 0; ab < 2; ++ab) { const int key = 32 * g + (c >> 2) * 8 + 4 * ab + (c & 3);
; #pragma unroll
;             for (int ks = 0; ks < 4; ++ks) Kf[g][ab][ks] = ld_b8(TOK + (size_t)(tc0 + key) * TOKP + TK_KR + h * HD + rq * 8 + ks * 32); }
;     f32x4 acc[2][8];
; #pragma unroll
;     for (int qb = 0; qb < 2; ++qb)
; #pragma unroll
;         for (int eb = 0; eb < 8; ++eb) acc[qb][eb] = (f32x4){0.f, 0.f, 0.f, 0.f};
;     const bf16* sp = ST + (((size_t)bhh * NCH + n) * HD + c) * HD + rq * 8;
; #pragma unroll
;     for (int eb = 0; eb < 8; ++eb)
; #pragma unroll
;         for (int ks = 0; ks < 4; ++ks) { const bf16x8 sf = ld_b8(sp + eb * 16 * HD + ks * 32);
; #pragma unroll
;             for (int qb = 0; qb < 2; ++qb) acc[qb][eb] = mfma16(sf, Qf[qb][ks], acc[qb][eb]); }
;     bf16x8 Vf[8];
; #pragma unroll
;     for (int eb = 0; eb < 8; ++eb) Vf[eb] = ld_b8(SWP + (size_t)(SW_VR + h * HD + eb * 16 + c) * SWPP + tc0 + 8 * rq);
; #pragma unroll
;     for (int qb = 0; qb < 2; ++qb) { const float f = fexp2((float)(qb2 * 32 + qb * 16 + c + 1) * lg);
; #pragma unroll
;         for (int eb = 0; eb < 8; ++eb) acc[qb][eb] *= f; }
.LBB0_655:
	s_bfe_u32 s1, s8, 0x50001
	s_ashr_i32 s0, s8, 9
	s_lshl_b32 s4, s0, 3
	s_lshl_b32 s0, s0, 11
	s_lshl_b32 s5, s1, 6
	v_and_b32_e32 v180, 15, v118
	s_or_b32 s0, s5, s0
	v_readlane_b32 s5, v251, 32
	v_ashrrev_i32_e32 v205, 4, v118
	s_or_b32 s4, s4, s9
	v_or_b32_e32 v209, s5, v180
	v_or_b32_e32 v196, s0, v209
	v_lshlrev_b32_e32 v202, 3, v205
	v_mov_b64_e32 v[160:161], s[80:81]
	s_movk_i32 s7, 0x2900
	s_ashr_i32 s5, s4, 31
	v_ashrrev_i32_e32 v203, 31, v202
	v_mad_i64_i32 v[198:199], s[12:13], v196, s7, v[160:161]
	s_lshl_b32 s96, s9, 8
	s_lshl_b64 s[4:5], s[4:5], 12
	s_lshl_b32 s1, s1, 7
	s_waitcnt lgkmcnt(0)
	v_lshl_add_u64 v[0:1], v[198:199], 0, s[96:97]
	v_lshlrev_b64 v[176:177], 1, v[202:203]
	s_or_b32 s1, s4, s1
	v_lshl_add_u64 v[8:9], v[0:1], 0, v[176:177]
	v_mov_b32_e32 v0, s1
	v_mov_b32_e32 v1, s5
	v_readlane_b32 s4, v253, 46
	v_lshlrev_b64 v[0:1], 8, v[0:1]
	v_readlane_b32 s5, v253, 47
	v_or_b32_e32 v194, 16, v196
	s_movk_i32 s6, 0x1000
	v_lshl_add_u64 v[0:1], s[4:5], 0, v[0:1]
	v_mad_i64_i32 v[200:201], s[4:5], v194, s7, v[160:161]
	v_add_co_u32_e32 v4, vcc, s6, v8
	s_mov_b64 s[4:5], 0x1000
	v_lshlrev_b32_e32 v2, 4, v180
	v_lshl_or_b32 v2, v205, 8, v2
	v_mov_b32_e32 v3, 0
	v_lshl_add_u64 v[36:37], v[0:1], 0, v[2:3]
	v_addc_co_u32_e32 v5, vcc, 0, v9, vcc
	v_lshl_add_u64 v[8:9], v[8:9], 0, s[4:5]
	global_load_dwordx4 v[0:3], v[36:37], off
	global_load_dwordx4 v[46:49], v[36:37], off offset:1024
	global_load_dwordx4 v[20:23], v[4:5], off
	global_load_dwordx4 v[52:55], v[8:9], off offset:64
	v_lshl_add_u64 v[4:5], v[200:201], 0, s[96:97]
	v_lshl_add_u64 v[12:13], v[4:5], 0, v[176:177]
	v_add_co_u32_e32 v4, vcc, s6, v12
	v_lshl_add_u64 v[80:81], v[12:13], 0, s[4:5]
	s_nop 0
	v_addc_co_u32_e32 v5, vcc, 0, v13, vcc
	global_load_dwordx4 v[24:27], v[4:5], off
	global_load_dwordx4 v[60:63], v[8:9], off offset:128
	global_load_dwordx4 v[56:59], v[80:81], off offset:64
	global_load_dwordx4 v[64:67], v[80:81], off offset:128
	s_movk_i32 s1, 0x2000
	v_add_co_u32_e32 v10, vcc, s1, v36
	s_movk_i32 s1, 0x4000
	s_nop 0
	v_addc_co_u32_e32 v11, vcc, 0, v37, vcc
	s_waitcnt lgkmcnt(0)
	global_load_dwordx4 v[14:17], v[10:11], off offset:-4096
	global_load_dwordx4 v[72:75], v[8:9], off offset:192
	s_waitcnt vmcnt(19)
	v_add_co_u32_e32 v50, vcc, s1, v36
	global_load_dwordx4 v[28:31], v[10:11], off
	s_nop 0
	v_addc_co_u32_e32 v51, vcc, 0, v37, vcc
	v_add_co_u32_e32 v84, vcc, s6, v36
	global_load_dwordx4 v[38:41], v[50:51], off offset:-4096
	global_load_dwordx4 v[112:115], v[50:51], off offset:2048
	v_addc_co_u32_e32 v85, vcc, 0, v37, vcc
	s_movk_i32 s1, 0x3000
	v_lshlrev_b32_e32 v119, 1, v118
	v_and_b32_e32 v118, 3, v118
	s_mov_b64 s[10:11], 0x1800
	s_lshl_b32 s9, s9, 7
	v_or_b32_e32 v228, 16, v209
	v_mov_b32_e32 v210, v202
	v_mov_b32_e32 v195, v202
	s_waitcnt vmcnt(10)
	v_mfma_f32_16x16x32_bf16 v[4:7], v[0:3], v[20:23], 0
	global_load_dwordx4 v[80:83], v[80:81], off offset:192
	s_waitcnt vmcnt(9)
	v_mfma_f32_16x16x32_bf16 v[0:3], v[0:3], v[24:27], 0
	v_mfma_f32_16x16x32_bf16 v[4:7], v[46:49], v[52:55], v[4:7]
	s_waitcnt vmcnt(7)
	v_mfma_f32_16x16x32_bf16 v[0:3], v[46:49], v[56:59], v[0:3]
	global_load_dwordx4 v[46:49], v[84:85], off offset:1024
	s_waitcnt vmcnt(6)
	v_mfma_f32_16x16x32_bf16 v[32:35], v[14:17], v[20:23], 0
	v_mfma_f32_16x16x32_bf16 v[14:17], v[14:17], v[24:27], 0
	s_waitcnt vmcnt(3)
	v_mfma_f32_16x16x32_bf16 v[68:71], v[38:41], v[20:23], 0
	s_waitcnt vmcnt(0)
	v_mfma_f32_16x16x32_bf16 v[12:15], v[46:49], v[56:59], v[14:17]
	s_nop 3
	global_load_dwordx4 v[16:19], v[10:11], off offset:1024
	v_mfma_f32_16x16x32_bf16 v[42:45], v[28:31], v[20:23], 0
	v_mfma_f32_16x16x32_bf16 v[28:31], v[28:31], v[24:27], 0
	v_mfma_f32_16x16x32_bf16 v[32:35], v[46:49], v[52:55], v[32:35]
	global_load_dwordx4 v[46:49], v[36:37], off offset:2048
	s_waitcnt vmcnt(1)
	v_mfma_f32_16x16x32_bf16 v[42:45], v[16:19], v[52:55], v[42:45]
	v_mfma_f32_16x16x32_bf16 v[16:19], v[16:19], v[56:59], v[28:31]
	s_nop 2
	global_load_dwordx4 v[28:31], v[84:85], off offset:2048
	s_waitcnt vmcnt(0)
	v_mfma_f32_16x16x32_bf16 v[76:79], v[28:31], v[64:67], v[12:15]
	s_nop 2
	global_load_dwordx4 v[12:15], v[36:37], off offset:3072
	v_mfma_f32_16x16x32_bf16 v[4:7], v[46:49], v[60:63], v[4:7]
	v_mfma_f32_16x16x32_bf16 v[0:3], v[46:49], v[64:67], v[0:3]
	v_mfma_f32_16x16x32_bf16 v[46:49], v[28:31], v[60:63], v[32:35]
	s_nop 2
	global_load_dwordx4 v[32:35], v[10:11], off offset:2048
	s_waitcnt vmcnt(1)
	v_mfma_f32_16x16x32_bf16 v[28:31], v[12:15], v[80:83], v[0:3]
	s_nop 2
	global_load_dwordx4 v[0:3], v[10:11], off offset:3072
	s_waitcnt vmcnt(1)
	v_mfma_f32_16x16x32_bf16 v[42:45], v[32:35], v[60:63], v[42:45]
	v_mfma_f32_16x16x32_bf16 v[16:19], v[32:35], v[64:67], v[16:19]
	v_mfma_f32_16x16x32_bf16 v[32:35], v[12:15], v[72:75], v[4:7]
	s_nop 2
	global_load_dwordx4 v[4:7], v[84:85], off offset:3072
	v_add_co_u32_e32 v84, vcc, s1, v36
	s_movk_i32 s1, 0x6000
	s_nop 0
	v_addc_co_u32_e32 v85, vcc, 0, v37, vcc
	s_waitcnt vmcnt(0)
	v_mfma_f32_16x16x32_bf16 v[12:15], v[4:7], v[72:75], v[46:49]
	s_nop 2
	global_load_dwordx4 v[46:49], v[84:85], off offset:1024
	v_add_co_u32_e32 v116, vcc, s1, v36
	v_mfma_f32_16x16x32_bf16 v[8:11], v[4:7], v[80:83], v[76:79]
	s_nop 0
	v_addc_co_u32_e32 v117, vcc, 0, v37, vcc
	s_movk_i32 s1, 0x5000
	v_mfma_f32_16x16x32_bf16 v[4:7], v[0:3], v[72:75], v[42:45]
	global_load_dwordx4 v[76:79], v[84:85], off offset:3072
	global_load_dwordx4 v[92:95], v[116:117], off
	global_load_dwordx4 v[88:91], v[116:117], off offset:1024
	global_load_dwordx4 v[42:45], v[84:85], off offset:2048
	v_mfma_f32_16x16x32_bf16 v[0:3], v[0:3], v[80:83], v[16:19]
	global_load_dwordx4 v[108:111], v[116:117], off offset:-4096
	v_mfma_f32_16x16x32_bf16 v[16:19], v[38:41], v[24:27], 0
	s_waitcnt vmcnt(5)
; __device__ __forceinline__ f32x4 mfma16(bf16x8 a, bf16x8 b, f32x4 c) { return __builtin_amdgcn_mfma_f32_16x16x32_bf16(a, b, c, 0, 0, 0); }
; __device__ __forceinline__ float fexp2(float x) { return __builtin_amdgcn_exp2f(x); }
; __device__ __forceinline__ void ret_task(const Frame& F, int l, int task) {
;     ...
;     bf16x8 Qf[2][4], Kf[2][2][4];
; #pragma unroll
;     for (int qb = 0; qb < 2; ++qb)
; #pragma unroll
;         for (int ks = 0; ks < 4; ++ks) Qf[qb][ks] = ld_b8(TOK + (size_t)(tq0 + qb * 16 + c) * TOKP + TK_QR + h * HD + ks * 32 + rq * 8);
; #pragma unroll
;     for (int g = 0; g < 2; ++g)
; #pragma unroll
;         for (int ab = 0; ab < 2; ++ab) { const int key = 32 * g + (c >> 2) * 8 + 4 * ab + (c & 3);
; #pragma unroll
;             for (int ks = 0; ks < 4; ++ks) Kf[g][ab][ks] = ld_b8(TOK + (size_t)(tc0 + key) * TOKP + TK_KR + h * HD + rq * 8 + ks * 32); }
;     f32x4 acc[2][8];
; #pragma unroll
;     for (int qb = 0; qb < 2; ++qb)
; #pragma unroll
;         for (int eb = 0; eb < 8; ++eb) acc[qb][eb] = (f32x4){0.f, 0.f, 0.f, 0.f};
;     const bf16* sp = ST + (((size_t)bhh * NCH + n) * HD + c) * HD + rq * 8;
; #pragma unroll
;     for (int eb = 0; eb < 8; ++eb)
; #pragma unroll
;         for (int ks = 0; ks < 4; ++ks) { const bf16x8 sf = ld_b8(sp + eb * 16 * HD + ks * 32);
; #pragma unroll
;             for (int qb = 0; qb < 2; ++qb) acc[qb][eb] = mfma16(sf, Qf[qb][ks], acc[qb][eb]); }
;     bf16x8 Vf[8];
; #pragma unroll
;     for (int eb = 0; eb < 8; ++eb) Vf[eb] = ld_b8(SWP + (size_t)(SW_VR + h * HD + eb * 16 + c) * SWPP + tc0 + 8 * rq);
; #pragma unroll
;     for (int qb = 0; qb < 2; ++qb) { const float f = fexp2((float)(qb2 * 32 + qb * 16 + c + 1) * lg);
; #pragma unroll
;         for (int eb = 0; eb < 8; ++eb) acc[qb][eb] *= f; }
	v_mfma_f32_16x16x32_bf16 v[38:41], v[46:49], v[52:55], v[68:71]
	s_nop 2
	global_load_dwordx4 v[68:71], v[50:51], off offset:1024
	global_load_dwordx4 v[84:87], v[50:51], off
	v_mfma_f32_16x16x32_bf16 v[16:19], v[46:49], v[56:59], v[16:19]
	s_waitcnt vmcnt(3)
	v_mfma_f32_16x16x32_bf16 v[38:41], v[42:45], v[60:63], v[38:41]
	v_mfma_f32_16x16x32_bf16 v[42:45], v[42:45], v[64:67], v[16:19]
	v_mfma_f32_16x16x32_bf16 v[16:19], v[76:79], v[72:75], v[38:41]
	s_nop 5
	v_add_co_u32_e32 v38, vcc, s1, v36
	v_mfma_f32_16x16x32_bf16 v[40:43], v[76:79], v[80:83], v[42:45]
	s_nop 0
	v_addc_co_u32_e32 v39, vcc, 0, v37, vcc
	global_load_dwordx4 v[96:99], v[38:39], off offset:3072
	global_load_dwordx4 v[104:107], v[38:39], off offset:1024
	global_load_dwordx4 v[100:103], v[38:39], off offset:2048
	s_waitcnt vmcnt(3)
	v_mfma_f32_16x16x32_bf16 v[44:47], v[84:87], v[20:23], 0
	global_load_dwordx4 v[48:51], v[50:51], off offset:3072
	s_movk_i32 s1, 0x7000
	v_mfma_f32_16x16x32_bf16 v[76:79], v[84:87], v[24:27], 0
	v_mfma_f32_16x16x32_bf16 v[44:47], v[68:71], v[52:55], v[44:47]
	v_mfma_f32_16x16x32_bf16 v[68:71], v[68:71], v[56:59], v[76:79]
	s_nop 5
	global_load_dwordx4 v[76:79], v[116:117], off offset:2048
	global_load_dwordx4 v[84:87], v[116:117], off offset:3072
	v_add_co_u32_e32 v116, vcc, s1, v36
	v_mfma_f32_16x16x32_bf16 v[44:47], v[112:115], v[60:63], v[44:47]
	s_nop 0
	v_addc_co_u32_e32 v117, vcc, 0, v37, vcc
	global_load_dwordx4 v[36:39], v[116:117], off offset:1024
	v_mfma_f32_16x16x32_bf16 v[112:115], v[112:115], v[64:67], v[68:71]
	s_ashr_i32 s1, s0, 31
	s_nop 1
	global_load_dwordx4 v[68:71], v[116:117], off
	s_waitcnt vmcnt(4)
	v_mfma_f32_16x16x32_bf16 v[44:47], v[48:51], v[72:75], v[44:47]
	v_mfma_f32_16x16x32_bf16 v[48:51], v[48:51], v[80:83], v[112:115]
	s_nop 2
	v_and_b32_e32 v112, 24, v119
	v_mfma_f32_16x16x32_bf16 v[120:123], v[108:111], v[20:23], 0
	v_or3_b32 v162, v118, v112, s0
	v_mad_i64_i32 v[118:119], s[4:5], v162, s7, v[160:161]
	v_mfma_f32_16x16x32_bf16 v[124:127], v[108:111], v[24:27], 0
	global_load_dwordx4 v[112:115], v[116:117], off offset:2048
	v_lshl_add_u64 v[118:119], v[118:119], 0, s[96:97]
	v_lshl_add_u64 v[128:129], v[118:119], 0, v[176:177]
	v_mfma_f32_16x16x32_bf16 v[120:123], v[104:107], v[52:55], v[120:123]
	v_add_co_u32_e32 v108, vcc, s6, v128
	v_mfma_f32_16x16x32_bf16 v[104:107], v[104:107], v[56:59], v[124:127]
	s_nop 0
	v_addc_co_u32_e32 v109, vcc, 0, v129, vcc
	v_lshl_add_u64 v[128:129], v[128:129], 0, s[10:11]
	v_or_b32_e32 v124, 4, v162
	v_mad_i64_i32 v[124:125], s[4:5], v124, s7, v[160:161]
	v_lshl_add_u64 v[124:125], v[124:125], 0, s[96:97]
	global_load_dwordx4 v[108:111], v[108:109], off offset:2048
	v_lshl_add_u64 v[130:131], v[124:125], 0, v[176:177]
	global_load_dwordx4 v[124:127], v[128:129], off offset:64
	v_mfma_f32_16x16x32_bf16 v[120:123], v[100:103], v[60:63], v[120:123]
	global_load_dwordx4 v[116:119], v[116:117], off offset:3072
	v_mfma_f32_16x16x32_bf16 v[100:103], v[100:103], v[64:67], v[104:107]
	s_nop 2
	v_add_co_u32_e32 v104, vcc, s6, v130
	v_mfma_f32_16x16x32_bf16 v[144:147], v[96:99], v[72:75], v[120:123]
	s_nop 0
	v_addc_co_u32_e32 v105, vcc, 0, v131, vcc
	v_or_b32_e32 v106, s9, v180
	global_load_dwordx4 v[120:123], v[104:105], off offset:2048
	v_mfma_f32_16x16x32_bf16 v[148:151], v[96:99], v[80:83], v[100:103]
	global_load_dwordx4 v[168:171], v[128:129], off offset:128
	global_load_dwordx4 v[96:99], v[128:129], off offset:192
	v_mul_u32_u24_e32 v106, 0x4080, v106
	v_lshlrev_b32_e32 v184, 1, v106
	v_mfma_f32_16x16x32_bf16 v[100:103], v[92:95], v[20:23], 0
	v_or_b32_e32 v104, 32, v162
	v_lshl_add_u64 v[106:107], s[64:65], 0, v[184:185]
	v_mad_i64_i32 v[104:105], s[4:5], v104, s7, v[160:161]
	v_mfma_f32_16x16x32_bf16 v[92:95], v[92:95], v[24:27], 0
	v_lshl_add_u64 v[106:107], s[0:1], 1, v[106:107]
	v_lshl_add_u64 v[178:179], v[106:107], 0, v[176:177]
	s_mov_b32 s4, 0x23c7000
	v_mfma_f32_16x16x32_bf16 v[100:103], v[88:91], v[52:55], v[100:103]
	v_add_co_u32_e32 v106, vcc, s4, v178
	v_lshl_add_u64 v[128:129], v[130:131], 0, s[10:11]
	v_mfma_f32_16x16x32_bf16 v[88:91], v[88:91], v[56:59], v[92:95]
	v_addc_co_u32_e32 v107, vcc, 0, v179, vcc
	s_waitcnt vmcnt(10)
	v_mfma_f32_16x16x32_bf16 v[92:95], v[76:79], v[60:63], v[100:103]
	v_mfma_f32_16x16x32_bf16 v[100:103], v[76:79], v[64:67], v[88:91]
	global_load_dwordx4 v[76:79], v[106:107], off
	global_load_dwordx4 v[172:175], v[128:129], off offset:64
	s_nop 1
	v_lshl_add_u64 v[88:89], v[104:105], 0, s[96:97]
	s_waitcnt vmcnt(11)
	v_mfma_f32_16x16x32_bf16 v[152:155], v[84:87], v[72:75], v[92:95]
	v_lshl_add_u64 v[104:105], v[88:89], 0, v[176:177]
	global_load_dwordx4 v[88:91], v[128:129], off offset:192
	v_lshl_add_u64 v[106:107], v[104:105], 0, s[10:11]
	v_mfma_f32_16x16x32_bf16 v[156:159], v[84:87], v[80:83], v[100:103]
	global_load_dwordx4 v[84:87], v[128:129], off offset:128
	v_add_co_u32_e32 v104, vcc, s6, v104
	s_waitcnt vmcnt(11)
	v_mfma_f32_16x16x32_bf16 v[92:95], v[68:71], v[20:23], 0
	v_addc_co_u32_e32 v105, vcc, 0, v105, vcc
	global_load_dwordx4 v[132:135], v[106:107], off offset:64
	global_load_dwordx4 v[128:131], v[106:107], off offset:128
	v_mfma_f32_16x16x32_bf16 v[100:103], v[68:71], v[24:27], 0
	v_or_b32_e32 v68, 36, v162
	v_mad_i64_i32 v[68:69], s[4:5], v68, s7, v[160:161]
	v_mfma_f32_16x16x32_bf16 v[92:95], v[36:39], v[52:55], v[92:95]
	s_mov_b32 s4, 0x2040000
	v_add_co_u32_e32 v70, vcc, s4, v178
	v_mfma_f32_16x16x32_bf16 v[36:39], v[36:39], v[56:59], v[100:103]
	s_nop 0
	v_addc_co_u32_e32 v71, vcc, 0, v179, vcc
	s_mov_b32 s4, 0x20c1000
	s_waitcnt vmcnt(12)
; __device__ __forceinline__ f32x4 mfma16(bf16x8 a, bf16x8 b, f32x4 c) { return __builtin_amdgcn_mfma_f32_16x16x32_bf16(a, b, c, 0, 0, 0); }
; __device__ __forceinline__ float fexp2(float x) { return __builtin_amdgcn_exp2f(x); }
; __device__ __forceinline__ void ret_task(const Frame& F, int l, int task) {
;     ...
;     for (int eb = 0; eb < 8; ++eb)
; #pragma unroll
;         for (int ks = 0; ks < 4; ++ks) { const bf16x8 sf = ld_b8(sp + eb * 16 * HD + ks * 32);
; #pragma unroll
;             for (int qb = 0; qb < 2; ++qb) acc[qb][eb] = mfma16(sf, Qf[qb][ks], acc[qb][eb]); }
;     bf16x8 Vf[8];
; #pragma unroll
;     for (int eb = 0; eb < 8; ++eb) Vf[eb] = ld_b8(SWP + (size_t)(SW_VR + h * HD + eb * 16 + c) * SWPP + tc0 + 8 * rq);
; #pragma unroll
;     for (int qb = 0; qb < 2; ++qb) { const float f = fexp2((float)(qb2 * 32 + qb * 16 + c + 1) * lg);
; #pragma unroll
;         for (int eb = 0; eb < 8; ++eb) acc[qb][eb] *= f; }
;     f32x4 g4[8]; u32x2 gwq[2][8];
; #pragma unroll
;     for (int g = 0; g < 2; ++g) {
;         if (g <= qb2) {
;             f32x4 sa[2][2];
; #pragma unroll
;             for (int qb = 0; qb < 2; ++qb)
; #pragma unroll
;                 for (int ab = 0; ab < 2; ++ab) sa[qb][ab] = (f32x4){0.f, 0.f, 0.f, 0.f};
; #pragma unroll
;             for (int ab = 0; ab < 2; ++ab)
; #pragma unroll
;                 for (int ks = 0; ks < 4; ++ks)
; #pragma unroll
;                     for (int qb = 0; qb < 2; ++qb) sa[qb][ab] = mfma16(Kf[g][ab][ks], Qf[qb][ks], sa[qb][ab]);
;             bf16x8 Pf[2];
; #pragma unroll
;             for (int qb = 0; qb < 2; ++qb) {
;                 const int i = qb2 * 32 + qb * 16 + c;
; #pragma unroll
;                 for (int ab = 0; ab < 2; ++ab)
; #pragma unroll
;                     for (int e = 0; e < 4; ++e) { const int diff = i - (32 * g + 8 * rq + 4 * ab + e);
;                         sa[qb][ab][e] = diff >= 0 ? sa[qb][ab][e] * fexp2((float)diff * lg) : 0.f; }
	v_mfma_f32_16x16x32_bf16 v[36:39], v[112:115], v[64:67], v[36:39]
	global_load_dwordx4 v[140:143], v[104:105], off offset:2048
	global_load_dwordx4 v[136:139], v[106:107], off offset:192
	v_lshl_add_u64 v[68:69], v[68:69], 0, s[96:97]
	v_lshl_add_u64 v[68:69], v[68:69], 0, v[176:177]
	v_mfma_f32_16x16x32_bf16 v[100:103], v[112:115], v[60:63], v[92:95]
	s_nop 2
	global_load_dwordx4 v[92:95], v[70:71], off
	v_add_co_u32_e32 v70, vcc, s4, v178
	s_mov_b32 s4, 0x2142000
	s_nop 0
	v_addc_co_u32_e32 v71, vcc, 0, v179, vcc
	v_add_co_u32_e32 v104, vcc, s4, v178
	s_waitcnt vmcnt(12)
	v_mfma_f32_16x16x32_bf16 v[164:167], v[116:119], v[80:83], v[36:39]
	v_addc_co_u32_e32 v105, vcc, 0, v179, vcc
	s_mov_b32 s4, 0x21c3000
	v_mfma_f32_16x16x32_bf16 v[36:39], v[108:111], v[20:23], 0
	v_mfma_f32_16x16x32_bf16 v[108:111], v[108:111], v[24:27], 0
	v_mfma_f32_16x16x32_bf16 v[160:163], v[116:119], v[72:75], v[100:103]
	s_nop 2
	global_load_dwordx4 v[100:103], v[70:71], off
	s_nop 0
	global_load_dwordx4 v[104:107], v[104:105], off
	v_add_co_u32_e32 v70, vcc, s4, v178
	s_mov_b32 s4, 0x2244000
	s_nop 0
	v_addc_co_u32_e32 v71, vcc, 0, v179, vcc
	v_add_co_u32_e32 v116, vcc, s4, v178
	v_readlane_b32 s4, v251, 33
	s_nop 0
	v_addc_co_u32_e32 v117, vcc, 0, v179, vcc
	v_mfma_f32_16x16x32_bf16 v[36:39], v[124:127], v[52:55], v[36:39]
	global_load_dwordx4 v[112:115], v[70:71], off
	s_nop 0
	global_load_dwordx4 v[116:119], v[116:117], off
	v_add_u32_e32 v70, s4, v180
	v_cvt_f32_ubyte0_e32 v71, v70
	v_mfma_f32_16x16x32_bf16 v[108:111], v[124:127], v[56:59], v[108:111]
	v_add_u32_e32 v70, 16, v70
	v_cvt_f32_ubyte0_e32 v70, v70
	v_or_b32_e32 v126, 2, v202
	v_mul_f32_e32 v71, v197, v71
	v_mul_f32_e32 v70, v197, v70
	s_waitcnt vmcnt(14)
	v_mfma_f32_16x16x32_bf16 v[36:39], v[168:171], v[60:63], v[36:39]
	v_exp_f32_e32 v204, v71
	v_exp_f32_e32 v206, v70
	v_or_b32_e32 v127, 3, v202
	v_mfma_f32_16x16x32_bf16 v[108:111], v[168:171], v[64:67], v[108:111]
	v_sub_u32_e32 v169, v209, v202
	v_sub_u32_e32 v170, v209, v126
	v_cvt_f32_u32_e32 v70, v169
	v_cvt_f32_u32_e32 v71, v170
	s_waitcnt vmcnt(13)
	v_mfma_f32_16x16x32_bf16 v[36:39], v[96:99], v[72:75], v[36:39]
	v_or_b32_e32 v168, 1, v202
	v_mul_f32_e32 v70, v197, v70
	v_mul_f32_e32 v71, v197, v71
	v_exp_f32_e32 v70, v70
	v_exp_f32_e32 v71, v71
	v_mfma_f32_16x16x32_bf16 v[96:99], v[96:99], v[80:83], v[108:111]
	s_nop 1
	v_mov_b32_e32 v124, v36
	v_mov_b32_e32 v125, v38
	v_pk_mul_f32 v[70:71], v[70:71], v[124:125]
	v_mfma_f32_16x16x32_bf16 v[108:111], v[120:123], v[20:23], 0
	v_cmp_lt_i32_e32 vcc, -1, v170
	v_sub_u32_e32 v125, v209, v127
	v_cvt_f32_u32_e32 v38, v125
	v_mfma_f32_16x16x32_bf16 v[120:123], v[120:123], v[24:27], 0
	v_cndmask_b32_e32 v124, 0, v71, vcc
	v_sub_u32_e32 v71, v209, v168
	v_cvt_f32_u32_e32 v36, v71
	s_waitcnt vmcnt(11)
	v_mfma_f32_16x16x32_bf16 v[108:111], v[172:175], v[52:55], v[108:111]
	v_cmp_lt_i32_e32 vcc, -1, v169
	v_pk_mul_f32 v[14:15], v[204:205], v[14:15] op_sel_hi:[0,1]
	v_mul_f32_e32 v36, v197, v36
	v_mfma_f32_16x16x32_bf16 v[120:123], v[172:175], v[56:59], v[120:123]
	v_mul_f32_e64 v12, v204, v12
	v_mul_f32_e64 v13, v204, v13
	s_mov_b32 s4, 0x22c5000
	v_pk_mul_f32 v[6:7], v[204:205], v[6:7] op_sel_hi:[0,1]
	s_waitcnt vmcnt(9)
	v_mfma_f32_16x16x32_bf16 v[108:111], v[84:87], v[60:63], v[108:111]
	v_mul_f32_e64 v4, v204, v4
	v_mul_f32_e64 v5, v204, v5
	v_pk_mul_f32 v[30:31], v[206:207], v[30:31] op_sel_hi:[0,1]
	v_pk_mul_f32 v[28:29], v[206:207], v[28:29] op_sel_hi:[0,1]
	v_mfma_f32_16x16x32_bf16 v[84:87], v[84:87], v[64:67], v[120:123]
	v_mul_f32_e64 v2, v206, v2
	v_mul_f32_e64 v3, v206, v3
	v_pk_mul_f32 v[0:1], v[206:207], v[0:1] op_sel_hi:[0,1]
	v_pk_mul_f32 v[34:35], v[204:205], v[34:35] op_sel_hi:[0,1]
	v_exp_f32_e32 v120, v36
	v_mul_f32_e32 v36, v197, v38
	v_exp_f32_e32 v121, v36
	v_mov_b32_e32 v38, v37
	v_cndmask_b32_e32 v122, 0, v70, vcc
	v_cmp_lt_i32_e32 vcc, -1, v71
	v_pk_mul_f32 v[36:37], v[120:121], v[38:39]
	v_mfma_f32_16x16x32_bf16 v[108:111], v[88:91], v[72:75], v[108:111]
	v_sub_u32_e32 v39, v228, v126
	v_cvt_f32_u32_e32 v70, v39
	v_sub_u32_e32 v120, v228, v127
	v_mfma_f32_16x16x32_bf16 v[84:87], v[88:91], v[80:83], v[84:87]
	v_cndmask_b32_e32 v88, 0, v36, vcc
	v_cmp_lt_i32_e32 vcc, -1, v125
	v_sub_u32_e32 v91, v228, v168
	v_sub_u32_e32 v89, v228, v202
	v_cndmask_b32_e32 v90, 0, v37, vcc
	v_cvt_f32_u32_e32 v37, v91
	v_cvt_f32_u32_e32 v36, v89
	v_mov_b32_e32 v71, v98
	v_cmp_lt_i32_e32 vcc, -1, v39
	v_mul_f32_e32 v37, v197, v37
	v_mul_f32_e32 v36, v197, v36
	v_exp_f32_e32 v38, v37
	v_mul_f32_e32 v37, v197, v70
	v_exp_f32_e32 v36, v36
	v_exp_f32_e32 v37, v37
	v_mov_b32_e32 v70, v96
	v_cvt_f32_u32_e32 v96, v120
	v_mov_b32_e32 v98, v97
	v_pk_mul_f32 v[36:37], v[36:37], v[70:71]
	v_or_b32_e32 v123, 5, v202
	v_cndmask_b32_e32 v121, 0, v37, vcc
	v_mul_f32_e32 v37, v197, v96
	v_exp_f32_e32 v39, v37
	v_cmp_lt_i32_e32 vcc, -1, v89
	v_or_b32_e32 v97, 6, v202
	v_sub_u32_e32 v125, v209, v123
	v_cndmask_b32_e32 v89, 0, v36, vcc
	v_pk_mul_f32 v[36:37], v[38:39], v[98:99]
	v_cmp_lt_i32_e32 vcc, -1, v91
	v_or_b32_e32 v98, 4, v202
	v_sub_u32_e32 v99, v209, v98
	v_cndmask_b32_e32 v91, 0, v36, vcc
	v_cmp_lt_i32_e32 vcc, -1, v120
	v_sub_u32_e32 v39, v209, v97
	v_cvt_f32_u32_e32 v36, v99
	v_cndmask_b32_e32 v96, 0, v37, vcc
	v_cvt_f32_u32_e32 v37, v125
	v_cvt_f32_u32_e32 v70, v39
	v_or_b32_e32 v120, 7, v202
	v_mul_f32_e32 v36, v197, v36
	v_mul_f32_e32 v37, v197, v37
	v_exp_f32_e32 v38, v37
	v_mul_f32_e32 v37, v197, v70
	v_exp_f32_e32 v36, v36
	v_sub_u32_e32 v126, v209, v120
	v_exp_f32_e32 v37, v37
	v_mov_b32_e32 v70, v108
	v_cvt_f32_u32_e32 v108, v126
	v_mov_b32_e32 v71, v110
	v_pk_mul_f32 v[36:37], v[36:37], v[70:71]
; __device__ __forceinline__ f32x4 mfma16(bf16x8 a, bf16x8 b, f32x4 c) { return __builtin_amdgcn_mfma_f32_16x16x32_bf16(a, b, c, 0, 0, 0); }
; __device__ __forceinline__ float fexp2(float x) { return __builtin_amdgcn_exp2f(x); }
; __device__ __forceinline__ void ret_task(const Frame& F, int l, int task) {
;     ...
;             bf16x8 Pf[2];
; #pragma unroll
;             for (int qb = 0; qb < 2; ++qb) {
;                 const int i = qb2 * 32 + qb * 16 + c;
; #pragma unroll
;                 for (int ab = 0; ab < 2; ++ab)
; #pragma unroll
;                     for (int e = 0; e < 4; ++e) { const int diff = i - (32 * g + 8 * rq + 4 * ab + e);
;                         sa[qb][ab][e] = diff >= 0 ? sa[qb][ab][e] * fexp2((float)diff * lg) : 0.f; }
;                 Pf[qb] = pack8(sa[qb][0], sa[qb][1]);
;             }
; #pragma unroll
;             for (int eb = 0; eb < 8; ++eb)
; #pragma unroll
;                 for (int qb = 0; qb < 2; ++qb) acc[qb][eb] = mfma16(Vf[eb], Pf[qb], acc[qb][eb]);
	v_cmp_lt_i32_e32 vcc, -1, v39
	v_mov_b32_e32 v110, v109
	v_sub_u32_e32 v98, v228, v98
	v_cndmask_b32_e32 v127, 0, v37, vcc
	v_mul_f32_e32 v37, v197, v108
	v_exp_f32_e32 v39, v37
	v_cmp_lt_i32_e32 vcc, -1, v99
	v_mov_b32_e32 v71, v86
	v_mov_b32_e32 v86, v85
	v_cndmask_b32_e32 v99, 0, v36, vcc
	v_pk_mul_f32 v[36:37], v[38:39], v[110:111]
	v_cmp_lt_i32_e32 vcc, -1, v125
	v_sub_u32_e32 v39, v228, v97
	v_sub_u32_e32 v97, v228, v123
	v_cndmask_b32_e32 v108, 0, v36, vcc
	v_cmp_lt_i32_e32 vcc, -1, v126
	v_cvt_f32_u32_e32 v36, v98
	v_cvt_f32_u32_e32 v70, v39
	v_cndmask_b32_e32 v109, 0, v37, vcc
	v_cvt_f32_u32_e32 v37, v97
	v_mul_f32_e32 v36, v197, v36
	v_exp_f32_e32 v36, v36
	v_sub_u32_e32 v110, v228, v120
	v_mul_f32_e32 v37, v197, v37
	v_exp_f32_e32 v38, v37
	v_mul_f32_e32 v37, v197, v70
	v_exp_f32_e32 v37, v37
	v_mov_b32_e32 v70, v84
	v_cvt_f32_u32_e32 v84, v110
	v_cmp_lt_i32_e32 vcc, -1, v39
	v_pk_mul_f32 v[36:37], v[36:37], v[70:71]
	s_nop 0
	v_cndmask_b32_e32 v70, 0, v37, vcc
	v_mul_f32_e32 v37, v197, v84
	v_exp_f32_e32 v39, v37
	v_cmp_lt_i32_e32 vcc, -1, v98
	s_nop 1
	v_cndmask_b32_e32 v71, 0, v36, vcc
	v_pk_mul_f32 v[36:37], v[38:39], v[86:87]
	v_bfe_u32 v38, v90, 16, 1
	v_bfe_u32 v39, v88, 16, 1
	v_add3_u32 v39, v88, v39, s76
	v_add3_u32 v38, v90, v38, s76
	s_nop 1
	v_bfe_u32 v88, v122, 16, 1
	v_bfe_u32 v90, v124, 16, 1
	v_cmp_lt_i32_e32 vcc, -1, v97
	v_add3_u32 v90, v124, v90, s76
	v_add3_u32 v88, v122, v88, s76
	s_nop 1
	v_cndmask_b32_e32 v36, 0, v36, vcc
	v_cmp_lt_i32_e32 vcc, -1, v110
	s_nop 2
	v_lshrrev_b32_e32 v88, 16, v88
	v_lshrrev_b32_e32 v90, 16, v90
	v_cndmask_b32_e32 v37, 0, v37, vcc
	v_and_or_b32 v231, v38, s75, v90
	v_and_or_b32 v230, v39, s75, v88
	v_cvt_pk_bf16_f32 v233, v127, v109
	v_cvt_pk_bf16_f32 v232, v99, v108
	v_bfe_u32 v84, v96, 16, 1
	v_bfe_u32 v38, v37, 16, 1
	v_add3_u32 v84, v96, v84, s76
	s_waitcnt vmcnt(3)
	v_mfma_f32_16x16x32_bf16 v[96:99], v[100:103], v[230:233], v[12:15]
	v_bfe_u32 v39, v36, 16, 1
	v_bfe_u32 v85, v91, 16, 1
	v_add3_u32 v37, v37, v38, s76
	v_add_co_u32_e32 v12, vcc, s4, v178
	v_bfe_u32 v38, v89, 16, 1
	s_nop 0
	v_addc_co_u32_e32 v13, vcc, 0, v179, vcc
	s_mov_b32 s4, 0x2346000
	v_add3_u32 v85, v91, v85, s76
	v_add3_u32 v36, v36, v39, s76
	v_bfe_u32 v39, v121, 16, 1
	v_add3_u32 v38, v89, v38, s76
	s_waitcnt vmcnt(2)
	v_mfma_f32_16x16x32_bf16 v[88:91], v[104:107], v[230:233], v[4:7]
	v_add3_u32 v39, v121, v39, s76
	global_load_dwordx4 v[120:123], v[12:13], off
	v_bfe_u32 v86, v71, 16, 1
	v_add_co_u32_e32 v4, vcc, s4, v178
	v_bfe_u32 v87, v70, 16, 1
	s_nop 0
	v_addc_co_u32_e32 v5, vcc, 0, v179, vcc
	global_load_dwordx4 v[124:127], v[4:5], off
	v_add_co_u32_e32 v6, vcc, s6, v68
	v_lshl_add_u64 v[4:5], v[68:69], 0, s[10:11]
	s_nop 0
	v_addc_co_u32_e32 v7, vcc, 0, v69, vcc
	global_load_dwordx4 v[172:175], v[4:5], off offset:64
	global_load_dwordx4 v[168:171], v[4:5], off offset:128
	global_load_dwordx4 v[180:183], v[6:7], off offset:2048
	global_load_dwordx4 v[176:179], v[4:5], off offset:192
	v_add3_u32 v70, v70, v87, s76
	v_add3_u32 v71, v71, v86, s76
	v_lshrrev_b32_e32 v38, 16, v38
	v_lshrrev_b32_e32 v39, 16, v39
	v_lshrrev_b32_e32 v71, 16, v71
	v_lshrrev_b32_e32 v70, 16, v70
	v_and_or_b32 v237, v37, s75, v70
	v_and_or_b32 v236, v36, s75, v71
	v_and_or_b32 v235, v84, s75, v39
	v_and_or_b32 v234, v85, s75, v38
	v_readlane_b32 s4, v251, 34
	v_pk_mul_f32 v[32:33], v[204:205], v[32:33] op_sel_hi:[0,1]
	v_mfma_f32_16x16x32_bf16 v[36:39], v[92:95], v[234:237], v[28:31]
	v_mul_f32_e64 v10, v206, v10
	v_mul_f32_e64 v11, v206, v11
	v_pk_mul_f32 v[8:9], v[206:207], v[8:9] op_sel_hi:[0,1]
	v_pk_mul_f32 v[6:7], v[206:207], v[150:151] op_sel_hi:[0,1]
	v_mfma_f32_16x16x32_bf16 v[28:31], v[104:107], v[234:237], v[0:3]
	v_mul_f32_e64 v4, v206, v148
	v_mul_f32_e64 v5, v206, v149
	v_readlane_b32 s5, v251, 35
	s_andn2_b64 vcc, exec, s[4:5]
	v_pk_mul_f32 v[2:3], v[204:205], v[18:19] op_sel_hi:[0,1]
	v_pk_mul_f32 v[0:1], v[204:205], v[16:17] op_sel_hi:[0,1]
	v_mfma_f32_16x16x32_bf16 v[108:111], v[92:95], v[230:233], v[32:35]
	s_waitcnt vmcnt(7)
	v_mfma_f32_16x16x32_bf16 v[84:87], v[112:115], v[230:233], v[0:3]
	s_nop 2
	v_mul_f32_e64 v2, v206, v42
	v_mul_f32_e64 v3, v206, v43
	v_pk_mul_f32 v[0:1], v[206:207], v[40:41] op_sel_hi:[0,1]
	v_mfma_f32_16x16x32_bf16 v[32:35], v[100:103], v[234:237], v[8:11]
	v_mul_f32_e64 v42, v204, v162
	v_mul_f32_e64 v43, v204, v163
	v_pk_mul_f32 v[40:41], v[204:205], v[160:161] op_sel_hi:[0,1]
	v_mfma_f32_16x16x32_bf16 v[16:19], v[112:115], v[234:237], v[0:3]
	s_nop 2
	v_mul_f32_e64 v2, v204, v46
	v_mul_f32_e64 v3, v204, v47
	v_pk_mul_f32 v[0:1], v[204:205], v[44:45] op_sel_hi:[0,1]
	s_waitcnt vmcnt(5)
	v_mfma_f32_16x16x32_bf16 v[8:11], v[120:123], v[234:237], v[4:7]
	v_mfma_f32_16x16x32_bf16 v[68:71], v[116:119], v[230:233], v[0:3]
	s_nop 2
	v_mul_f32_e64 v2, v206, v50
	v_mul_f32_e64 v3, v206, v51
	v_pk_mul_f32 v[0:1], v[206:207], v[48:49] op_sel_hi:[0,1]
	v_mfma_f32_16x16x32_bf16 v[40:43], v[76:79], v[230:233], v[40:43]
	s_nop 0
	v_mfma_f32_16x16x32_bf16 v[12:15], v[116:119], v[234:237], v[0:3]
	s_nop 2
	v_mul_f32_e64 v2, v204, v146
	v_mul_f32_e64 v3, v204, v147
	v_pk_mul_f32 v[0:1], v[204:205], v[144:145] op_sel_hi:[0,1]
	v_pk_mul_f32 v[146:147], v[206:207], v[166:167] op_sel_hi:[0,1]
	v_pk_mul_f32 v[144:145], v[206:207], v[164:165] op_sel_hi:[0,1]
	v_mfma_f32_16x16x32_bf16 v[48:51], v[120:123], v[230:233], v[0:3]
	s_nop 2
	v_mul_f32_e64 v2, v204, v154
	v_mul_f32_e64 v3, v204, v155
	v_pk_mul_f32 v[0:1], v[204:205], v[152:153] op_sel_hi:[0,1]
	s_waitcnt vmcnt(4)
	s_nop 0
	v_mfma_f32_16x16x32_bf16 v[44:47], v[124:127], v[230:233], v[0:3]
	s_nop 2
	v_mul_f32_e64 v2, v206, v158
	v_mul_f32_e64 v3, v206, v159
	v_pk_mul_f32 v[0:1], v[206:207], v[156:157] op_sel_hi:[0,1]
	s_nop 1
	v_mfma_f32_16x16x32_bf16 v[4:7], v[124:127], v[234:237], v[0:3]
	s_nop 2
	v_cndmask_b32_e64 v0, 0, 1, s[4:5]
	v_cmp_ne_u32_e64 s[34:35], 1, v0
	v_mfma_f32_16x16x32_bf16 v[0:3], v[76:79], v[234:237], v[144:147]
	s_cbranch_vccnz .LBB0_657
; __device__ __forceinline__ f32x4 mfma16(bf16x8 a, bf16x8 b, f32x4 c) { return __builtin_amdgcn_mfma_f32_16x16x32_bf16(a, b, c, 0, 0, 0); }
; __device__ __forceinline__ void ret_task(const Frame& F, int l, int task) {
;     ...
;     for (int g = 0; g < 2; ++g) {
;         if (g <= qb2) {
;             f32x4 sa[2][2];
; #pragma unroll
;             for (int qb = 0; qb < 2; ++qb)
; #pragma unroll
;                 for (int ab = 0; ab < 2; ++ab) sa[qb][ab] = (f32x4){0.f, 0.f, 0.f, 0.f};
; #pragma unroll
;             for (int ab = 0; ab < 2; ++ab)
; #pragma unroll
;                 for (int ks = 0; ks < 4; ++ks)
; #pragma unroll
;                     for (int qb = 0; qb < 2; ++qb) sa[qb][ab] = mfma16(Kf[g][ab][ks], Qf[qb][ks], sa[qb][ab]);
;     ...
;         if (g == 0) {
;             if (qb2) {
; #pragma unroll
;                 for (int eb = 0; eb < 8; ++eb) Vf[eb] = ld_b8(SWP + (size_t)(SW_VR + h * HD + eb * 16 + c) * SWPP + tc0 + 32 + 8 * rq);
;             }
; #pragma unroll
;             for (int eb = 0; eb < 8; ++eb) { const int e0 = h * HD + eb * 16 + rq * 4;
; #pragma unroll
;                 for (int qb = 0; qb < 2; ++qb) gwq[qb][eb] = ld_u2(TOK + (size_t)(tq0 + qb * 16 + c) * TOKP + TK_GR + e0); }
	s_lshl_b64 s[0:1], s[0:1], 1
	s_add_u32 s0, s64, s0
	s_addc_u32 s1, s65, s1
	v_lshl_add_u64 v[76:77], s[0:1], 0, v[184:185]
	v_lshl_add_u64 v[76:77], v[202:203], 1, v[76:77]
	v_add_co_u32_e32 v78, vcc, 0x2040000, v76
	s_nop 1
	v_addc_co_u32_e32 v79, vcc, 0, v77, vcc
	v_add_co_u32_e32 v100, vcc, 0x20c1000, v76
	s_nop 1
	v_addc_co_u32_e32 v101, vcc, 0, v77, vcc
	global_load_dwordx4 v[92:95], v[78:79], off offset:64
	s_nop 0
	global_load_dwordx4 v[100:103], v[100:101], off offset:64
	v_add_co_u32_e32 v78, vcc, 0x2142000, v76
	s_nop 1
	v_addc_co_u32_e32 v79, vcc, 0, v77, vcc
	v_add_co_u32_e32 v112, vcc, 0x21c3000, v76
	s_nop 1
	v_addc_co_u32_e32 v113, vcc, 0, v77, vcc
	global_load_dwordx4 v[104:107], v[78:79], off offset:64
	s_nop 0
	global_load_dwordx4 v[112:115], v[112:113], off offset:64
	v_add_co_u32_e32 v78, vcc, 0x2244000, v76
	s_nop 1
	v_addc_co_u32_e32 v79, vcc, 0, v77, vcc
	v_add_co_u32_e32 v120, vcc, 0x22c5000, v76
	s_nop 1
	v_addc_co_u32_e32 v121, vcc, 0, v77, vcc
	global_load_dwordx4 v[116:119], v[78:79], off offset:64
	s_nop 0
	global_load_dwordx4 v[120:123], v[120:121], off offset:64
	v_add_co_u32_e32 v78, vcc, 0x2346000, v76
	s_nop 1
	v_addc_co_u32_e32 v79, vcc, 0, v77, vcc
	v_add_co_u32_e32 v76, vcc, 0x23c7000, v76
	s_nop 1
	v_addc_co_u32_e32 v77, vcc, 0, v77, vcc
	global_load_dwordx4 v[124:127], v[78:79], off offset:64
	s_nop 0
	global_load_dwordx4 v[76:79], v[76:77], off offset:64
.LBB0_657:
	v_lshlrev_b32_e32 v208, 2, v205
	s_nop 0
	v_add_u32_e32 v144, s9, v208
	v_ashrrev_i32_e32 v145, 31, v144
	v_lshlrev_b64 v[156:157], 1, v[144:145]
	v_lshl_add_u64 v[144:145], v[198:199], 0, v[156:157]
	s_mov_b64 s[0:1], 0x2000
	v_lshl_add_u64 v[146:147], v[144:145], 0, s[0:1]
	v_add_co_u32_e32 v144, vcc, 0x2000, v144
	v_lshl_add_u64 v[148:149], v[200:201], 0, v[156:157]
	s_nop 0
	v_addc_co_u32_e32 v145, vcc, 0, v145, vcc
	v_lshl_add_u64 v[230:231], v[148:149], 0, s[0:1]
	v_add_co_u32_e32 v148, vcc, 0x2000, v148
	s_movk_i32 s33, 0x1100
	s_nop 0
	v_addc_co_u32_e32 v149, vcc, 0, v149, vcc
	global_load_dwordx2 v[204:205], v[146:147], off offset:32
	global_load_dwordx2 v[202:203], v[146:147], off offset:64
	global_load_dwordx2 v[200:201], v[146:147], off offset:96
	global_load_dwordx2 v[198:199], v[146:147], off offset:128
	global_load_dwordx2 v[158:159], v[230:231], off offset:32
	global_load_dwordx2 v[154:155], v[230:231], off offset:64
	global_load_dwordx2 v[152:153], v[230:231], off offset:96
	global_load_dwordx2 v[150:151], v[230:231], off offset:128
	global_load_dwordx2 v[206:207], v[144:145], off
	global_load_dwordx2 v[166:167], v[146:147], off offset:160
	global_load_dwordx2 v[164:165], v[146:147], off offset:192
	global_load_dwordx2 v[162:163], v[146:147], off offset:224
	global_load_dwordx2 v[160:161], v[148:149], off
	s_nop 0
	global_load_dwordx2 v[148:149], v[230:231], off offset:160
	global_load_dwordx2 v[146:147], v[230:231], off offset:192
	global_load_dwordx2 v[144:145], v[230:231], off offset:224
	s_and_b64 vcc, exec, s[34:35]
	s_cbranch_vccnz .LBB0_633
	v_mfma_f32_16x16x32_bf16 v[230:233], v[140:143], v[20:23], 0
	s_waitcnt vmcnt(17)
	v_mfma_f32_16x16x32_bf16 v[20:23], v[180:183], v[20:23], 0
	v_mfma_f32_16x16x32_bf16 v[140:143], v[140:143], v[24:27], 0
	v_mfma_f32_16x16x32_bf16 v[24:27], v[180:183], v[24:27], 0
	v_mfma_f32_16x16x32_bf16 v[230:233], v[132:135], v[52:55], v[230:233]
	v_mfma_f32_16x16x32_bf16 v[20:23], v[172:175], v[52:55], v[20:23]
	v_mfma_f32_16x16x32_bf16 v[24:27], v[172:175], v[56:59], v[24:27]
	v_mfma_f32_16x16x32_bf16 v[132:135], v[132:135], v[56:59], v[140:143]
	v_add_u32_e32 v58, 32, v210
	v_add_u32_e32 v59, 34, v195
	v_mfma_f32_16x16x32_bf16 v[140:143], v[128:131], v[60:63], v[230:233]
	v_mfma_f32_16x16x32_bf16 v[20:23], v[168:171], v[60:63], v[20:23]
	v_add_u32_e32 v60, 33, v210
	v_add_u32_e32 v61, 35, v195
	v_add_u32_e32 v62, 36, v210
	v_mfma_f32_16x16x32_bf16 v[52:55], v[168:171], v[64:67], v[24:27]
	v_add_u32_e32 v63, 38, v195
	v_mfma_f32_16x16x32_bf16 v[128:131], v[128:131], v[64:67], v[132:135]
	v_sub_u32_e32 v66, v209, v58
	v_sub_u32_e32 v67, v209, v61
	v_add_u32_e32 v64, 37, v210
	v_mfma_f32_16x16x32_bf16 v[132:135], v[136:139], v[72:75], v[140:143]
	v_add_u32_e32 v65, 39, v195
	v_sub_u32_e32 v58, v228, v58
	s_waitcnt vmcnt(16)
; __device__ __forceinline__ f32x4 mfma16(bf16x8 a, bf16x8 b, f32x4 c) { return __builtin_amdgcn_mfma_f32_16x16x32_bf16(a, b, c, 0, 0, 0); }
; __device__ __forceinline__ float fexp2(float x) { return __builtin_amdgcn_exp2f(x); }
; __device__ __forceinline__ void ret_task(const Frame& F, int l, int task) {
;     ...
;             bf16x8 Pf[2];
; #pragma unroll
;             for (int qb = 0; qb < 2; ++qb) {
;                 const int i = qb2 * 32 + qb * 16 + c;
; #pragma unroll
;                 for (int ab = 0; ab < 2; ++ab)
; #pragma unroll
;                     for (int e = 0; e < 4; ++e) { const int diff = i - (32 * g + 8 * rq + 4 * ab + e);
;                         sa[qb][ab][e] = diff >= 0 ? sa[qb][ab][e] * fexp2((float)diff * lg) : 0.f; }
;                 Pf[qb] = pack8(sa[qb][0], sa[qb][1]);
;             }
; #pragma unroll
;             for (int eb = 0; eb < 8; ++eb)
; #pragma unroll
;                 for (int qb = 0; qb < 2; ++qb) acc[qb][eb] = mfma16(Vf[eb], Pf[qb], acc[qb][eb]);
	v_mfma_f32_16x16x32_bf16 v[24:27], v[176:179], v[72:75], v[20:23]
	v_sub_u32_e32 v72, v209, v60
	s_nop 2
	v_mov_b32_e32 v56, v132
	v_mov_b32_e32 v57, v134
	v_mfma_f32_16x16x32_bf16 v[20:23], v[176:179], v[80:83], v[52:55]
	v_mov_b32_e32 v134, v133
	v_sub_u32_e32 v74, v209, v62
	v_sub_u32_e32 v75, v209, v65
	v_cvt_f32_u32_e32 v53, v72
	v_sub_u32_e32 v55, v209, v59
	v_cvt_f32_u32_e32 v52, v66
	v_cmp_lt_i32_e32 vcc, -1, v55
	v_mul_f32_e32 v53, v197, v53
	v_exp_f32_e32 v54, v53
	v_cvt_f32_u32_e32 v53, v55
	v_mul_f32_e32 v52, v197, v52
	v_exp_f32_e32 v52, v52
	v_mfma_f32_16x16x32_bf16 v[128:131], v[136:139], v[80:83], v[128:131]
	v_mul_f32_e32 v53, v197, v53
	v_exp_f32_e32 v53, v53
	v_sub_u32_e32 v80, v209, v64
	v_sub_u32_e32 v60, v228, v60
	v_sub_u32_e32 v64, v228, v64
	v_pk_mul_f32 v[52:53], v[52:53], v[56:57]
	v_mov_b32_e32 v56, v24
	v_cndmask_b32_e32 v73, 0, v53, vcc
	v_cmp_lt_i32_e32 vcc, -1, v66
	v_cvt_f32_u32_e32 v24, v75
	v_mov_b32_e32 v57, v26
	v_cndmask_b32_e32 v66, 0, v52, vcc
	v_cvt_f32_u32_e32 v52, v67
	v_cmp_lt_i32_e32 vcc, -1, v72
	v_mul_f32_e32 v24, v197, v24
	v_mov_b32_e32 v26, v25
	v_mul_f32_e32 v52, v197, v52
	v_exp_f32_e32 v55, v52
	v_sub_u32_e32 v62, v228, v62
	v_pk_mul_f32 v[52:53], v[54:55], v[134:135]
	s_nop 0
	v_cndmask_b32_e32 v72, 0, v52, vcc
	v_cmp_lt_i32_e32 vcc, -1, v67
	v_sub_u32_e32 v55, v209, v63
	v_cvt_f32_u32_e32 v52, v74
	v_cndmask_b32_e32 v67, 0, v53, vcc
	v_cvt_f32_u32_e32 v53, v80
	v_cmp_lt_i32_e32 vcc, -1, v55
	v_mul_f32_e32 v52, v197, v52
	v_exp_f32_e32 v52, v52
	v_mul_f32_e32 v53, v197, v53
	v_exp_f32_e32 v54, v53
	v_cvt_f32_u32_e32 v53, v55
	v_exp_f32_e32 v55, v24
	v_mul_f32_e32 v53, v197, v53
	v_exp_f32_e32 v53, v53
	v_pk_mul_f32 v[24:25], v[54:55], v[26:27]
	s_nop 1
	v_pk_mul_f32 v[52:53], v[52:53], v[56:57]
	s_nop 0
	v_cndmask_b32_e32 v53, 0, v53, vcc
	v_cmp_lt_i32_e32 vcc, -1, v74
	v_bfe_u32 v57, v53, 16, 1
	v_add3_u32 v53, v53, v57, s76
	v_cndmask_b32_e32 v52, 0, v52, vcc
	v_cmp_lt_i32_e32 vcc, -1, v80
	v_bfe_u32 v56, v52, 16, 1
	v_add3_u32 v52, v52, v56, s76
	v_cndmask_b32_e32 v24, 0, v24, vcc
	v_bfe_u32 v27, v24, 16, 1
	v_cmp_lt_i32_e32 vcc, -1, v75
	v_add3_u32 v24, v24, v27, s76
	s_nop 0
	v_cndmask_b32_e32 v25, 0, v25, vcc
	s_nop 0
	v_bfe_u32 v26, v25, 16, 1
	s_nop 0
	v_lshrrev_b32_e32 v27, 16, v53
	v_cvt_f32_u32_e32 v53, v60
	v_add3_u32 v25, v25, v26, s76
	s_nop 2
	v_lshrrev_b32_e32 v26, 16, v52
	s_nop 0
	v_and_or_b32 v26, v24, s75, v26
	v_cvt_pk_bf16_f32 v24, v66, v72
	v_sub_u32_e32 v55, v228, v59
	v_mul_f32_e32 v53, v197, v53
	v_and_or_b32 v27, v25, s75, v27
	v_cvt_pk_bf16_f32 v25, v73, v67
	v_cvt_f32_u32_e32 v52, v58
	v_exp_f32_e32 v54, v53
	v_cvt_f32_u32_e32 v53, v55
	v_mov_b32_e32 v56, v128
	v_mul_f32_e32 v52, v197, v52
	v_exp_f32_e32 v52, v52
	v_mul_f32_e32 v53, v197, v53
	v_exp_f32_e32 v53, v53
	v_mov_b32_e32 v57, v130
	v_cmp_lt_i32_e32 vcc, -1, v55
	v_sub_u32_e32 v59, v228, v61
	v_pk_mul_f32 v[52:53], v[52:53], v[56:57]
	v_mov_b32_e32 v130, v129
	v_cndmask_b32_e32 v61, 0, v53, vcc
	v_cmp_lt_i32_e32 vcc, -1, v58
	v_mov_b32_e32 v56, v20
	v_mov_b32_e32 v57, v22
	v_cndmask_b32_e32 v58, 0, v52, vcc
	v_cvt_f32_u32_e32 v52, v59
	v_cmp_lt_i32_e32 vcc, -1, v60
	v_mov_b32_e32 v22, v21
	v_mfma_f32_16x16x32_bf16 v[108:111], v[92:95], v[24:27], v[108:111]
	v_mul_f32_e32 v52, v197, v52
	v_exp_f32_e32 v55, v52
	v_mfma_f32_16x16x32_bf16 v[96:99], v[100:103], v[24:27], v[96:99]
	v_mul_f32_e64 v52, v54, v130
	v_mul_f32_e64 v53, v55, v131
	v_cndmask_b32_e32 v60, 0, v52, vcc
	v_cmp_lt_i32_e32 vcc, -1, v59
	v_sub_u32_e32 v55, v228, v63
	v_cvt_f32_u32_e32 v52, v62
	v_cndmask_b32_e32 v59, 0, v53, vcc
	v_cvt_f32_u32_e32 v53, v64
	v_sub_u32_e32 v63, v228, v65
	v_cvt_f32_u32_e32 v20, v63
	v_mul_f32_e32 v52, v197, v52
	v_mul_f32_e32 v53, v197, v53
	v_exp_f32_e32 v54, v53
	v_cvt_f32_u32_e32 v53, v55
	v_exp_f32_e32 v52, v52
	v_mul_f32_e32 v20, v197, v20
	v_cmp_lt_i32_e32 vcc, -1, v55
	v_mul_f32_e32 v53, v197, v53
	v_exp_f32_e32 v53, v53
	v_exp_f32_e32 v55, v20
	v_mfma_f32_16x16x32_bf16 v[88:91], v[104:107], v[24:27], v[88:91]
	v_mul_f32_e64 v52, v52, v56
	v_mul_f32_e64 v53, v53, v57
	v_cndmask_b32_e32 v53, 0, v53, vcc
	v_cmp_lt_i32_e32 vcc, -1, v62
	v_pk_mul_f32 v[20:21], v[54:55], v[22:23]
	v_bfe_u32 v57, v53, 16, 1
	v_cndmask_b32_e32 v52, 0, v52, vcc
	v_cmp_lt_i32_e32 vcc, -1, v64
	v_bfe_u32 v56, v52, 16, 1
	v_bfe_u32 v54, v59, 16, 1
	v_cndmask_b32_e32 v20, 0, v20, vcc
	v_cmp_lt_i32_e32 vcc, -1, v63
	v_bfe_u32 v23, v20, 16, 1
	v_add3_u32 v20, v20, v23, s76
	v_cndmask_b32_e32 v21, 0, v21, vcc
	v_bfe_u32 v22, v21, 16, 1
	v_add3_u32 v21, v21, v22, s76
	v_bfe_u32 v22, v58, 16, 1
	v_bfe_u32 v23, v61, 16, 1
	v_bfe_u32 v55, v60, 16, 1
	v_add3_u32 v53, v53, v57, s76
	v_add3_u32 v52, v52, v56, s76
	v_add3_u32 v23, v61, v23, s76
	v_add3_u32 v22, v58, v22, s76
	v_add3_u32 v55, v60, v55, s76
	v_add3_u32 v54, v59, v54, s76
	v_lshrrev_b32_e32 v56, 16, v22
	v_lshrrev_b32_e32 v57, 16, v23
	v_lshrrev_b32_e32 v22, 16, v52
	v_lshrrev_b32_e32 v23, 16, v53
	v_and_or_b32 v23, v21, s75, v23
	v_and_or_b32 v22, v20, s75, v22
	v_cvt_pk_bf16_f32 v21, v61, v59
	v_cvt_pk_bf16_f32 v20, v58, v60
	v_mfma_f32_16x16x32_bf16 v[84:87], v[112:115], v[24:27], v[84:87]
	s_nop 0
	v_mfma_f32_16x16x32_bf16 v[36:39], v[92:95], v[20:23], v[36:39]
	v_mfma_f32_16x16x32_bf16 v[32:35], v[100:103], v[20:23], v[32:35]
	v_mfma_f32_16x16x32_bf16 v[28:31], v[104:107], v[20:23], v[28:31]
	v_mfma_f32_16x16x32_bf16 v[16:19], v[112:115], v[20:23], v[16:19]
	v_mfma_f32_16x16x32_bf16 v[68:71], v[116:119], v[24:27], v[68:71]
	v_mfma_f32_16x16x32_bf16 v[12:15], v[116:119], v[20:23], v[12:15]
	v_mfma_f32_16x16x32_bf16 v[48:51], v[120:123], v[24:27], v[48:51]
	v_mfma_f32_16x16x32_bf16 v[8:11], v[120:123], v[20:23], v[8:11]
	v_mfma_f32_16x16x32_bf16 v[44:47], v[124:127], v[24:27], v[44:47]
	v_mfma_f32_16x16x32_bf16 v[4:7], v[124:127], v[20:23], v[4:7]
	v_mfma_f32_16x16x32_bf16 v[40:43], v[76:79], v[24:27], v[40:43]
	v_mfma_f32_16x16x32_bf16 v[0:3], v[76:79], v[20:23], v[0:3]
	s_branch .LBB0_633
